# E6 plus nt cache policy on the once-read f32 weight loads of the conversion loops (prologue and windows)
# speedup vs baseline: 1.0105x; 1.0105x over previous
.LBB0_60:
	s_lshl_b32 s8, s23, 14
	s_add_i32 s9, s8, 0
	s_lshl_b32 s8, s26, 6
	v_bfe_u32 v78, v2, 4, 2
	v_or_b32_e32 v0, s8, v78
	s_ashr_i32 s18, s8, 31
	s_mul_i32 s23, s16, s18
	v_mul_lo_u32 v3, s17, v0
	v_mad_u64_u32 v[0:1], s[18:19], s16, v0, 0
	v_add3_u32 v1, v1, s23, v3
	v_lshlrev_b32_e32 v3, 2, v2
	v_and_b32_e32 v64, 60, v3
	v_lshlrev_b32_e32 v72, 2, v64
	v_lshl_add_u32 v6, v78, 8, s9
	v_lshlrev_b32_e32 v7, 2, v78
	v_add3_u32 v79, v6, v7, v72
	v_bitop3_b32 v7, v64, v78, 1 bitop3:0x36
	v_lshl_add_u32 v80, v7, 2, v6
	v_bitop3_b32 v7, v64, v78, 2 bitop3:0x36
	v_lshl_add_u32 v81, v7, 2, v6
	v_bitop3_b32 v7, v64, v78, 3 bitop3:0x36
	v_lshl_add_u32 v82, v7, 2, v6
	v_or_b32_e32 v6, 4, v78
	v_lshl_add_u32 v7, v6, 8, s9
	v_bitop3_b32 v8, v78, v64, 4 bitop3:0x36
	v_lshl_add_u32 v83, v8, 2, v7
	v_bitop3_b32 v8, v64, v6, 1 bitop3:0x36
	v_lshl_add_u32 v84, v8, 2, v7
	v_bitop3_b32 v8, v64, v6, 2 bitop3:0x36
	v_bitop3_b32 v6, v64, v6, 3 bitop3:0x36
	v_lshl_add_u32 v86, v6, 2, v7
	v_or_b32_e32 v6, 8, v78
	v_lshl_add_u32 v85, v8, 2, v7
	v_lshl_add_u32 v7, v6, 8, s9
	v_bitop3_b32 v8, v78, v64, 8 bitop3:0x36
	v_lshl_add_u32 v87, v8, 2, v7
	v_bitop3_b32 v8, v64, v6, 1 bitop3:0x36
	v_lshl_add_u32 v88, v8, 2, v7
	v_bitop3_b32 v8, v64, v6, 2 bitop3:0x36
	v_bitop3_b32 v6, v64, v6, 3 bitop3:0x36
	v_lshl_add_u32 v90, v6, 2, v7
	v_or_b32_e32 v6, 12, v78
	v_lshl_add_u32 v89, v8, 2, v7
	v_lshl_add_u32 v7, v6, 8, s9
	v_bitop3_b32 v8, v78, v64, 12 bitop3:0x36
	v_lshl_add_u32 v91, v8, 2, v7
	v_bitop3_b32 v8, v64, v6, 1 bitop3:0x36
	v_lshl_add_u32 v92, v8, 2, v7
	v_bitop3_b32 v8, v64, v6, 2 bitop3:0x36
	v_bitop3_b32 v6, v64, v6, 3 bitop3:0x36
	v_lshl_add_u32 v94, v6, 2, v7
	v_or_b32_e32 v6, 16, v78
	v_lshl_add_u32 v93, v8, 2, v7
	v_lshl_add_u32 v7, v6, 8, s9
	v_bitop3_b32 v8, v78, v64, 16 bitop3:0x36
	v_lshl_add_u32 v95, v8, 2, v7
	v_bitop3_b32 v8, v64, v6, 1 bitop3:0x36
	v_lshl_add_u32 v96, v8, 2, v7
	v_bitop3_b32 v8, v64, v6, 2 bitop3:0x36
	v_bitop3_b32 v6, v64, v6, 3 bitop3:0x36
	v_lshl_add_u32 v98, v6, 2, v7
	v_or_b32_e32 v6, 20, v78
	v_lshl_add_u32 v97, v8, 2, v7
	v_lshl_add_u32 v7, v6, 8, s9
	v_bitop3_b32 v8, v78, v64, 20 bitop3:0x36
	v_lshl_add_u32 v99, v8, 2, v7
	v_bitop3_b32 v8, v64, v6, 1 bitop3:0x36
	v_lshl_add_u32 v100, v8, 2, v7
	v_bitop3_b32 v8, v64, v6, 2 bitop3:0x36
	v_bitop3_b32 v6, v64, v6, 3 bitop3:0x36
	v_lshl_add_u32 v102, v6, 2, v7
	v_or_b32_e32 v6, 24, v78
	v_lshl_add_u32 v101, v8, 2, v7
	v_lshl_add_u32 v7, v6, 8, s9
	v_bitop3_b32 v8, v78, v64, 24 bitop3:0x36
	v_lshl_add_u32 v103, v8, 2, v7
	v_bitop3_b32 v8, v64, v6, 1 bitop3:0x36
	v_lshl_add_u32 v104, v8, 2, v7
	v_bitop3_b32 v8, v64, v6, 2 bitop3:0x36
	v_bitop3_b32 v6, v64, v6, 3 bitop3:0x36
	v_lshl_add_u32 v106, v6, 2, v7
	v_or_b32_e32 v6, 28, v78
	v_lshl_add_u32 v105, v8, 2, v7
	v_lshl_add_u32 v7, v6, 8, s9
	v_bitop3_b32 v8, v78, v64, 28 bitop3:0x36
	v_lshl_add_u32 v107, v8, 2, v7
	v_bitop3_b32 v8, v64, v6, 1 bitop3:0x36
	v_lshl_add_u32 v108, v8, 2, v7
	v_bitop3_b32 v8, v64, v6, 2 bitop3:0x36
	v_bitop3_b32 v6, v64, v6, 3 bitop3:0x36
	v_lshl_add_u32 v110, v6, 2, v7
	v_or_b32_e32 v6, 36, v78
	v_or_b32_e32 v3, 1, v64
	v_lshl_add_u32 v109, v8, 2, v7
	v_lshl_add_u32 v7, v6, 8, s9
	v_bitop3_b32 v8, v6, v64, 7 bitop3:0x6c
	v_or_b32_e32 v4, 2, v64
	v_or_b32_e32 v5, 3, v64
	v_lshl_add_u32 v111, v8, 2, v7
	v_bitop3_b32 v8, v6, v3, 7 bitop3:0x6c
	v_lshl_add_u32 v112, v8, 2, v7
	v_bitop3_b32 v8, v6, v4, 7 bitop3:0x6c
	v_bitop3_b32 v6, v6, v5, 7 bitop3:0x6c
	v_lshl_add_u32 v114, v6, 2, v7
	v_or_b32_e32 v6, 40, v78
	v_lshl_add_u32 v113, v8, 2, v7
	v_lshl_add_u32 v7, v6, 8, s9
	v_bitop3_b32 v8, v6, v64, 11 bitop3:0x6c
	v_lshl_add_u32 v115, v8, 2, v7
	v_bitop3_b32 v8, v6, v3, 11 bitop3:0x6c
	v_lshl_add_u32 v116, v8, 2, v7
	v_bitop3_b32 v8, v6, v4, 11 bitop3:0x6c
	v_bitop3_b32 v6, v6, v5, 11 bitop3:0x6c
	v_lshl_add_u32 v118, v6, 2, v7
	v_or_b32_e32 v6, 44, v78
	v_lshl_add_u32 v117, v8, 2, v7
	v_lshl_add_u32 v7, v6, 8, s9
	v_bitop3_b32 v8, v6, v64, 15 bitop3:0x6c
	v_lshl_add_u32 v119, v8, 2, v7
	v_bitop3_b32 v8, v6, v3, 15 bitop3:0x6c
	v_lshl_add_u32 v120, v8, 2, v7
	v_bitop3_b32 v8, v6, v4, 15 bitop3:0x6c
	v_bitop3_b32 v6, v6, v5, 15 bitop3:0x6c
	v_lshl_add_u32 v122, v6, 2, v7
	v_or_b32_e32 v6, 48, v78
	v_lshl_add_u32 v121, v8, 2, v7
	v_lshl_add_u32 v7, v6, 8, s9
	v_bitop3_b32 v8, v6, v64, 19 bitop3:0x6c
	v_lshl_add_u32 v123, v8, 2, v7
	v_bitop3_b32 v8, v6, v3, 19 bitop3:0x6c
	v_lshl_add_u32 v124, v8, 2, v7
	v_bitop3_b32 v8, v6, v4, 19 bitop3:0x6c
	v_bitop3_b32 v6, v6, v5, 19 bitop3:0x6c
	v_lshl_add_u32 v126, v6, 2, v7
	v_or_b32_e32 v6, 52, v78
	v_lshl_add_u32 v125, v8, 2, v7
	v_lshl_add_u32 v7, v6, 8, s9
	v_bitop3_b32 v8, v6, v64, 23 bitop3:0x6c
	v_lshl_add_u32 v127, v8, 2, v7
	v_bitop3_b32 v8, v6, v3, 23 bitop3:0x6c
	v_lshl_add_u32 v128, v8, 2, v7
	v_bitop3_b32 v8, v6, v4, 23 bitop3:0x6c
	v_bitop3_b32 v6, v6, v5, 23 bitop3:0x6c
	v_lshl_add_u32 v130, v6, 2, v7
	v_or_b32_e32 v6, 56, v78
	v_lshl_add_u32 v129, v8, 2, v7
	v_lshl_add_u32 v7, v6, 8, s9
	v_bitop3_b32 v8, v6, v64, 27 bitop3:0x6c
	v_lshl_add_u32 v131, v8, 2, v7
	v_bitop3_b32 v8, v6, v3, 27 bitop3:0x6c
	v_lshl_add_u32 v132, v8, 2, v7
	v_bitop3_b32 v8, v6, v4, 27 bitop3:0x6c
	v_bitop3_b32 v6, v6, v5, 27 bitop3:0x6c
	v_lshl_add_u32 v134, v6, 2, v7
	v_or_b32_e32 v6, 60, v78
	v_lshl_add_u32 v133, v8, 2, v7
	v_bitop3_b32 v3, v6, v3, 31 bitop3:0x6c
	v_lshl_add_u32 v7, v6, 8, s9
	v_lshl_add_u32 v136, v3, 2, v7
	v_and_b32_e32 v3, 63, v2
	v_lshlrev_b32_e32 v3, 3, v3
	v_bitop3_b32 v4, v6, v4, 31 bitop3:0x6c
	v_bitop3_b32 v5, v6, v5, 31 bitop3:0x6c
	v_bfe_u32 v139, v2, 3, 3
	v_and_b32_e32 v2, 24, v3
	v_and_b32_e32 v74, 56, v3
	v_lshl_add_u32 v137, v4, 2, v7
	v_lshl_add_u32 v138, v5, 2, v7
	v_lshlrev_b32_e32 v2, 2, v2
	v_lshl_add_u32 v4, v74, 8, s9
	v_lshlrev_b32_e32 v5, 2, v139
	v_or_b32_e32 v141, 8, v139
	v_add3_u32 v140, v4, v2, v5
	v_bitop3_b32 v2, v3, v141, 24 bitop3:0x6c
	v_or_b32_e32 v143, 16, v139
	v_lshl_add_u32 v142, v2, 2, v4
	v_bitop3_b32 v2, v3, v143, 24 bitop3:0x6c
	v_lshl_add_u32 v144, v2, 2, v4
	v_bitop3_b32 v2, v3, v139, 24 bitop3:0x4e
	v_or_b32_e32 v146, 40, v139
	v_lshl_add_u32 v145, v2, 2, v4
	v_bitop3_b32 v2, v3, v146, 24 bitop3:0x6c
	v_or_b32_e32 v148, 48, v139
	v_lshl_add_u32 v147, v2, 2, v4
	v_bitop3_b32 v2, v3, v148, 24 bitop3:0x6c
	v_or_b32_e32 v150, 56, v139
	v_lshl_add_u32 v149, v2, 2, v4
	v_bitop3_b32 v2, v3, v150, 24 bitop3:0x6c
	v_lshl_add_u32 v151, v2, 2, v4
	v_or_b32_e32 v2, 1, v74
	v_bitop3_b32 v3, v2, v139, 25 bitop3:0x6c
	v_lshl_add_u32 v4, v2, 8, s9
	v_lshl_add_u32 v152, v3, 2, v4
	v_bitop3_b32 v3, v2, v141, 25 bitop3:0x6c
	v_lshl_add_u32 v153, v3, 2, v4
	v_bitop3_b32 v3, v2, v143, 25 bitop3:0x6c
	v_or_b32_e32 v155, 24, v139
	v_lshl_add_u32 v154, v3, 2, v4
	v_bitop3_b32 v3, v2, v155, 25 bitop3:0x6c
	v_or_b32_e32 v157, 32, v139
	v_lshl_add_u32 v156, v3, 2, v4
	v_bitop3_b32 v3, v2, v157, 25 bitop3:0x6c
	v_lshl_add_u32 v158, v3, 2, v4
	v_bitop3_b32 v3, v2, v146, 25 bitop3:0x6c
	v_lshl_add_u32 v159, v3, 2, v4
	v_bitop3_b32 v3, v2, v148, 25 bitop3:0x6c
	v_bitop3_b32 v2, v2, v150, 25 bitop3:0x6c
	v_lshl_add_u32 v161, v2, 2, v4
	v_or_b32_e32 v2, 2, v74
	v_lshl_add_u32 v160, v3, 2, v4
	v_bitop3_b32 v3, v2, v139, 26 bitop3:0x6c
	v_lshl_add_u32 v4, v2, 8, s9
	v_lshl_add_u32 v162, v3, 2, v4
	v_bitop3_b32 v3, v2, v141, 26 bitop3:0x6c
	v_lshl_add_u32 v163, v3, 2, v4
	v_bitop3_b32 v3, v2, v143, 26 bitop3:0x6c
	v_lshl_add_u32 v164, v3, 2, v4
	v_bitop3_b32 v3, v2, v155, 26 bitop3:0x6c
	v_lshl_add_u32 v165, v3, 2, v4
	v_bitop3_b32 v3, v2, v157, 26 bitop3:0x6c
	v_lshl_add_u32 v166, v3, 2, v4
	v_bitop3_b32 v3, v2, v146, 26 bitop3:0x6c
	v_lshl_add_u32 v167, v3, 2, v4
	v_bitop3_b32 v3, v2, v148, 26 bitop3:0x6c
	v_bitop3_b32 v2, v2, v150, 26 bitop3:0x6c
	v_lshl_add_u32 v169, v2, 2, v4
	v_or_b32_e32 v2, 3, v74
	v_lshl_add_u32 v168, v3, 2, v4
	v_bitop3_b32 v3, v2, v139, 27 bitop3:0x6c
	v_lshl_add_u32 v4, v2, 8, s9
	v_lshl_add_u32 v170, v3, 2, v4
	v_bitop3_b32 v3, v2, v141, 27 bitop3:0x6c
	v_lshl_add_u32 v171, v3, 2, v4
	v_bitop3_b32 v3, v2, v143, 27 bitop3:0x6c
	v_lshl_add_u32 v172, v3, 2, v4
	v_bitop3_b32 v3, v2, v155, 27 bitop3:0x6c
	v_lshl_add_u32 v173, v3, 2, v4
	v_bitop3_b32 v3, v2, v157, 27 bitop3:0x6c
	v_lshl_add_u32 v174, v3, 2, v4
	v_bitop3_b32 v3, v2, v146, 27 bitop3:0x6c
	v_lshl_add_u32 v175, v3, 2, v4
	v_bitop3_b32 v3, v2, v148, 27 bitop3:0x6c
	v_bitop3_b32 v2, v2, v150, 27 bitop3:0x6c
	v_or_b32_e32 v65, 4, v74
	v_lshl_add_u32 v177, v2, 2, v4
	v_bitop3_b32 v2, v65, v139, 28 bitop3:0x6c
	v_lshl_add_u32 v66, v65, 8, s9
	s_lshl_b32 s44, s15, 3
	v_lshl_add_u64 v[0:1], v[0:1], 2, s[12:13]
	s_ashr_i32 s15, s14, 31
	v_lshl_add_u32 v178, v2, 2, v66
	v_bitop3_b32 v2, v65, v141, 28 bitop3:0x6c
	v_lshl_add_u64 v[0:1], s[14:15], 2, v[0:1]
	v_mov_b32_e32 v73, 0
	s_lshl_b64 s[12:13], s[16:17], 4
	v_bitop3_b32 v6, v6, v64, 31 bitop3:0x6c
	v_lshl_add_u32 v176, v3, 2, v4
	v_lshl_add_u32 v179, v2, 2, v66
	v_bitop3_b32 v2, v65, v143, 28 bitop3:0x6c
	s_mov_b32 s19, 0
	v_lshl_add_u64 v[4:5], v[0:1], 0, v[72:73]
	s_mul_i32 s18, s16, 0xf0
	s_sub_u32 s12, 0, s12
	v_lshl_add_u32 v135, v6, 2, v7
	v_lshl_add_u32 v180, v2, 2, v66
	v_bitop3_b32 v2, v65, v155, 28 bitop3:0x6c
	s_subb_u32 s13, 0, s13
	v_lshl_add_u64 v[6:7], v[4:5], 0, s[18:19]
	v_lshl_add_u32 v181, v2, 2, v66
	v_bitop3_b32 v2, v65, v157, 28 bitop3:0x6c
	v_lshl_add_u64 v[0:1], v[6:7], 0, s[12:13]
	v_lshl_add_u32 v182, v2, 2, v66
	v_lshl_add_u64 v[2:3], v[0:1], 0, s[12:13]
	v_lshl_add_u64 v[8:9], v[2:3], 0, s[12:13]
	global_load_dwordx4 v[56:59], v[0:1], off nt
	global_load_dwordx4 v[40:43], v[2:3], off nt
	v_lshl_add_u64 v[0:1], v[8:9], 0, s[12:13]
	v_lshl_add_u64 v[2:3], v[0:1], 0, s[12:13]
	global_load_dwordx4 v[52:55], v[8:9], off nt
	global_load_dwordx4 v[36:39], v[0:1], off nt
	v_lshl_add_u64 v[0:1], v[2:3], 0, s[12:13]
	v_lshl_add_u64 v[8:9], v[0:1], 0, s[12:13]
	global_load_dwordx4 v[48:51], v[2:3], off nt
	global_load_dwordx4 v[32:35], v[0:1], off nt
	v_lshl_add_u64 v[0:1], v[8:9], 0, s[12:13]
	v_lshl_add_u64 v[2:3], v[0:1], 0, s[12:13]
	global_load_dwordx4 v[24:27], v[0:1], off nt
	v_lshl_add_u64 v[0:1], v[2:3], 0, s[12:13]
	global_load_dwordx4 v[44:47], v[2:3], off nt
	v_lshl_add_u64 v[2:3], v[0:1], 0, s[12:13]
	global_load_dwordx4 v[16:19], v[0:1], off nt
	v_lshl_add_u64 v[0:1], v[2:3], 0, s[12:13]
	global_load_dwordx4 v[20:23], v[2:3], off nt
	v_lshl_add_u64 v[2:3], v[0:1], 0, s[12:13]
	global_load_dwordx4 v[28:31], v[8:9], off nt
	v_bitop3_b32 v67, v65, v146, 28 bitop3:0x6c
	global_load_dwordx4 v[8:11], v[0:1], off nt
	v_lshl_add_u64 v[0:1], v[2:3], 0, s[12:13]
	global_load_dwordx4 v[12:15], v[2:3], off nt
	s_nop 0
	global_load_dwordx4 v[0:3], v[0:1], off nt
	s_nop 0
	global_load_dwordx4 v[60:63], v[6:7], off nt
	s_nop 0
	global_load_dwordx4 v[4:7], v[4:5], off nt
	v_lshl_add_u32 v183, v67, 2, v66
	v_bitop3_b32 v67, v65, v148, 28 bitop3:0x6c
	v_bitop3_b32 v65, v65, v150, 28 bitop3:0x6c
	v_lshl_add_u32 v185, v65, 2, v66
	v_or_b32_e32 v65, 5, v74
	v_lshl_add_u32 v184, v67, 2, v66
	v_bitop3_b32 v66, v65, v139, 29 bitop3:0x6c
	v_lshl_add_u32 v67, v65, 8, s9
	v_lshl_add_u32 v186, v66, 2, v67
	v_bitop3_b32 v66, v65, v141, 29 bitop3:0x6c
	v_lshl_add_u32 v187, v66, 2, v67
	v_bitop3_b32 v66, v65, v143, 29 bitop3:0x6c
	v_lshl_add_u32 v188, v66, 2, v67
	v_bitop3_b32 v66, v65, v155, 29 bitop3:0x6c
	v_lshl_add_u32 v189, v66, 2, v67
	v_bitop3_b32 v66, v65, v157, 29 bitop3:0x6c
	v_lshl_add_u32 v190, v66, 2, v67
	v_bitop3_b32 v66, v65, v146, 29 bitop3:0x6c
	v_lshl_add_u32 v191, v66, 2, v67
	v_bitop3_b32 v66, v65, v148, 29 bitop3:0x6c
	v_bitop3_b32 v65, v65, v150, 29 bitop3:0x6c
	v_lshl_add_u32 v193, v65, 2, v67
	v_or_b32_e32 v65, 6, v74
	v_lshl_add_u32 v192, v66, 2, v67
	v_bitop3_b32 v66, v65, v139, 30 bitop3:0x6c
	v_lshl_add_u32 v67, v65, 8, s9
	s_add_u32 s45, s21, 0x1a000000
	v_lshl_add_u32 v194, v66, 2, v67
	v_bitop3_b32 v66, v65, v141, 30 bitop3:0x6c
	s_addc_u32 s46, s22, 0
	v_lshl_add_u32 v195, v66, 2, v67
	v_bitop3_b32 v66, v65, v143, 30 bitop3:0x6c
	s_add_u32 s47, s21, 0x2000000
	v_lshl_add_u32 v196, v66, 2, v67
	v_bitop3_b32 v66, v65, v155, 30 bitop3:0x6c
	s_addc_u32 s48, s22, 0
	v_lshl_add_u32 v197, v66, 2, v67
	v_bitop3_b32 v66, v65, v157, 30 bitop3:0x6c
	s_add_u32 s49, s21, 0x1a00000
	v_lshl_add_u32 v198, v66, 2, v67
	v_bitop3_b32 v66, v65, v146, 30 bitop3:0x6c
	s_addc_u32 s50, s22, 0
	v_lshl_add_u32 v199, v66, 2, v67
	v_bitop3_b32 v66, v65, v148, 30 bitop3:0x6c
	v_bitop3_b32 v65, v65, v150, 30 bitop3:0x6c
	s_add_u32 s51, s21, 0x1800000
	v_lshl_add_u32 v201, v65, 2, v67
	v_or_b32_e32 v65, 7, v74
	s_addc_u32 s52, s22, 0
	v_lshl_add_u32 v200, v66, 2, v67
	v_bitop3_b32 v66, v65, v139, 31 bitop3:0x6c
	v_lshl_add_u32 v67, v65, 8, s9
	s_add_u32 s53, s21, 0x1500000
	v_lshl_add_u32 v202, v66, 2, v67
	v_bitop3_b32 v66, v65, v141, 31 bitop3:0x6c
	s_addc_u32 s54, s22, 0
	v_lshl_add_u32 v203, v66, 2, v67
	v_bitop3_b32 v66, v65, v143, 31 bitop3:0x6c
	s_add_u32 s55, s21, 0x1200000
	v_lshl_add_u32 v204, v66, 2, v67
	v_bitop3_b32 v66, v65, v155, 31 bitop3:0x6c
	s_addc_u32 s56, s22, 0
	v_lshl_add_u32 v205, v66, 2, v67
	v_bitop3_b32 v66, v65, v157, 31 bitop3:0x6c
	s_add_u32 s57, s21, 0xe00000
	v_lshl_add_u32 v206, v66, 2, v67
	v_bitop3_b32 v66, v65, v146, 31 bitop3:0x6c
	s_addc_u32 s58, s22, 0
	v_lshl_add_u32 v207, v66, 2, v67
	v_bitop3_b32 v66, v65, v148, 31 bitop3:0x6c
	v_bitop3_b32 v65, v65, v150, 31 bitop3:0x6c
	s_add_u32 s59, s21, 0x200000
	v_lshl_add_u32 v208, v66, 2, v67
	v_lshl_add_u32 v209, v65, 2, v67
	s_addc_u32 s60, s22, 0
	s_add_i32 s61, s61, s44
	v_lshlrev_b32_e32 v76, 2, v64
	v_lshlrev_b32_e32 v72, 1, v74
	s_branch .LBB0_66

.LBB0_62:
	s_lshl_b32 s21, s64, 6
	v_or_b32_e32 v0, s21, v78
	s_ashr_i32 s9, s21, 31
	s_mul_i32 s9, s24, s9
	v_mul_lo_u32 v2, s25, v0
	v_mad_u64_u32 v[0:1], s[64:65], s24, v0, 0
	v_add3_u32 v1, v1, s9, v2
	v_lshl_add_u64 v[0:1], v[0:1], 2, s[18:19]
	s_ashr_i32 s23, s22, 31
	v_lshl_add_u64 v[0:1], s[22:23], 2, v[0:1]
	v_mov_b32_e32 v77, v73
	v_lshl_add_u64 v[0:1], v[0:1], 0, v[76:77]
	s_lshl_b64 s[18:19], s[24:25], 4
	v_lshl_add_u64 v[8:9], v[0:1], 0, s[18:19]
	global_load_dwordx4 v[4:7], v[0:1], off nt
	s_nop 0
	global_load_dwordx4 v[0:3], v[8:9], off nt
	v_lshl_add_u64 v[8:9], v[8:9], 0, s[18:19]
	v_lshl_add_u64 v[16:17], v[8:9], 0, s[18:19]
	global_load_dwordx4 v[12:15], v[8:9], off nt
	s_nop 0
	global_load_dwordx4 v[8:11], v[16:17], off nt
	v_lshl_add_u64 v[16:17], v[16:17], 0, s[18:19]
	v_lshl_add_u64 v[24:25], v[16:17], 0, s[18:19]
	global_load_dwordx4 v[20:23], v[16:17], off nt
	s_nop 0
	global_load_dwordx4 v[16:19], v[24:25], off nt
	v_lshl_add_u64 v[24:25], v[24:25], 0, s[18:19]
	v_lshl_add_u64 v[28:29], v[24:25], 0, s[18:19]
	v_lshl_add_u64 v[32:33], v[28:29], 0, s[18:19]
	v_lshl_add_u64 v[36:37], v[32:33], 0, s[18:19]
	global_load_dwordx4 v[44:47], v[24:25], off nt
	s_nop 0
	global_load_dwordx4 v[24:27], v[28:29], off nt
	s_nop 0
	global_load_dwordx4 v[28:31], v[32:33], off nt
	s_nop 0
	global_load_dwordx4 v[32:35], v[36:37], off nt
	v_lshl_add_u64 v[36:37], v[36:37], 0, s[18:19]
	v_lshl_add_u64 v[40:41], v[36:37], 0, s[18:19]
	global_load_dwordx4 v[48:51], v[36:37], off nt
	s_nop 0
	global_load_dwordx4 v[36:39], v[40:41], off nt
	v_lshl_add_u64 v[40:41], v[40:41], 0, s[18:19]
	v_lshl_add_u64 v[56:57], v[40:41], 0, s[18:19]
	v_lshl_add_u64 v[60:61], v[56:57], 0, s[18:19]
	global_load_dwordx4 v[52:55], v[40:41], off nt
	s_nop 0
	global_load_dwordx4 v[40:43], v[56:57], off nt
	s_nop 0
	global_load_dwordx4 v[56:59], v[60:61], off nt
	v_lshl_add_u64 v[60:61], v[60:61], 0, s[18:19]
	global_load_dwordx4 v[60:63], v[60:61], off nt

.LBB0_637:
	s_lshl_b32 s6, s18, 14
	s_add_i32 s7, s6, 0
	s_lshl_b32 s6, s23, 6
	v_bfe_u32 v75, v65, 4, 2
	v_or_b32_e32 v0, s6, v75
	s_ashr_i32 s13, s6, 31
	s_mul_i32 s13, s14, s13
	v_mul_lo_u32 v2, s15, v0
	v_mad_u64_u32 v[0:1], s[30:31], s14, v0, 0
	v_add3_u32 v1, v1, s13, v2
	v_lshlrev_b32_e32 v2, 2, v65
	v_lshl_add_u64 v[0:1], v[0:1], 2, s[8:9]
	s_ashr_i32 s13, s12, 31
	v_and_b32_e32 v64, 60, v2
	v_lshl_add_u64 v[0:1], s[12:13], 2, v[0:1]
	v_mov_b32_e32 v73, 0
	v_lshlrev_b32_e32 v72, 2, v64
	s_lshl_b64 s[8:9], s[14:15], 4
	s_mov_b32 s17, 0
	v_lshl_add_u64 v[66:67], v[0:1], 0, v[72:73]
	s_mul_i32 s16, s14, 0xf0
	s_sub_u32 s8, 0, s8
	v_lshl_add_u64 v[68:69], v[66:67], 0, s[16:17]
	s_subb_u32 s9, 0, s9
	v_lshl_add_u64 v[8:9], v[68:69], 0, s[8:9]
	v_lshl_add_u64 v[10:11], v[8:9], 0, s[8:9]
	global_load_dwordx4 v[4:7], v[8:9], off nt
	global_load_dwordx4 v[0:3], v[10:11], off nt
	v_lshl_add_u64 v[8:9], v[10:11], 0, s[8:9]
	v_lshl_add_u64 v[10:11], v[8:9], 0, s[8:9]
	global_load_dwordx4 v[24:27], v[8:9], off nt
	global_load_dwordx4 v[12:15], v[10:11], off nt
	v_lshl_add_u64 v[8:9], v[10:11], 0, s[8:9]
	v_lshl_add_u64 v[10:11], v[8:9], 0, s[8:9]
	global_load_dwordx4 v[52:55], v[8:9], off nt
	global_load_dwordx4 v[36:39], v[10:11], off nt
	v_lshl_add_u64 v[8:9], v[10:11], 0, s[8:9]
	global_load_dwordx4 v[48:51], v[8:9], off nt
	v_lshl_add_u64 v[8:9], v[8:9], 0, s[8:9]
	global_load_dwordx4 v[44:47], v[8:9], off nt
	v_lshl_add_u64 v[8:9], v[8:9], 0, s[8:9]
	global_load_dwordx4 v[56:59], v[8:9], off nt
	v_lshl_add_u64 v[8:9], v[8:9], 0, s[8:9]
	global_load_dwordx4 v[32:35], v[8:9], off nt
	v_lshl_add_u64 v[8:9], v[8:9], 0, s[8:9]
	global_load_dwordx4 v[40:43], v[8:9], off nt
	v_lshl_add_u64 v[8:9], v[8:9], 0, s[8:9]
	global_load_dwordx4 v[20:23], v[8:9], off nt
	v_lshl_add_u64 v[8:9], v[8:9], 0, s[8:9]
	v_lshl_add_u64 v[70:71], v[8:9], 0, s[8:9]
	global_load_dwordx4 v[28:31], v[8:9], off nt
	s_nop 0
	global_load_dwordx4 v[8:11], v[70:71], off nt
	global_load_dwordx4 v[60:63], v[68:69], off nt
	global_load_dwordx4 v[16:19], v[66:67], off nt
	v_lshl_add_u32 v69, v75, 8, s7
	v_lshlrev_b32_e32 v70, 2, v75
	v_add3_u32 v78, v69, v70, v72
	v_bitop3_b32 v70, v64, v75, 1 bitop3:0x36
	v_lshl_add_u32 v79, v70, 2, v69
	v_bitop3_b32 v70, v64, v75, 2 bitop3:0x36
	v_lshl_add_u32 v80, v70, 2, v69
	v_bitop3_b32 v70, v64, v75, 3 bitop3:0x36
	v_lshl_add_u32 v81, v70, 2, v69
	v_or_b32_e32 v69, 4, v75
	v_lshl_add_u32 v70, v69, 8, s7
	v_bitop3_b32 v71, v75, v64, 4 bitop3:0x36
	v_lshl_add_u32 v82, v71, 2, v70
	v_bitop3_b32 v71, v64, v69, 1 bitop3:0x36
	v_lshl_add_u32 v83, v71, 2, v70
	v_bitop3_b32 v71, v64, v69, 2 bitop3:0x36
	v_bitop3_b32 v69, v64, v69, 3 bitop3:0x36
	v_lshl_add_u32 v85, v69, 2, v70
	v_or_b32_e32 v69, 8, v75
	v_lshl_add_u32 v84, v71, 2, v70
	v_lshl_add_u32 v70, v69, 8, s7
	v_bitop3_b32 v71, v75, v64, 8 bitop3:0x36
	v_lshl_add_u32 v86, v71, 2, v70
	v_bitop3_b32 v71, v64, v69, 1 bitop3:0x36
	v_lshl_add_u32 v87, v71, 2, v70
	v_bitop3_b32 v71, v64, v69, 2 bitop3:0x36
	v_bitop3_b32 v69, v64, v69, 3 bitop3:0x36
	v_lshl_add_u32 v89, v69, 2, v70
	v_or_b32_e32 v69, 12, v75
	v_lshl_add_u32 v88, v71, 2, v70
	v_lshl_add_u32 v70, v69, 8, s7
	v_bitop3_b32 v71, v75, v64, 12 bitop3:0x36
	v_lshl_add_u32 v90, v71, 2, v70
	v_bitop3_b32 v71, v64, v69, 1 bitop3:0x36
	v_lshl_add_u32 v91, v71, 2, v70
	v_bitop3_b32 v71, v64, v69, 2 bitop3:0x36
	v_bitop3_b32 v69, v64, v69, 3 bitop3:0x36
	v_lshl_add_u32 v93, v69, 2, v70
	v_or_b32_e32 v69, 16, v75
	v_lshl_add_u32 v92, v71, 2, v70
	v_lshl_add_u32 v70, v69, 8, s7
	v_bitop3_b32 v71, v75, v64, 16 bitop3:0x36
	v_lshl_add_u32 v94, v71, 2, v70
	v_bitop3_b32 v71, v64, v69, 1 bitop3:0x36
	v_lshl_add_u32 v95, v71, 2, v70
	v_bitop3_b32 v71, v64, v69, 2 bitop3:0x36
	v_bitop3_b32 v69, v64, v69, 3 bitop3:0x36
	v_lshl_add_u32 v97, v69, 2, v70
	v_or_b32_e32 v69, 20, v75
	v_lshl_add_u32 v96, v71, 2, v70
	v_lshl_add_u32 v70, v69, 8, s7
	v_bitop3_b32 v71, v75, v64, 20 bitop3:0x36
	v_lshl_add_u32 v98, v71, 2, v70
	v_bitop3_b32 v71, v64, v69, 1 bitop3:0x36
	v_lshl_add_u32 v99, v71, 2, v70
	v_bitop3_b32 v71, v64, v69, 2 bitop3:0x36
	v_bitop3_b32 v69, v64, v69, 3 bitop3:0x36
	v_lshl_add_u32 v101, v69, 2, v70
	v_or_b32_e32 v69, 24, v75
	v_lshl_add_u32 v100, v71, 2, v70
	v_lshl_add_u32 v70, v69, 8, s7
	v_bitop3_b32 v71, v75, v64, 24 bitop3:0x36
	v_lshl_add_u32 v102, v71, 2, v70
	v_bitop3_b32 v71, v64, v69, 1 bitop3:0x36
	v_lshl_add_u32 v103, v71, 2, v70
	v_bitop3_b32 v71, v64, v69, 2 bitop3:0x36
	v_bitop3_b32 v69, v64, v69, 3 bitop3:0x36
	v_lshl_add_u32 v105, v69, 2, v70
	v_or_b32_e32 v69, 28, v75
	v_lshl_add_u32 v104, v71, 2, v70
	v_lshl_add_u32 v70, v69, 8, s7
	v_bitop3_b32 v71, v75, v64, 28 bitop3:0x36
	v_lshl_add_u32 v106, v71, 2, v70
	v_bitop3_b32 v71, v64, v69, 1 bitop3:0x36
	v_lshl_add_u32 v107, v71, 2, v70
	v_bitop3_b32 v71, v64, v69, 2 bitop3:0x36
	v_bitop3_b32 v69, v64, v69, 3 bitop3:0x36
	v_lshl_add_u32 v109, v69, 2, v70
	v_or_b32_e32 v69, 36, v75
	v_or_b32_e32 v66, 1, v64
	v_lshl_add_u32 v108, v71, 2, v70
	v_lshl_add_u32 v70, v69, 8, s7
	v_bitop3_b32 v71, v69, v64, 7 bitop3:0x6c
	v_or_b32_e32 v67, 2, v64
	v_or_b32_e32 v68, 3, v64
	v_lshl_add_u32 v110, v71, 2, v70
	v_bitop3_b32 v71, v69, v66, 7 bitop3:0x6c
	v_lshl_add_u32 v111, v71, 2, v70
	v_bitop3_b32 v71, v69, v67, 7 bitop3:0x6c
	v_bitop3_b32 v69, v69, v68, 7 bitop3:0x6c
	v_lshl_add_u32 v113, v69, 2, v70
	v_or_b32_e32 v69, 40, v75
	v_lshl_add_u32 v112, v71, 2, v70
	v_lshl_add_u32 v70, v69, 8, s7
	v_bitop3_b32 v71, v69, v64, 11 bitop3:0x6c
	v_lshl_add_u32 v114, v71, 2, v70
	v_bitop3_b32 v71, v69, v66, 11 bitop3:0x6c
	v_lshl_add_u32 v115, v71, 2, v70
	v_bitop3_b32 v71, v69, v67, 11 bitop3:0x6c
	v_bitop3_b32 v69, v69, v68, 11 bitop3:0x6c
	v_lshl_add_u32 v117, v69, 2, v70
	v_or_b32_e32 v69, 44, v75
	v_lshl_add_u32 v116, v71, 2, v70
	v_lshl_add_u32 v70, v69, 8, s7
	v_bitop3_b32 v71, v69, v64, 15 bitop3:0x6c
	v_lshl_add_u32 v118, v71, 2, v70
	v_bitop3_b32 v71, v69, v66, 15 bitop3:0x6c
	v_lshl_add_u32 v119, v71, 2, v70
	v_bitop3_b32 v71, v69, v67, 15 bitop3:0x6c
	v_bitop3_b32 v69, v69, v68, 15 bitop3:0x6c
	v_lshl_add_u32 v121, v69, 2, v70
	v_or_b32_e32 v69, 48, v75
	v_lshl_add_u32 v120, v71, 2, v70
	v_lshl_add_u32 v70, v69, 8, s7
	v_bitop3_b32 v71, v69, v64, 19 bitop3:0x6c
	v_lshl_add_u32 v122, v71, 2, v70
	v_bitop3_b32 v71, v69, v66, 19 bitop3:0x6c
	v_lshl_add_u32 v123, v71, 2, v70
	v_bitop3_b32 v71, v69, v67, 19 bitop3:0x6c
	v_bitop3_b32 v69, v69, v68, 19 bitop3:0x6c
	v_lshl_add_u32 v125, v69, 2, v70
	v_or_b32_e32 v69, 52, v75
	v_lshl_add_u32 v124, v71, 2, v70
	v_lshl_add_u32 v70, v69, 8, s7
	v_bitop3_b32 v71, v69, v64, 23 bitop3:0x6c
	v_lshl_add_u32 v126, v71, 2, v70
	v_bitop3_b32 v71, v69, v66, 23 bitop3:0x6c
	v_lshl_add_u32 v127, v71, 2, v70
	v_bitop3_b32 v71, v69, v67, 23 bitop3:0x6c
	v_bitop3_b32 v69, v69, v68, 23 bitop3:0x6c
	v_lshl_add_u32 v129, v69, 2, v70
	v_or_b32_e32 v69, 56, v75
	v_lshl_add_u32 v128, v71, 2, v70
	v_lshl_add_u32 v70, v69, 8, s7
	v_bitop3_b32 v71, v69, v64, 27 bitop3:0x6c
	v_lshl_add_u32 v130, v71, 2, v70
	v_bitop3_b32 v71, v69, v66, 27 bitop3:0x6c
	v_lshl_add_u32 v131, v71, 2, v70
	v_bitop3_b32 v71, v69, v67, 27 bitop3:0x6c
	v_bitop3_b32 v69, v69, v68, 27 bitop3:0x6c
	v_lshl_add_u32 v133, v69, 2, v70
	v_or_b32_e32 v69, 60, v75
	v_lshl_add_u32 v132, v71, 2, v70
	v_lshl_add_u32 v70, v69, 8, s7
	v_bitop3_b32 v66, v69, v66, 31 bitop3:0x6c
	v_lshl_add_u32 v135, v66, 2, v70
	v_bitop3_b32 v66, v69, v67, 31 bitop3:0x6c
	v_and_b32_e32 v74, 63, v65
	v_lshl_add_u32 v136, v66, 2, v70
	v_bitop3_b32 v66, v69, v68, 31 bitop3:0x6c
	s_add_u32 s27, s21, 0x1a000000
	v_lshl_add_u32 v137, v66, 2, v70
	s_addc_u32 s30, s22, 0
	v_lshlrev_b32_e32 v66, 3, v74
	s_add_u32 s31, s21, 0x2000000
	v_and_b32_e32 v74, 56, v66
	v_bfe_u32 v138, v65, 3, 3
	v_and_b32_e32 v65, 24, v66
	s_addc_u32 s36, s22, 0
	v_lshl_add_u32 v67, v74, 8, s7
	v_lshlrev_b32_e32 v65, 2, v65
	v_lshlrev_b32_e32 v68, 2, v138
	s_add_u32 s37, s21, 0x1a00000
	v_add3_u32 v146, v67, v65, v68
	v_or_b32_e32 v65, 1, v74
	v_bitop3_b32 v71, v69, v64, 31 bitop3:0x6c
	s_addc_u32 s38, s22, 0
	v_bitop3_b32 v68, v65, v138, 25 bitop3:0x6c
	v_lshl_add_u32 v69, v65, 8, s7
	s_add_u32 s39, s21, 0x1800000
	v_lshl_add_u32 v147, v68, 2, v69
	v_or_b32_e32 v68, 2, v74
	v_lshl_add_u32 v134, v71, 2, v70
	s_addc_u32 s40, s22, 0
	v_bitop3_b32 v70, v68, v138, 26 bitop3:0x6c
	v_lshl_add_u32 v71, v68, 8, s7
	s_add_u32 s41, s21, 0x1500000
	v_or_b32_e32 v139, 8, v138
	v_or_b32_e32 v140, 16, v138
	v_or_b32_e32 v141, 24, v138
	v_or_b32_e32 v142, 32, v138
	v_or_b32_e32 v143, 40, v138
	v_or_b32_e32 v144, 48, v138
	v_or_b32_e32 v145, 56, v138
	v_lshl_add_u32 v148, v70, 2, v71
	v_or_b32_e32 v70, 3, v74
	s_addc_u32 s45, s22, 0
	v_bitop3_b32 v72, v70, v138, 27 bitop3:0x6c
	v_lshl_add_u32 v76, v70, 8, s7
	v_bitop3_b32 v155, v65, v139, 25 bitop3:0x6c
	v_bitop3_b32 v163, v65, v140, 25 bitop3:0x6c
	v_bitop3_b32 v171, v65, v141, 25 bitop3:0x6c
	v_bitop3_b32 v178, v65, v142, 25 bitop3:0x6c
	v_bitop3_b32 v186, v65, v143, 25 bitop3:0x6c
	v_bitop3_b32 v194, v65, v144, 25 bitop3:0x6c
	v_bitop3_b32 v65, v65, v145, 25 bitop3:0x6c
	s_add_u32 s46, s21, 0x1200000
	v_lshl_add_u32 v149, v72, 2, v76
	v_or_b32_e32 v72, 4, v74
	v_lshl_add_u32 v202, v65, 2, v69
	v_bitop3_b32 v65, v68, v145, 26 bitop3:0x6c
	s_addc_u32 s47, s22, 0
	v_bitop3_b32 v77, v72, v138, 28 bitop3:0x6c
	v_lshl_add_u32 v205, v72, 8, s7
	v_lshl_add_u32 v203, v65, 2, v71
	v_bitop3_b32 v65, v70, v145, 27 bitop3:0x6c
	s_add_u32 s48, s21, 0xe00000
	v_lshl_add_u32 v150, v77, 2, v205
	v_or_b32_e32 v77, 5, v74
	v_bitop3_b32 v158, v72, v139, 28 bitop3:0x6c
	v_bitop3_b32 v166, v72, v140, 28 bitop3:0x6c
	v_bitop3_b32 v174, v72, v141, 28 bitop3:0x6c
	v_bitop3_b32 v181, v72, v142, 28 bitop3:0x6c
	v_bitop3_b32 v189, v72, v143, 28 bitop3:0x6c
	v_bitop3_b32 v197, v72, v144, 28 bitop3:0x6c
	v_lshl_add_u32 v204, v65, 2, v76
	v_bitop3_b32 v65, v72, v145, 28 bitop3:0x6c
	s_addc_u32 s49, s22, 0
	v_bitop3_b32 v151, v77, v138, 29 bitop3:0x6c
	v_lshl_add_u32 v206, v77, 8, s7
	v_or_b32_e32 v207, 6, v74
	v_lshl_add_u32 v158, v158, 2, v205
	v_bitop3_b32 v159, v77, v139, 29 bitop3:0x6c
	v_lshl_add_u32 v166, v166, 2, v205
	v_bitop3_b32 v167, v77, v140, 29 bitop3:0x6c
	v_lshl_add_u32 v174, v174, 2, v205
	v_bitop3_b32 v175, v77, v141, 29 bitop3:0x6c
	v_lshl_add_u32 v181, v181, 2, v205
	v_bitop3_b32 v182, v77, v142, 29 bitop3:0x6c
	v_lshl_add_u32 v189, v189, 2, v205
	v_bitop3_b32 v190, v77, v143, 29 bitop3:0x6c
	v_lshl_add_u32 v197, v197, 2, v205
	v_bitop3_b32 v198, v77, v144, 29 bitop3:0x6c
	v_lshl_add_u32 v205, v65, 2, v205
	v_bitop3_b32 v65, v77, v145, 29 bitop3:0x6c
	s_add_u32 s50, s21, 0x200000
	v_lshl_add_u32 v151, v151, 2, v206
	v_lshl_add_u32 v208, v207, 8, s7
	v_or_b32_e32 v209, 7, v74
	v_lshl_add_u32 v159, v159, 2, v206
	v_lshl_add_u32 v167, v167, 2, v206
	v_lshl_add_u32 v175, v175, 2, v206
	v_lshl_add_u32 v182, v182, 2, v206
	v_lshl_add_u32 v190, v190, 2, v206
	v_lshl_add_u32 v198, v198, 2, v206
	v_lshl_add_u32 v206, v65, 2, v206
	v_bitop3_b32 v65, v207, v145, 30 bitop3:0x6c
	s_addc_u32 s51, s22, 0
	v_bitop3_b32 v152, v207, v138, 30 bitop3:0x6c
	v_bitop3_b32 v153, v209, v138, 31 bitop3:0x6c
	v_lshl_add_u32 v210, v209, 8, s7
	v_bitop3_b32 v154, v66, v139, 24 bitop3:0x6c
	v_bitop3_b32 v156, v68, v139, 26 bitop3:0x6c
	v_bitop3_b32 v157, v70, v139, 27 bitop3:0x6c
	v_bitop3_b32 v160, v207, v139, 30 bitop3:0x6c
	v_bitop3_b32 v161, v209, v139, 31 bitop3:0x6c
	v_bitop3_b32 v162, v66, v140, 24 bitop3:0x6c
	v_bitop3_b32 v164, v68, v140, 26 bitop3:0x6c
	v_bitop3_b32 v165, v70, v140, 27 bitop3:0x6c
	v_bitop3_b32 v168, v207, v140, 30 bitop3:0x6c
	v_bitop3_b32 v169, v209, v140, 31 bitop3:0x6c
	v_bitop3_b32 v170, v66, v138, 24 bitop3:0x4e
	v_bitop3_b32 v172, v68, v141, 26 bitop3:0x6c
	v_bitop3_b32 v173, v70, v141, 27 bitop3:0x6c
	v_bitop3_b32 v176, v207, v141, 30 bitop3:0x6c
	v_bitop3_b32 v177, v209, v141, 31 bitop3:0x6c
	v_bitop3_b32 v179, v68, v142, 26 bitop3:0x6c
	v_bitop3_b32 v180, v70, v142, 27 bitop3:0x6c
	v_bitop3_b32 v183, v207, v142, 30 bitop3:0x6c
	v_bitop3_b32 v184, v209, v142, 31 bitop3:0x6c
	v_bitop3_b32 v185, v66, v143, 24 bitop3:0x6c
	v_bitop3_b32 v187, v68, v143, 26 bitop3:0x6c
	v_bitop3_b32 v188, v70, v143, 27 bitop3:0x6c
	v_bitop3_b32 v191, v207, v143, 30 bitop3:0x6c
	v_bitop3_b32 v192, v209, v143, 31 bitop3:0x6c
	v_bitop3_b32 v193, v66, v144, 24 bitop3:0x6c
	v_bitop3_b32 v195, v68, v144, 26 bitop3:0x6c
	v_bitop3_b32 v196, v70, v144, 27 bitop3:0x6c
	v_bitop3_b32 v199, v207, v144, 30 bitop3:0x6c
	v_bitop3_b32 v200, v209, v144, 31 bitop3:0x6c
	v_bitop3_b32 v66, v66, v145, 24 bitop3:0x6c
	v_lshl_add_u32 v207, v65, 2, v208
	v_bitop3_b32 v65, v209, v145, 31 bitop3:0x6c
	s_add_i32 s7, s19, s18
	v_lshl_add_u32 v152, v152, 2, v208
	v_lshl_add_u32 v153, v153, 2, v210
	v_lshl_add_u32 v154, v154, 2, v67
	v_lshl_add_u32 v155, v155, 2, v69
	v_lshl_add_u32 v156, v156, 2, v71
	v_lshl_add_u32 v157, v157, 2, v76
	v_lshl_add_u32 v160, v160, 2, v208
	v_lshl_add_u32 v161, v161, 2, v210
	v_lshl_add_u32 v162, v162, 2, v67
	v_lshl_add_u32 v163, v163, 2, v69
	v_lshl_add_u32 v164, v164, 2, v71
	v_lshl_add_u32 v165, v165, 2, v76
	v_lshl_add_u32 v168, v168, 2, v208
	v_lshl_add_u32 v169, v169, 2, v210
	v_lshl_add_u32 v170, v170, 2, v67
	v_lshl_add_u32 v171, v171, 2, v69
	v_lshl_add_u32 v172, v172, 2, v71
	v_lshl_add_u32 v173, v173, 2, v76
	v_lshl_add_u32 v176, v176, 2, v208
	v_lshl_add_u32 v177, v177, 2, v210
	v_lshl_add_u32 v178, v178, 2, v69
	v_lshl_add_u32 v179, v179, 2, v71
	v_lshl_add_u32 v180, v180, 2, v76
	v_lshl_add_u32 v183, v183, 2, v208
	v_lshl_add_u32 v184, v184, 2, v210
	v_lshl_add_u32 v185, v185, 2, v67
	v_lshl_add_u32 v186, v186, 2, v69
	v_lshl_add_u32 v187, v187, 2, v71
	v_lshl_add_u32 v188, v188, 2, v76
	v_lshl_add_u32 v191, v191, 2, v208
	v_lshl_add_u32 v192, v192, 2, v210
	v_lshl_add_u32 v193, v193, 2, v67
	v_lshl_add_u32 v194, v194, 2, v69
	v_lshl_add_u32 v195, v195, 2, v71
	v_lshl_add_u32 v196, v196, 2, v76
	v_lshl_add_u32 v199, v199, 2, v208
	v_lshl_add_u32 v200, v200, 2, v210
	v_lshl_add_u32 v201, v66, 2, v67
	v_lshl_add_u32 v208, v65, 2, v210
	s_add_i32 s52, s7, 0x7400
	s_lshl_b32 s53, s20, 6
	v_lshlrev_b32_e32 v76, 2, v64
	v_lshlrev_b32_e32 v72, 1, v74
	s_branch .LBB0_643

.LBB0_639:
	s_lshl_b32 s16, s19, 6
	v_or_b32_e32 v0, s16, v75
	s_ashr_i32 s7, s16, 31
	s_mul_i32 s7, s20, s7
	v_mul_lo_u32 v2, s21, v0
	v_mad_u64_u32 v[0:1], s[56:57], s20, v0, 0
	v_add3_u32 v1, v1, s7, v2
	v_lshl_add_u64 v[0:1], v[0:1], 2, s[14:15]
	s_ashr_i32 s19, s18, 31
	v_lshl_add_u64 v[0:1], s[18:19], 2, v[0:1]
	v_mov_b32_e32 v77, v73
	v_lshl_add_u64 v[0:1], v[0:1], 0, v[76:77]
	s_lshl_b64 s[14:15], s[20:21], 4
	v_lshl_add_u64 v[2:3], v[0:1], 0, s[14:15]
	global_load_dwordx4 v[16:19], v[0:1], off nt
	global_load_dwordx4 v[8:11], v[2:3], off nt
	v_lshl_add_u64 v[0:1], v[2:3], 0, s[14:15]
	v_lshl_add_u64 v[2:3], v[0:1], 0, s[14:15]
	global_load_dwordx4 v[28:31], v[0:1], off nt
	global_load_dwordx4 v[20:23], v[2:3], off nt
	v_lshl_add_u64 v[0:1], v[2:3], 0, s[14:15]
	v_lshl_add_u64 v[2:3], v[0:1], 0, s[14:15]
	global_load_dwordx4 v[40:43], v[0:1], off nt
	global_load_dwordx4 v[32:35], v[2:3], off nt
	v_lshl_add_u64 v[0:1], v[2:3], 0, s[14:15]
	v_lshl_add_u64 v[2:3], v[0:1], 0, s[14:15]
	global_load_dwordx4 v[56:59], v[0:1], off nt
	global_load_dwordx4 v[44:47], v[2:3], off nt
	v_lshl_add_u64 v[0:1], v[2:3], 0, s[14:15]
	global_load_dwordx4 v[48:51], v[0:1], off nt
	v_lshl_add_u64 v[0:1], v[0:1], 0, s[14:15]
	global_load_dwordx4 v[36:39], v[0:1], off nt
	v_lshl_add_u64 v[0:1], v[0:1], 0, s[14:15]
	global_load_dwordx4 v[52:55], v[0:1], off nt
	v_lshl_add_u64 v[0:1], v[0:1], 0, s[14:15]
	global_load_dwordx4 v[12:15], v[0:1], off nt
	v_lshl_add_u64 v[0:1], v[0:1], 0, s[14:15]
	v_lshl_add_u64 v[4:5], v[0:1], 0, s[14:15]
	v_lshl_add_u64 v[60:61], v[4:5], 0, s[14:15]
	global_load_dwordx4 v[24:27], v[0:1], off nt
	s_nop 0
	global_load_dwordx4 v[0:3], v[4:5], off nt
	s_nop 0
	global_load_dwordx4 v[4:7], v[60:61], off nt
	v_lshl_add_u64 v[60:61], v[60:61], 0, s[14:15]
	global_load_dwordx4 v[60:63], v[60:61], off nt

.LBB0_846:
	s_lshl_b32 s8, s15, 14
	s_add_i32 s9, s8, 0
	s_lshl_b32 s8, s26, 6
	v_bfe_u32 v75, v65, 4, 2
	v_or_b32_e32 v0, s8, v75
	s_ashr_i32 s15, s8, 31
	s_mul_i32 s15, s16, s15
	v_mul_lo_u32 v2, s17, v0
	v_mad_u64_u32 v[0:1], s[26:27], s16, v0, 0
	v_add3_u32 v1, v1, s15, v2
	v_lshlrev_b32_e32 v2, 2, v65
	v_lshl_add_u64 v[0:1], v[0:1], 2, s[12:13]
	s_ashr_i32 s15, s14, 31
	v_and_b32_e32 v64, 60, v2
	v_lshl_add_u64 v[0:1], s[14:15], 2, v[0:1]
	v_mov_b32_e32 v73, 0
	v_lshlrev_b32_e32 v72, 2, v64
	s_lshl_b64 s[12:13], s[16:17], 4
	s_mov_b32 s19, 0
	v_lshl_add_u64 v[66:67], v[0:1], 0, v[72:73]
	s_mul_i32 s18, s16, 0xf0
	s_sub_u32 s12, 0, s12
	v_lshl_add_u64 v[68:69], v[66:67], 0, s[18:19]
	s_subb_u32 s13, 0, s13
	v_lshl_add_u64 v[8:9], v[68:69], 0, s[12:13]
	v_lshl_add_u64 v[10:11], v[8:9], 0, s[12:13]
	global_load_dwordx4 v[4:7], v[8:9], off nt
	global_load_dwordx4 v[0:3], v[10:11], off nt
	v_lshl_add_u64 v[8:9], v[10:11], 0, s[12:13]
	v_lshl_add_u64 v[10:11], v[8:9], 0, s[12:13]
	global_load_dwordx4 v[24:27], v[8:9], off nt
	global_load_dwordx4 v[12:15], v[10:11], off nt
	v_lshl_add_u64 v[8:9], v[10:11], 0, s[12:13]
	v_lshl_add_u64 v[10:11], v[8:9], 0, s[12:13]
	global_load_dwordx4 v[52:55], v[8:9], off nt
	global_load_dwordx4 v[36:39], v[10:11], off nt
	v_lshl_add_u64 v[8:9], v[10:11], 0, s[12:13]
	global_load_dwordx4 v[48:51], v[8:9], off nt
	v_lshl_add_u64 v[8:9], v[8:9], 0, s[12:13]
	global_load_dwordx4 v[44:47], v[8:9], off nt
	v_lshl_add_u64 v[8:9], v[8:9], 0, s[12:13]
	global_load_dwordx4 v[56:59], v[8:9], off nt
	v_lshl_add_u64 v[8:9], v[8:9], 0, s[12:13]
	global_load_dwordx4 v[32:35], v[8:9], off nt
	v_lshl_add_u64 v[8:9], v[8:9], 0, s[12:13]
	global_load_dwordx4 v[40:43], v[8:9], off nt
	v_lshl_add_u64 v[8:9], v[8:9], 0, s[12:13]
	global_load_dwordx4 v[20:23], v[8:9], off nt
	v_lshl_add_u64 v[8:9], v[8:9], 0, s[12:13]
	v_lshl_add_u64 v[70:71], v[8:9], 0, s[12:13]
	global_load_dwordx4 v[28:31], v[8:9], off nt
	s_nop 0
	global_load_dwordx4 v[8:11], v[70:71], off nt
	global_load_dwordx4 v[60:63], v[68:69], off nt
	global_load_dwordx4 v[16:19], v[66:67], off nt
	v_lshl_add_u32 v69, v75, 8, s9
	v_lshlrev_b32_e32 v70, 2, v75
	v_add3_u32 v78, v69, v70, v72
	v_bitop3_b32 v70, v64, v75, 1 bitop3:0x36
	v_lshl_add_u32 v79, v70, 2, v69
	v_bitop3_b32 v70, v64, v75, 2 bitop3:0x36
	v_lshl_add_u32 v80, v70, 2, v69
	v_bitop3_b32 v70, v64, v75, 3 bitop3:0x36
	v_lshl_add_u32 v81, v70, 2, v69
	v_or_b32_e32 v69, 4, v75
	v_lshl_add_u32 v70, v69, 8, s9
	v_bitop3_b32 v71, v75, v64, 4 bitop3:0x36
	v_lshl_add_u32 v82, v71, 2, v70
	v_bitop3_b32 v71, v64, v69, 1 bitop3:0x36
	v_lshl_add_u32 v83, v71, 2, v70
	v_bitop3_b32 v71, v64, v69, 2 bitop3:0x36
	v_bitop3_b32 v69, v64, v69, 3 bitop3:0x36
	v_lshl_add_u32 v85, v69, 2, v70
	v_or_b32_e32 v69, 8, v75
	v_lshl_add_u32 v84, v71, 2, v70
	v_lshl_add_u32 v70, v69, 8, s9
	v_bitop3_b32 v71, v75, v64, 8 bitop3:0x36
	v_lshl_add_u32 v86, v71, 2, v70
	v_bitop3_b32 v71, v64, v69, 1 bitop3:0x36
	v_lshl_add_u32 v87, v71, 2, v70
	v_bitop3_b32 v71, v64, v69, 2 bitop3:0x36
	v_bitop3_b32 v69, v64, v69, 3 bitop3:0x36
	v_lshl_add_u32 v89, v69, 2, v70
	v_or_b32_e32 v69, 12, v75
	v_lshl_add_u32 v88, v71, 2, v70
	v_lshl_add_u32 v70, v69, 8, s9
	v_bitop3_b32 v71, v75, v64, 12 bitop3:0x36
	v_lshl_add_u32 v90, v71, 2, v70
	v_bitop3_b32 v71, v64, v69, 1 bitop3:0x36
	v_lshl_add_u32 v91, v71, 2, v70
	v_bitop3_b32 v71, v64, v69, 2 bitop3:0x36
	v_bitop3_b32 v69, v64, v69, 3 bitop3:0x36
	v_lshl_add_u32 v93, v69, 2, v70
	v_or_b32_e32 v69, 16, v75
	v_lshl_add_u32 v92, v71, 2, v70
	v_lshl_add_u32 v70, v69, 8, s9
	v_bitop3_b32 v71, v75, v64, 16 bitop3:0x36
	v_lshl_add_u32 v94, v71, 2, v70
	v_bitop3_b32 v71, v64, v69, 1 bitop3:0x36
	v_lshl_add_u32 v95, v71, 2, v70
	v_bitop3_b32 v71, v64, v69, 2 bitop3:0x36
	v_bitop3_b32 v69, v64, v69, 3 bitop3:0x36
	v_lshl_add_u32 v97, v69, 2, v70
	v_or_b32_e32 v69, 20, v75
	v_lshl_add_u32 v96, v71, 2, v70
	v_lshl_add_u32 v70, v69, 8, s9
	v_bitop3_b32 v71, v75, v64, 20 bitop3:0x36
	v_lshl_add_u32 v98, v71, 2, v70
	v_bitop3_b32 v71, v64, v69, 1 bitop3:0x36
	v_lshl_add_u32 v99, v71, 2, v70
	v_bitop3_b32 v71, v64, v69, 2 bitop3:0x36
	v_bitop3_b32 v69, v64, v69, 3 bitop3:0x36
	v_lshl_add_u32 v101, v69, 2, v70
	v_or_b32_e32 v69, 24, v75
	v_lshl_add_u32 v100, v71, 2, v70
	v_lshl_add_u32 v70, v69, 8, s9
	v_bitop3_b32 v71, v75, v64, 24 bitop3:0x36
	v_lshl_add_u32 v102, v71, 2, v70
	v_bitop3_b32 v71, v64, v69, 1 bitop3:0x36
	v_lshl_add_u32 v103, v71, 2, v70
	v_bitop3_b32 v71, v64, v69, 2 bitop3:0x36
	v_bitop3_b32 v69, v64, v69, 3 bitop3:0x36
	v_lshl_add_u32 v105, v69, 2, v70
	v_or_b32_e32 v69, 28, v75
	v_lshl_add_u32 v104, v71, 2, v70
	v_lshl_add_u32 v70, v69, 8, s9
	v_bitop3_b32 v71, v75, v64, 28 bitop3:0x36
	v_lshl_add_u32 v106, v71, 2, v70
	v_bitop3_b32 v71, v64, v69, 1 bitop3:0x36
	v_lshl_add_u32 v107, v71, 2, v70
	v_bitop3_b32 v71, v64, v69, 2 bitop3:0x36
	v_bitop3_b32 v69, v64, v69, 3 bitop3:0x36
	v_lshl_add_u32 v109, v69, 2, v70
	v_or_b32_e32 v69, 36, v75
	v_or_b32_e32 v66, 1, v64
	v_lshl_add_u32 v108, v71, 2, v70
	v_lshl_add_u32 v70, v69, 8, s9
	v_bitop3_b32 v71, v69, v64, 7 bitop3:0x6c
	v_or_b32_e32 v67, 2, v64
	v_or_b32_e32 v68, 3, v64
	v_lshl_add_u32 v110, v71, 2, v70
	v_bitop3_b32 v71, v69, v66, 7 bitop3:0x6c
	v_lshl_add_u32 v111, v71, 2, v70
	v_bitop3_b32 v71, v69, v67, 7 bitop3:0x6c
	v_bitop3_b32 v69, v69, v68, 7 bitop3:0x6c
	v_lshl_add_u32 v113, v69, 2, v70
	v_or_b32_e32 v69, 40, v75
	v_lshl_add_u32 v112, v71, 2, v70
	v_lshl_add_u32 v70, v69, 8, s9
	v_bitop3_b32 v71, v69, v64, 11 bitop3:0x6c
	v_lshl_add_u32 v114, v71, 2, v70
	v_bitop3_b32 v71, v69, v66, 11 bitop3:0x6c
	v_lshl_add_u32 v115, v71, 2, v70
	v_bitop3_b32 v71, v69, v67, 11 bitop3:0x6c
	v_bitop3_b32 v69, v69, v68, 11 bitop3:0x6c
	v_lshl_add_u32 v117, v69, 2, v70
	v_or_b32_e32 v69, 44, v75
	v_lshl_add_u32 v116, v71, 2, v70
	v_lshl_add_u32 v70, v69, 8, s9
	v_bitop3_b32 v71, v69, v64, 15 bitop3:0x6c
	v_lshl_add_u32 v118, v71, 2, v70
	v_bitop3_b32 v71, v69, v66, 15 bitop3:0x6c
	v_lshl_add_u32 v119, v71, 2, v70
	v_bitop3_b32 v71, v69, v67, 15 bitop3:0x6c
	v_bitop3_b32 v69, v69, v68, 15 bitop3:0x6c
	v_lshl_add_u32 v121, v69, 2, v70
	v_or_b32_e32 v69, 48, v75
	v_lshl_add_u32 v120, v71, 2, v70
	v_lshl_add_u32 v70, v69, 8, s9
	v_bitop3_b32 v71, v69, v64, 19 bitop3:0x6c
	v_lshl_add_u32 v122, v71, 2, v70
	v_bitop3_b32 v71, v69, v66, 19 bitop3:0x6c
	v_lshl_add_u32 v123, v71, 2, v70
	v_bitop3_b32 v71, v69, v67, 19 bitop3:0x6c
	v_bitop3_b32 v69, v69, v68, 19 bitop3:0x6c
	v_lshl_add_u32 v125, v69, 2, v70
	v_or_b32_e32 v69, 52, v75
	v_lshl_add_u32 v124, v71, 2, v70
	v_lshl_add_u32 v70, v69, 8, s9
	v_bitop3_b32 v71, v69, v64, 23 bitop3:0x6c
	v_lshl_add_u32 v126, v71, 2, v70
	v_bitop3_b32 v71, v69, v66, 23 bitop3:0x6c
	v_lshl_add_u32 v127, v71, 2, v70
	v_bitop3_b32 v71, v69, v67, 23 bitop3:0x6c
	v_bitop3_b32 v69, v69, v68, 23 bitop3:0x6c
	v_lshl_add_u32 v129, v69, 2, v70
	v_or_b32_e32 v69, 56, v75
	v_lshl_add_u32 v128, v71, 2, v70
	v_lshl_add_u32 v70, v69, 8, s9
	v_bitop3_b32 v71, v69, v64, 27 bitop3:0x6c
	v_lshl_add_u32 v130, v71, 2, v70
	v_bitop3_b32 v71, v69, v66, 27 bitop3:0x6c
	v_lshl_add_u32 v131, v71, 2, v70
	v_bitop3_b32 v71, v69, v67, 27 bitop3:0x6c
	v_bitop3_b32 v69, v69, v68, 27 bitop3:0x6c
	v_lshl_add_u32 v133, v69, 2, v70
	v_or_b32_e32 v69, 60, v75
	v_lshl_add_u32 v132, v71, 2, v70
	v_lshl_add_u32 v70, v69, 8, s9
	v_bitop3_b32 v66, v69, v66, 31 bitop3:0x6c
	v_lshl_add_u32 v135, v66, 2, v70
	v_bitop3_b32 v66, v69, v67, 31 bitop3:0x6c
	s_add_u32 s37, s23, 0x1a000000
	v_and_b32_e32 v74, 63, v65
	v_lshl_add_u32 v136, v66, 2, v70
	v_bitop3_b32 v66, v69, v68, 31 bitop3:0x6c
	s_addc_u32 s38, s24, 0
	v_lshl_add_u32 v137, v66, 2, v70
	s_add_u32 s39, s23, 0x2000000
	v_lshlrev_b32_e32 v66, 3, v74
	s_addc_u32 s40, s24, 0
	v_and_b32_e32 v74, 56, v66
	v_bfe_u32 v138, v65, 3, 3
	v_and_b32_e32 v65, 24, v66
	s_add_u32 s41, s23, 0x1a00000
	v_lshl_add_u32 v67, v74, 8, s9
	v_lshlrev_b32_e32 v65, 2, v65
	v_lshlrev_b32_e32 v68, 2, v138
	s_addc_u32 s45, s24, 0
	v_add3_u32 v146, v67, v65, v68
	v_or_b32_e32 v65, 1, v74
	v_bitop3_b32 v71, v69, v64, 31 bitop3:0x6c
	s_add_u32 s46, s23, 0x1800000
	v_bitop3_b32 v68, v65, v138, 25 bitop3:0x6c
	v_lshl_add_u32 v69, v65, 8, s9
	s_addc_u32 s47, s24, 0
	v_lshl_add_u32 v147, v68, 2, v69
	v_or_b32_e32 v68, 2, v74
	v_lshl_add_u32 v134, v71, 2, v70
	s_add_u32 s48, s23, 0x1500000
	v_bitop3_b32 v70, v68, v138, 26 bitop3:0x6c
	v_lshl_add_u32 v71, v68, 8, s9
	s_addc_u32 s49, s24, 0
	v_or_b32_e32 v139, 8, v138
	v_or_b32_e32 v140, 16, v138
	v_or_b32_e32 v141, 24, v138
	v_or_b32_e32 v142, 32, v138
	v_or_b32_e32 v143, 40, v138
	v_or_b32_e32 v144, 48, v138
	v_or_b32_e32 v145, 56, v138
	v_lshl_add_u32 v148, v70, 2, v71
	v_or_b32_e32 v70, 3, v74
	s_add_u32 s50, s23, 0x1200000
	v_bitop3_b32 v72, v70, v138, 27 bitop3:0x6c
	v_lshl_add_u32 v76, v70, 8, s9
	v_bitop3_b32 v155, v65, v139, 25 bitop3:0x6c
	v_bitop3_b32 v163, v65, v140, 25 bitop3:0x6c
	v_bitop3_b32 v171, v65, v141, 25 bitop3:0x6c
	v_bitop3_b32 v178, v65, v142, 25 bitop3:0x6c
	v_bitop3_b32 v186, v65, v143, 25 bitop3:0x6c
	v_bitop3_b32 v194, v65, v144, 25 bitop3:0x6c
	v_bitop3_b32 v65, v65, v145, 25 bitop3:0x6c
	s_addc_u32 s51, s24, 0
	v_lshl_add_u32 v149, v72, 2, v76
	v_or_b32_e32 v72, 4, v74
	v_lshl_add_u32 v202, v65, 2, v69
	v_bitop3_b32 v65, v68, v145, 26 bitop3:0x6c
	s_add_u32 s52, s23, 0xe00000
	v_bitop3_b32 v77, v72, v138, 28 bitop3:0x6c
	v_lshl_add_u32 v205, v72, 8, s9
	v_lshl_add_u32 v203, v65, 2, v71
	v_bitop3_b32 v65, v70, v145, 27 bitop3:0x6c
	s_addc_u32 s53, s24, 0
	v_lshl_add_u32 v150, v77, 2, v205
	v_or_b32_e32 v77, 5, v74
	v_bitop3_b32 v158, v72, v139, 28 bitop3:0x6c
	v_bitop3_b32 v166, v72, v140, 28 bitop3:0x6c
	v_bitop3_b32 v174, v72, v141, 28 bitop3:0x6c
	v_bitop3_b32 v181, v72, v142, 28 bitop3:0x6c
	v_bitop3_b32 v189, v72, v143, 28 bitop3:0x6c
	v_bitop3_b32 v197, v72, v144, 28 bitop3:0x6c
	v_lshl_add_u32 v204, v65, 2, v76
	v_bitop3_b32 v65, v72, v145, 28 bitop3:0x6c
	s_add_u32 s54, s23, 0x200000
	v_bitop3_b32 v151, v77, v138, 29 bitop3:0x6c
	v_lshl_add_u32 v206, v77, 8, s9
	v_or_b32_e32 v207, 6, v74
	v_or_b32_e32 v209, 7, v74
	v_lshl_add_u32 v158, v158, 2, v205
	v_bitop3_b32 v159, v77, v139, 29 bitop3:0x6c
	v_lshl_add_u32 v166, v166, 2, v205
	v_bitop3_b32 v167, v77, v140, 29 bitop3:0x6c
	v_lshl_add_u32 v174, v174, 2, v205
	v_bitop3_b32 v175, v77, v141, 29 bitop3:0x6c
	v_lshl_add_u32 v181, v181, 2, v205
	v_bitop3_b32 v182, v77, v142, 29 bitop3:0x6c
	v_lshl_add_u32 v189, v189, 2, v205
	v_bitop3_b32 v190, v77, v143, 29 bitop3:0x6c
	v_lshl_add_u32 v197, v197, 2, v205
	v_bitop3_b32 v198, v77, v144, 29 bitop3:0x6c
	v_lshl_add_u32 v205, v65, 2, v205
	v_bitop3_b32 v65, v77, v145, 29 bitop3:0x6c
	s_addc_u32 s55, s24, 0
	v_lshl_add_u32 v151, v151, 2, v206
	v_lshl_add_u32 v208, v207, 8, s9
	v_lshl_add_u32 v210, v209, 8, s9
	v_lshl_add_u32 v159, v159, 2, v206
	v_lshl_add_u32 v167, v167, 2, v206
	v_lshl_add_u32 v175, v175, 2, v206
	v_lshl_add_u32 v182, v182, 2, v206
	v_lshl_add_u32 v190, v190, 2, v206
	v_lshl_add_u32 v198, v198, 2, v206
	v_lshl_add_u32 v206, v65, 2, v206
	v_bitop3_b32 v65, v207, v145, 30 bitop3:0x6c
	s_add_i32 s9, s22, s21
	v_bitop3_b32 v152, v207, v138, 30 bitop3:0x6c
	v_bitop3_b32 v153, v209, v138, 31 bitop3:0x6c
	v_bitop3_b32 v154, v66, v139, 24 bitop3:0x6c
	v_bitop3_b32 v156, v68, v139, 26 bitop3:0x6c
	v_bitop3_b32 v157, v70, v139, 27 bitop3:0x6c
	v_bitop3_b32 v160, v207, v139, 30 bitop3:0x6c
	v_bitop3_b32 v161, v209, v139, 31 bitop3:0x6c
	v_bitop3_b32 v162, v66, v140, 24 bitop3:0x6c
	v_bitop3_b32 v164, v68, v140, 26 bitop3:0x6c
	v_bitop3_b32 v165, v70, v140, 27 bitop3:0x6c
	v_bitop3_b32 v168, v207, v140, 30 bitop3:0x6c
	v_bitop3_b32 v169, v209, v140, 31 bitop3:0x6c
	v_bitop3_b32 v170, v66, v138, 24 bitop3:0x4e
	v_bitop3_b32 v172, v68, v141, 26 bitop3:0x6c
	v_bitop3_b32 v173, v70, v141, 27 bitop3:0x6c
	v_bitop3_b32 v176, v207, v141, 30 bitop3:0x6c
	v_bitop3_b32 v177, v209, v141, 31 bitop3:0x6c
	v_bitop3_b32 v179, v68, v142, 26 bitop3:0x6c
	v_bitop3_b32 v180, v70, v142, 27 bitop3:0x6c
	v_bitop3_b32 v183, v207, v142, 30 bitop3:0x6c
	v_bitop3_b32 v184, v209, v142, 31 bitop3:0x6c
	v_bitop3_b32 v185, v66, v143, 24 bitop3:0x6c
	v_bitop3_b32 v187, v68, v143, 26 bitop3:0x6c
	v_bitop3_b32 v188, v70, v143, 27 bitop3:0x6c
	v_bitop3_b32 v191, v207, v143, 30 bitop3:0x6c
	v_bitop3_b32 v192, v209, v143, 31 bitop3:0x6c
	v_bitop3_b32 v193, v66, v144, 24 bitop3:0x6c
	v_bitop3_b32 v195, v68, v144, 26 bitop3:0x6c
	v_bitop3_b32 v196, v70, v144, 27 bitop3:0x6c
	v_bitop3_b32 v199, v207, v144, 30 bitop3:0x6c
	v_bitop3_b32 v200, v209, v144, 31 bitop3:0x6c
	v_bitop3_b32 v66, v66, v145, 24 bitop3:0x6c
	v_lshl_add_u32 v207, v65, 2, v208
	v_bitop3_b32 v65, v209, v145, 31 bitop3:0x6c
	s_add_i32 s56, s9, 0x6800
	s_lshl_b32 s9, s20, 9
	s_lshl_b32 s12, s21, 6
	v_lshl_add_u32 v152, v152, 2, v208
	v_lshl_add_u32 v153, v153, 2, v210
	v_lshl_add_u32 v154, v154, 2, v67
	v_lshl_add_u32 v155, v155, 2, v69
	v_lshl_add_u32 v156, v156, 2, v71
	v_lshl_add_u32 v157, v157, 2, v76
	v_lshl_add_u32 v160, v160, 2, v208
	v_lshl_add_u32 v161, v161, 2, v210
	v_lshl_add_u32 v162, v162, 2, v67
	v_lshl_add_u32 v163, v163, 2, v69
	v_lshl_add_u32 v164, v164, 2, v71
	v_lshl_add_u32 v165, v165, 2, v76
	v_lshl_add_u32 v168, v168, 2, v208
	v_lshl_add_u32 v169, v169, 2, v210
	v_lshl_add_u32 v170, v170, 2, v67
	v_lshl_add_u32 v171, v171, 2, v69
	v_lshl_add_u32 v172, v172, 2, v71
	v_lshl_add_u32 v173, v173, 2, v76
	v_lshl_add_u32 v176, v176, 2, v208
	v_lshl_add_u32 v177, v177, 2, v210
	v_lshl_add_u32 v178, v178, 2, v69
	v_lshl_add_u32 v179, v179, 2, v71
	v_lshl_add_u32 v180, v180, 2, v76
	v_lshl_add_u32 v183, v183, 2, v208
	v_lshl_add_u32 v184, v184, 2, v210
	v_lshl_add_u32 v185, v185, 2, v67
	v_lshl_add_u32 v186, v186, 2, v69
	v_lshl_add_u32 v187, v187, 2, v71
	v_lshl_add_u32 v188, v188, 2, v76
	v_lshl_add_u32 v191, v191, 2, v208
	v_lshl_add_u32 v192, v192, 2, v210
	v_lshl_add_u32 v193, v193, 2, v67
	v_lshl_add_u32 v194, v194, 2, v69
	v_lshl_add_u32 v195, v195, 2, v71
	v_lshl_add_u32 v196, v196, 2, v76
	v_lshl_add_u32 v199, v199, 2, v208
	v_lshl_add_u32 v200, v200, 2, v210
	v_lshl_add_u32 v201, v66, 2, v67
	v_lshl_add_u32 v208, v65, 2, v210
	s_add_i32 s57, s9, s12
	v_lshlrev_b32_e32 v76, 2, v64
	v_lshlrev_b32_e32 v72, 1, v74
	s_branch .LBB0_852

.LBB0_848:
	s_lshl_b32 s20, s23, 6
	v_or_b32_e32 v0, s20, v75
	s_ashr_i32 s9, s20, 31
	s_mul_i32 s9, s24, s9
	v_mul_lo_u32 v2, s25, v0
	v_mad_u64_u32 v[0:1], s[60:61], s24, v0, 0
	v_add3_u32 v1, v1, s9, v2
	v_lshl_add_u64 v[0:1], v[0:1], 2, s[18:19]
	s_ashr_i32 s23, s22, 31
	v_lshl_add_u64 v[0:1], s[22:23], 2, v[0:1]
	v_mov_b32_e32 v77, v73
	v_lshl_add_u64 v[0:1], v[0:1], 0, v[76:77]
	s_lshl_b64 s[18:19], s[24:25], 4
	v_lshl_add_u64 v[2:3], v[0:1], 0, s[18:19]
	global_load_dwordx4 v[16:19], v[0:1], off nt
	global_load_dwordx4 v[8:11], v[2:3], off nt
	v_lshl_add_u64 v[0:1], v[2:3], 0, s[18:19]
	v_lshl_add_u64 v[2:3], v[0:1], 0, s[18:19]
	global_load_dwordx4 v[28:31], v[0:1], off nt
	global_load_dwordx4 v[20:23], v[2:3], off nt
	v_lshl_add_u64 v[0:1], v[2:3], 0, s[18:19]
	v_lshl_add_u64 v[2:3], v[0:1], 0, s[18:19]
	global_load_dwordx4 v[40:43], v[0:1], off nt
	global_load_dwordx4 v[32:35], v[2:3], off nt
	v_lshl_add_u64 v[0:1], v[2:3], 0, s[18:19]
	v_lshl_add_u64 v[2:3], v[0:1], 0, s[18:19]
	global_load_dwordx4 v[56:59], v[0:1], off nt
	global_load_dwordx4 v[44:47], v[2:3], off nt
	v_lshl_add_u64 v[0:1], v[2:3], 0, s[18:19]
	global_load_dwordx4 v[48:51], v[0:1], off nt
	v_lshl_add_u64 v[0:1], v[0:1], 0, s[18:19]
	global_load_dwordx4 v[36:39], v[0:1], off nt
	v_lshl_add_u64 v[0:1], v[0:1], 0, s[18:19]
	global_load_dwordx4 v[52:55], v[0:1], off nt
	v_lshl_add_u64 v[0:1], v[0:1], 0, s[18:19]
	global_load_dwordx4 v[12:15], v[0:1], off nt
	v_lshl_add_u64 v[0:1], v[0:1], 0, s[18:19]
	v_lshl_add_u64 v[4:5], v[0:1], 0, s[18:19]
	v_lshl_add_u64 v[60:61], v[4:5], 0, s[18:19]
	global_load_dwordx4 v[24:27], v[0:1], off nt
	s_nop 0
	global_load_dwordx4 v[0:3], v[4:5], off nt
	s_nop 0
	global_load_dwordx4 v[4:7], v[60:61], off nt
	v_lshl_add_u64 v[60:61], v[60:61], 0, s[18:19]
	global_load_dwordx4 v[60:63], v[60:61], off nt

.LBB0_933:
	s_lshl_b32 s8, s15, 14
	s_add_i32 s9, s8, 0
	s_lshl_b32 s8, s30, 6
	v_bfe_u32 v75, v65, 4, 2
	v_or_b32_e32 v0, s8, v75
	s_ashr_i32 s15, s8, 31
	s_mul_i32 s15, s16, s15
	v_mul_lo_u32 v2, s17, v0
	v_mad_u64_u32 v[0:1], s[24:25], s16, v0, 0
	v_add3_u32 v1, v1, s15, v2
	v_lshlrev_b32_e32 v2, 2, v65
	v_lshl_add_u64 v[0:1], v[0:1], 2, s[12:13]
	s_ashr_i32 s15, s14, 31
	v_and_b32_e32 v64, 60, v2
	s_lshl_b32 s29, s29, 3
	v_lshl_add_u64 v[0:1], s[14:15], 2, v[0:1]
	v_mov_b32_e32 v73, 0
	v_lshlrev_b32_e32 v72, 2, v64
	s_lshl_b64 s[12:13], s[16:17], 4
	s_mov_b32 s19, 0
	v_lshl_add_u64 v[66:67], v[0:1], 0, v[72:73]
	s_mul_i32 s18, s16, 0xf0
	s_sub_u32 s12, 0, s12
	v_lshl_add_u64 v[68:69], v[66:67], 0, s[18:19]
	s_subb_u32 s13, 0, s13
	v_lshl_add_u64 v[8:9], v[68:69], 0, s[12:13]
	v_lshl_add_u64 v[10:11], v[8:9], 0, s[12:13]
	global_load_dwordx4 v[4:7], v[8:9], off nt
	global_load_dwordx4 v[0:3], v[10:11], off nt
	v_lshl_add_u64 v[8:9], v[10:11], 0, s[12:13]
	v_lshl_add_u64 v[10:11], v[8:9], 0, s[12:13]
	global_load_dwordx4 v[24:27], v[8:9], off nt
	global_load_dwordx4 v[12:15], v[10:11], off nt
	v_lshl_add_u64 v[8:9], v[10:11], 0, s[12:13]
	v_lshl_add_u64 v[10:11], v[8:9], 0, s[12:13]
	global_load_dwordx4 v[52:55], v[8:9], off nt
	global_load_dwordx4 v[36:39], v[10:11], off nt
	v_lshl_add_u64 v[8:9], v[10:11], 0, s[12:13]
	global_load_dwordx4 v[48:51], v[8:9], off nt
	v_lshl_add_u64 v[8:9], v[8:9], 0, s[12:13]
	global_load_dwordx4 v[44:47], v[8:9], off nt
	v_lshl_add_u64 v[8:9], v[8:9], 0, s[12:13]
	global_load_dwordx4 v[56:59], v[8:9], off nt
	v_lshl_add_u64 v[8:9], v[8:9], 0, s[12:13]
	global_load_dwordx4 v[32:35], v[8:9], off nt
	v_lshl_add_u64 v[8:9], v[8:9], 0, s[12:13]
	global_load_dwordx4 v[40:43], v[8:9], off nt
	v_lshl_add_u64 v[8:9], v[8:9], 0, s[12:13]
	global_load_dwordx4 v[20:23], v[8:9], off nt
	v_lshl_add_u64 v[8:9], v[8:9], 0, s[12:13]
	v_lshl_add_u64 v[70:71], v[8:9], 0, s[12:13]
	global_load_dwordx4 v[28:31], v[8:9], off nt
	s_nop 0
	global_load_dwordx4 v[8:11], v[70:71], off nt
	global_load_dwordx4 v[60:63], v[68:69], off nt
	global_load_dwordx4 v[16:19], v[66:67], off nt
	v_lshl_add_u32 v69, v75, 8, s9
	v_lshlrev_b32_e32 v70, 2, v75
	v_add3_u32 v78, v69, v70, v72
	v_bitop3_b32 v70, v64, v75, 1 bitop3:0x36
	v_lshl_add_u32 v79, v70, 2, v69
	v_bitop3_b32 v70, v64, v75, 2 bitop3:0x36
	v_lshl_add_u32 v80, v70, 2, v69
	v_bitop3_b32 v70, v64, v75, 3 bitop3:0x36
	v_lshl_add_u32 v81, v70, 2, v69
	v_or_b32_e32 v69, 4, v75
	v_lshl_add_u32 v70, v69, 8, s9
	v_bitop3_b32 v71, v75, v64, 4 bitop3:0x36
	v_lshl_add_u32 v82, v71, 2, v70
	v_bitop3_b32 v71, v64, v69, 1 bitop3:0x36
	v_lshl_add_u32 v83, v71, 2, v70
	v_bitop3_b32 v71, v64, v69, 2 bitop3:0x36
	v_bitop3_b32 v69, v64, v69, 3 bitop3:0x36
	v_lshl_add_u32 v85, v69, 2, v70
	v_or_b32_e32 v69, 8, v75
	v_lshl_add_u32 v84, v71, 2, v70
	v_lshl_add_u32 v70, v69, 8, s9
	v_bitop3_b32 v71, v75, v64, 8 bitop3:0x36
	v_lshl_add_u32 v86, v71, 2, v70
	v_bitop3_b32 v71, v64, v69, 1 bitop3:0x36
	v_lshl_add_u32 v87, v71, 2, v70
	v_bitop3_b32 v71, v64, v69, 2 bitop3:0x36
	v_bitop3_b32 v69, v64, v69, 3 bitop3:0x36
	v_lshl_add_u32 v89, v69, 2, v70
	v_or_b32_e32 v69, 12, v75
	v_lshl_add_u32 v88, v71, 2, v70
	v_lshl_add_u32 v70, v69, 8, s9
	v_bitop3_b32 v71, v75, v64, 12 bitop3:0x36
	v_lshl_add_u32 v90, v71, 2, v70
	v_bitop3_b32 v71, v64, v69, 1 bitop3:0x36
	v_lshl_add_u32 v91, v71, 2, v70
	v_bitop3_b32 v71, v64, v69, 2 bitop3:0x36
	v_bitop3_b32 v69, v64, v69, 3 bitop3:0x36
	v_lshl_add_u32 v93, v69, 2, v70
	v_or_b32_e32 v69, 16, v75
	v_lshl_add_u32 v92, v71, 2, v70
	v_lshl_add_u32 v70, v69, 8, s9
	v_bitop3_b32 v71, v75, v64, 16 bitop3:0x36
	v_lshl_add_u32 v94, v71, 2, v70
	v_bitop3_b32 v71, v64, v69, 1 bitop3:0x36
	v_lshl_add_u32 v95, v71, 2, v70
	v_bitop3_b32 v71, v64, v69, 2 bitop3:0x36
	v_bitop3_b32 v69, v64, v69, 3 bitop3:0x36
	v_lshl_add_u32 v97, v69, 2, v70
	v_or_b32_e32 v69, 20, v75
	v_lshl_add_u32 v96, v71, 2, v70
	v_lshl_add_u32 v70, v69, 8, s9
	v_bitop3_b32 v71, v75, v64, 20 bitop3:0x36
	v_lshl_add_u32 v98, v71, 2, v70
	v_bitop3_b32 v71, v64, v69, 1 bitop3:0x36
	v_lshl_add_u32 v99, v71, 2, v70
	v_bitop3_b32 v71, v64, v69, 2 bitop3:0x36
	v_bitop3_b32 v69, v64, v69, 3 bitop3:0x36
	v_lshl_add_u32 v101, v69, 2, v70
	v_or_b32_e32 v69, 24, v75
	v_lshl_add_u32 v100, v71, 2, v70
	v_lshl_add_u32 v70, v69, 8, s9
	v_bitop3_b32 v71, v75, v64, 24 bitop3:0x36
	v_lshl_add_u32 v102, v71, 2, v70
	v_bitop3_b32 v71, v64, v69, 1 bitop3:0x36
	v_lshl_add_u32 v103, v71, 2, v70
	v_bitop3_b32 v71, v64, v69, 2 bitop3:0x36
	v_bitop3_b32 v69, v64, v69, 3 bitop3:0x36
	v_lshl_add_u32 v105, v69, 2, v70
	v_or_b32_e32 v69, 28, v75
	v_lshl_add_u32 v104, v71, 2, v70
	v_lshl_add_u32 v70, v69, 8, s9
	v_bitop3_b32 v71, v75, v64, 28 bitop3:0x36
	v_lshl_add_u32 v106, v71, 2, v70
	v_bitop3_b32 v71, v64, v69, 1 bitop3:0x36
	v_lshl_add_u32 v107, v71, 2, v70
	v_bitop3_b32 v71, v64, v69, 2 bitop3:0x36
	v_bitop3_b32 v69, v64, v69, 3 bitop3:0x36
	v_lshl_add_u32 v109, v69, 2, v70
	v_or_b32_e32 v69, 36, v75
	v_or_b32_e32 v66, 1, v64
	v_lshl_add_u32 v108, v71, 2, v70
	v_lshl_add_u32 v70, v69, 8, s9
	v_bitop3_b32 v71, v69, v64, 7 bitop3:0x6c
	v_or_b32_e32 v67, 2, v64
	v_or_b32_e32 v68, 3, v64
	v_lshl_add_u32 v110, v71, 2, v70
	v_bitop3_b32 v71, v69, v66, 7 bitop3:0x6c
	v_lshl_add_u32 v111, v71, 2, v70
	v_bitop3_b32 v71, v69, v67, 7 bitop3:0x6c
	v_bitop3_b32 v69, v69, v68, 7 bitop3:0x6c
	v_lshl_add_u32 v113, v69, 2, v70
	v_or_b32_e32 v69, 40, v75
	v_lshl_add_u32 v112, v71, 2, v70
	v_lshl_add_u32 v70, v69, 8, s9
	v_bitop3_b32 v71, v69, v64, 11 bitop3:0x6c
	v_lshl_add_u32 v114, v71, 2, v70
	v_bitop3_b32 v71, v69, v66, 11 bitop3:0x6c
	v_lshl_add_u32 v115, v71, 2, v70
	v_bitop3_b32 v71, v69, v67, 11 bitop3:0x6c
	v_bitop3_b32 v69, v69, v68, 11 bitop3:0x6c
	v_lshl_add_u32 v117, v69, 2, v70
	v_or_b32_e32 v69, 44, v75
	v_lshl_add_u32 v116, v71, 2, v70
	v_lshl_add_u32 v70, v69, 8, s9
	v_bitop3_b32 v71, v69, v64, 15 bitop3:0x6c
	v_lshl_add_u32 v118, v71, 2, v70
	v_bitop3_b32 v71, v69, v66, 15 bitop3:0x6c
	v_lshl_add_u32 v119, v71, 2, v70
	v_bitop3_b32 v71, v69, v67, 15 bitop3:0x6c
	v_bitop3_b32 v69, v69, v68, 15 bitop3:0x6c
	v_lshl_add_u32 v121, v69, 2, v70
	v_or_b32_e32 v69, 48, v75
	v_lshl_add_u32 v120, v71, 2, v70
	v_lshl_add_u32 v70, v69, 8, s9
	v_bitop3_b32 v71, v69, v64, 19 bitop3:0x6c
	v_lshl_add_u32 v122, v71, 2, v70
	v_bitop3_b32 v71, v69, v66, 19 bitop3:0x6c
	v_lshl_add_u32 v123, v71, 2, v70
	v_bitop3_b32 v71, v69, v67, 19 bitop3:0x6c
	v_bitop3_b32 v69, v69, v68, 19 bitop3:0x6c
	v_lshl_add_u32 v125, v69, 2, v70
	v_or_b32_e32 v69, 52, v75
	v_lshl_add_u32 v124, v71, 2, v70
	v_lshl_add_u32 v70, v69, 8, s9
	v_bitop3_b32 v71, v69, v64, 23 bitop3:0x6c
	v_lshl_add_u32 v126, v71, 2, v70
	v_bitop3_b32 v71, v69, v66, 23 bitop3:0x6c
	v_lshl_add_u32 v127, v71, 2, v70
	v_bitop3_b32 v71, v69, v67, 23 bitop3:0x6c
	v_bitop3_b32 v69, v69, v68, 23 bitop3:0x6c
	v_lshl_add_u32 v129, v69, 2, v70
	v_or_b32_e32 v69, 56, v75
	v_lshl_add_u32 v128, v71, 2, v70
	v_lshl_add_u32 v70, v69, 8, s9
	v_bitop3_b32 v71, v69, v64, 27 bitop3:0x6c
	v_lshl_add_u32 v130, v71, 2, v70
	v_bitop3_b32 v71, v69, v66, 27 bitop3:0x6c
	v_lshl_add_u32 v131, v71, 2, v70
	v_bitop3_b32 v71, v69, v67, 27 bitop3:0x6c
	v_bitop3_b32 v69, v69, v68, 27 bitop3:0x6c
	v_lshl_add_u32 v133, v69, 2, v70
	v_or_b32_e32 v69, 60, v75
	v_lshl_add_u32 v132, v71, 2, v70
	v_lshl_add_u32 v70, v69, 8, s9
	v_bitop3_b32 v66, v69, v66, 31 bitop3:0x6c
	s_add_u32 s30, s22, 0x1a000000
	v_lshl_add_u32 v135, v66, 2, v70
	v_bitop3_b32 v66, v69, v67, 31 bitop3:0x6c
	s_addc_u32 s31, s23, 0
	v_and_b32_e32 v74, 63, v65
	v_lshl_add_u32 v136, v66, 2, v70
	v_bitop3_b32 v66, v69, v68, 31 bitop3:0x6c
	s_add_u32 s36, s22, 0x2000000
	v_lshl_add_u32 v137, v66, 2, v70
	s_addc_u32 s37, s23, 0
	v_lshlrev_b32_e32 v66, 3, v74
	s_add_u32 s38, s22, 0x1a00000
	v_and_b32_e32 v74, 56, v66
	v_bfe_u32 v138, v65, 3, 3
	v_and_b32_e32 v65, 24, v66
	s_addc_u32 s39, s23, 0
	v_lshl_add_u32 v67, v74, 8, s9
	v_lshlrev_b32_e32 v65, 2, v65
	v_lshlrev_b32_e32 v68, 2, v138
	s_add_u32 s40, s22, 0x1800000
	v_add3_u32 v146, v67, v65, v68
	v_or_b32_e32 v65, 1, v74
	v_bitop3_b32 v71, v69, v64, 31 bitop3:0x6c
	s_addc_u32 s41, s23, 0
	v_bitop3_b32 v68, v65, v138, 25 bitop3:0x6c
	v_lshl_add_u32 v69, v65, 8, s9
	s_add_u32 s45, s22, 0x1500000
	v_lshl_add_u32 v147, v68, 2, v69
	v_or_b32_e32 v68, 2, v74
	v_lshl_add_u32 v134, v71, 2, v70
	s_addc_u32 s46, s23, 0
	v_bitop3_b32 v70, v68, v138, 26 bitop3:0x6c
	v_lshl_add_u32 v71, v68, 8, s9
	s_add_u32 s47, s22, 0x1200000
	v_lshl_add_u32 v148, v70, 2, v71
	v_or_b32_e32 v70, 3, v74
	s_addc_u32 s48, s23, 0
	v_bitop3_b32 v72, v70, v138, 27 bitop3:0x6c
	v_lshl_add_u32 v76, v70, 8, s9
	s_add_u32 s49, s22, 0xe00000
	v_lshl_add_u32 v149, v72, 2, v76
	v_or_b32_e32 v72, 4, v74
	s_addc_u32 s50, s23, 0
	v_bitop3_b32 v77, v72, v138, 28 bitop3:0x6c
	v_lshl_add_u32 v205, v72, 8, s9
	s_add_u32 s51, s22, 0x200000
	v_lshl_add_u32 v150, v77, 2, v205
	v_or_b32_e32 v77, 5, v74
	v_or_b32_e32 v207, 6, v74
	v_or_b32_e32 v209, 7, v74
	s_addc_u32 s52, s23, 0
	v_or_b32_e32 v139, 8, v138
	v_or_b32_e32 v140, 16, v138
	v_or_b32_e32 v141, 24, v138
	v_or_b32_e32 v142, 32, v138
	v_or_b32_e32 v143, 40, v138
	v_or_b32_e32 v144, 48, v138
	v_or_b32_e32 v145, 56, v138
	v_lshl_add_u32 v206, v77, 8, s9
	v_lshl_add_u32 v208, v207, 8, s9
	v_lshl_add_u32 v210, v209, 8, s9
	s_lshr_b32 s9, s28, 8
	v_bitop3_b32 v155, v65, v139, 25 bitop3:0x6c
	v_bitop3_b32 v163, v65, v140, 25 bitop3:0x6c
	v_bitop3_b32 v171, v65, v141, 25 bitop3:0x6c
	v_bitop3_b32 v178, v65, v142, 25 bitop3:0x6c
	v_bitop3_b32 v186, v65, v143, 25 bitop3:0x6c
	v_bitop3_b32 v194, v65, v144, 25 bitop3:0x6c
	v_bitop3_b32 v65, v65, v145, 25 bitop3:0x6c
	s_lshl_b32 s53, s20, 3
	s_lshl_b32 s12, s9, 12
	v_lshl_add_u32 v202, v65, 2, v69
	v_bitop3_b32 v65, v68, v145, 26 bitop3:0x6c
	s_add_i32 s13, s21, s12
	s_add_i32 s12, s12, s53
	v_lshl_add_u32 v203, v65, 2, v71
	v_bitop3_b32 v65, v70, v145, 27 bitop3:0x6c
	s_mul_i32 s14, s44, 48
	s_add_i32 s12, s12, s21
	v_bitop3_b32 v158, v72, v139, 28 bitop3:0x6c
	v_bitop3_b32 v166, v72, v140, 28 bitop3:0x6c
	v_bitop3_b32 v174, v72, v141, 28 bitop3:0x6c
	v_bitop3_b32 v181, v72, v142, 28 bitop3:0x6c
	v_bitop3_b32 v189, v72, v143, 28 bitop3:0x6c
	v_bitop3_b32 v197, v72, v144, 28 bitop3:0x6c
	v_lshl_add_u32 v204, v65, 2, v76
	v_bitop3_b32 v65, v72, v145, 28 bitop3:0x6c
	s_sub_i32 s12, s12, s14
	v_bitop3_b32 v151, v77, v138, 29 bitop3:0x6c
	v_lshl_add_u32 v158, v158, 2, v205
	v_bitop3_b32 v159, v77, v139, 29 bitop3:0x6c
	v_lshl_add_u32 v166, v166, 2, v205
	v_bitop3_b32 v167, v77, v140, 29 bitop3:0x6c
	v_lshl_add_u32 v174, v174, 2, v205
	v_bitop3_b32 v175, v77, v141, 29 bitop3:0x6c
	v_lshl_add_u32 v181, v181, 2, v205
	v_bitop3_b32 v182, v77, v142, 29 bitop3:0x6c
	v_lshl_add_u32 v189, v189, 2, v205
	v_bitop3_b32 v190, v77, v143, 29 bitop3:0x6c
	v_lshl_add_u32 v197, v197, 2, v205
	v_bitop3_b32 v198, v77, v144, 29 bitop3:0x6c
	v_lshl_add_u32 v205, v65, 2, v205
	v_bitop3_b32 v65, v77, v145, 29 bitop3:0x6c
	s_sub_i32 s28, s13, s14
	s_add_i32 s54, s12, 0x5800
	s_lshl_b32 s12, s9, 11
	s_add_i32 s13, s13, s53
	v_lshl_add_u32 v151, v151, 2, v206
	v_lshl_add_u32 v159, v159, 2, v206
	v_lshl_add_u32 v167, v167, 2, v206
	v_lshl_add_u32 v175, v175, 2, v206
	v_lshl_add_u32 v182, v182, 2, v206
	v_lshl_add_u32 v190, v190, 2, v206
	v_lshl_add_u32 v198, v198, 2, v206
	v_lshl_add_u32 v206, v65, 2, v206
	v_bitop3_b32 v65, v207, v145, 30 bitop3:0x6c
	s_mul_i32 s15, s44, 24
	s_sub_i32 s13, s13, s14
	s_lshl_b32 s9, s9, 17
	s_mulk_i32 s44, 0x600
	s_add_i32 s21, s21, s12
	v_bitop3_b32 v152, v207, v138, 30 bitop3:0x6c
	v_bitop3_b32 v153, v209, v138, 31 bitop3:0x6c
	v_bitop3_b32 v154, v66, v139, 24 bitop3:0x6c
	v_bitop3_b32 v156, v68, v139, 26 bitop3:0x6c
	v_bitop3_b32 v157, v70, v139, 27 bitop3:0x6c
	v_bitop3_b32 v160, v207, v139, 30 bitop3:0x6c
	v_bitop3_b32 v161, v209, v139, 31 bitop3:0x6c
	v_bitop3_b32 v162, v66, v140, 24 bitop3:0x6c
	v_bitop3_b32 v164, v68, v140, 26 bitop3:0x6c
	v_bitop3_b32 v165, v70, v140, 27 bitop3:0x6c
	v_bitop3_b32 v168, v207, v140, 30 bitop3:0x6c
	v_bitop3_b32 v169, v209, v140, 31 bitop3:0x6c
	v_bitop3_b32 v170, v66, v138, 24 bitop3:0x4e
	v_bitop3_b32 v172, v68, v141, 26 bitop3:0x6c
	v_bitop3_b32 v173, v70, v141, 27 bitop3:0x6c
	v_bitop3_b32 v176, v207, v141, 30 bitop3:0x6c
	v_bitop3_b32 v177, v209, v141, 31 bitop3:0x6c
	v_bitop3_b32 v179, v68, v142, 26 bitop3:0x6c
	v_bitop3_b32 v180, v70, v142, 27 bitop3:0x6c
	v_bitop3_b32 v183, v207, v142, 30 bitop3:0x6c
	v_bitop3_b32 v184, v209, v142, 31 bitop3:0x6c
	v_bitop3_b32 v185, v66, v143, 24 bitop3:0x6c
	v_bitop3_b32 v187, v68, v143, 26 bitop3:0x6c
	v_bitop3_b32 v188, v70, v143, 27 bitop3:0x6c
	v_bitop3_b32 v191, v207, v143, 30 bitop3:0x6c
	v_bitop3_b32 v192, v209, v143, 31 bitop3:0x6c
	v_bitop3_b32 v193, v66, v144, 24 bitop3:0x6c
	v_bitop3_b32 v195, v68, v144, 26 bitop3:0x6c
	v_bitop3_b32 v196, v70, v144, 27 bitop3:0x6c
	v_bitop3_b32 v199, v207, v144, 30 bitop3:0x6c
	v_bitop3_b32 v200, v209, v144, 31 bitop3:0x6c
	v_bitop3_b32 v66, v66, v145, 24 bitop3:0x6c
	v_lshl_add_u32 v207, v65, 2, v208
	v_bitop3_b32 v65, v209, v145, 31 bitop3:0x6c
	s_lshl_b32 s13, s13, 6
	s_sub_i32 s44, s9, s44
	s_sub_i32 s9, s21, s15
	v_lshl_add_u32 v152, v152, 2, v208
	v_lshl_add_u32 v153, v153, 2, v210
	v_lshl_add_u32 v154, v154, 2, v67
	v_lshl_add_u32 v155, v155, 2, v69
	v_lshl_add_u32 v156, v156, 2, v71
	v_lshl_add_u32 v157, v157, 2, v76
	v_lshl_add_u32 v160, v160, 2, v208
	v_lshl_add_u32 v161, v161, 2, v210
	v_lshl_add_u32 v162, v162, 2, v67
	v_lshl_add_u32 v163, v163, 2, v69
	v_lshl_add_u32 v164, v164, 2, v71
	v_lshl_add_u32 v165, v165, 2, v76
	v_lshl_add_u32 v168, v168, 2, v208
	v_lshl_add_u32 v169, v169, 2, v210
	v_lshl_add_u32 v170, v170, 2, v67
	v_lshl_add_u32 v171, v171, 2, v69
	v_lshl_add_u32 v172, v172, 2, v71
	v_lshl_add_u32 v173, v173, 2, v76
	v_lshl_add_u32 v176, v176, 2, v208
	v_lshl_add_u32 v177, v177, 2, v210
	v_lshl_add_u32 v178, v178, 2, v69
	v_lshl_add_u32 v179, v179, 2, v71
	v_lshl_add_u32 v180, v180, 2, v76
	v_lshl_add_u32 v183, v183, 2, v208
	v_lshl_add_u32 v184, v184, 2, v210
	v_lshl_add_u32 v185, v185, 2, v67
	v_lshl_add_u32 v186, v186, 2, v69
	v_lshl_add_u32 v187, v187, 2, v71
	v_lshl_add_u32 v188, v188, 2, v76
	v_lshl_add_u32 v191, v191, 2, v208
	v_lshl_add_u32 v192, v192, 2, v210
	v_lshl_add_u32 v193, v193, 2, v67
	v_lshl_add_u32 v194, v194, 2, v69
	v_lshl_add_u32 v195, v195, 2, v71
	v_lshl_add_u32 v196, v196, 2, v76
	v_lshl_add_u32 v199, v199, 2, v208
	v_lshl_add_u32 v200, v200, 2, v210
	v_lshl_add_u32 v201, v66, 2, v67
	v_lshl_add_u32 v208, v65, 2, v210
	s_sub_i32 s55, s12, s15
	s_add_i32 s56, s13, 0xfffe0000
	s_add_i32 s57, s9, 0xfffff800
	v_lshlrev_b32_e32 v76, 2, v64
	v_lshlrev_b32_e32 v72, 1, v74
	s_branch .LBB0_939

.LBB0_935:
	s_lshl_b32 s18, s21, 6
	v_or_b32_e32 v0, s18, v75
	s_ashr_i32 s9, s18, 31
	s_mul_i32 s9, s22, s9
	v_mul_lo_u32 v2, s23, v0
	v_mad_u64_u32 v[0:1], s[60:61], s22, v0, 0
	v_add3_u32 v1, v1, s9, v2
	v_lshl_add_u64 v[0:1], v[0:1], 2, s[16:17]
	s_ashr_i32 s21, s20, 31
	v_lshl_add_u64 v[0:1], s[20:21], 2, v[0:1]
	v_mov_b32_e32 v77, v73
	v_lshl_add_u64 v[0:1], v[0:1], 0, v[76:77]
	s_lshl_b64 s[16:17], s[22:23], 4
	v_lshl_add_u64 v[2:3], v[0:1], 0, s[16:17]
	global_load_dwordx4 v[16:19], v[0:1], off nt
	global_load_dwordx4 v[8:11], v[2:3], off nt
	v_lshl_add_u64 v[0:1], v[2:3], 0, s[16:17]
	v_lshl_add_u64 v[2:3], v[0:1], 0, s[16:17]
	global_load_dwordx4 v[28:31], v[0:1], off nt
	global_load_dwordx4 v[20:23], v[2:3], off nt
	v_lshl_add_u64 v[0:1], v[2:3], 0, s[16:17]
	v_lshl_add_u64 v[2:3], v[0:1], 0, s[16:17]
	global_load_dwordx4 v[40:43], v[0:1], off nt
	global_load_dwordx4 v[32:35], v[2:3], off nt
	v_lshl_add_u64 v[0:1], v[2:3], 0, s[16:17]
	v_lshl_add_u64 v[2:3], v[0:1], 0, s[16:17]
	global_load_dwordx4 v[56:59], v[0:1], off nt
	global_load_dwordx4 v[44:47], v[2:3], off nt
	v_lshl_add_u64 v[0:1], v[2:3], 0, s[16:17]
	global_load_dwordx4 v[48:51], v[0:1], off nt
	v_lshl_add_u64 v[0:1], v[0:1], 0, s[16:17]
	global_load_dwordx4 v[36:39], v[0:1], off nt
	v_lshl_add_u64 v[0:1], v[0:1], 0, s[16:17]
	global_load_dwordx4 v[52:55], v[0:1], off nt
	v_lshl_add_u64 v[0:1], v[0:1], 0, s[16:17]
	global_load_dwordx4 v[12:15], v[0:1], off nt
	v_lshl_add_u64 v[0:1], v[0:1], 0, s[16:17]
	v_lshl_add_u64 v[4:5], v[0:1], 0, s[16:17]
	v_lshl_add_u64 v[60:61], v[4:5], 0, s[16:17]
	global_load_dwordx4 v[24:27], v[0:1], off nt
	s_nop 0
	global_load_dwordx4 v[0:3], v[4:5], off nt
	s_nop 0
	global_load_dwordx4 v[4:7], v[60:61], off nt
	v_lshl_add_u64 v[60:61], v[60:61], 0, s[16:17]
	global_load_dwordx4 v[60:63], v[60:61], off nt

.LBB0_1290:
	s_lshl_b32 s8, s20, 14
	s_add_i32 s9, s8, 0
	s_lshl_b32 s8, s25, 6
	v_bfe_u32 v75, v65, 4, 2
	v_or_b32_e32 v0, s8, v75
	s_ashr_i32 s15, s8, 31
	s_mul_i32 s15, s16, s15
	v_mul_lo_u32 v2, s17, v0
	v_mad_u64_u32 v[0:1], s[30:31], s16, v0, 0
	v_add3_u32 v1, v1, s15, v2
	v_lshlrev_b32_e32 v2, 2, v65
	v_lshl_add_u64 v[0:1], v[0:1], 2, s[12:13]
	s_ashr_i32 s15, s14, 31
	v_and_b32_e32 v64, 60, v2
	v_lshl_add_u64 v[0:1], s[14:15], 2, v[0:1]
	v_mov_b32_e32 v73, 0
	v_lshlrev_b32_e32 v72, 2, v64
	s_lshl_b64 s[12:13], s[16:17], 4
	s_mov_b32 s19, 0
	v_lshl_add_u64 v[66:67], v[0:1], 0, v[72:73]
	s_mul_i32 s18, s16, 0xf0
	s_sub_u32 s12, 0, s12
	v_lshl_add_u64 v[68:69], v[66:67], 0, s[18:19]
	s_subb_u32 s13, 0, s13
	v_lshl_add_u64 v[8:9], v[68:69], 0, s[12:13]
	v_lshl_add_u64 v[10:11], v[8:9], 0, s[12:13]
	global_load_dwordx4 v[4:7], v[8:9], off nt
	global_load_dwordx4 v[0:3], v[10:11], off nt
	v_lshl_add_u64 v[8:9], v[10:11], 0, s[12:13]
	v_lshl_add_u64 v[10:11], v[8:9], 0, s[12:13]
	global_load_dwordx4 v[24:27], v[8:9], off nt
	global_load_dwordx4 v[12:15], v[10:11], off nt
	v_lshl_add_u64 v[8:9], v[10:11], 0, s[12:13]
	v_lshl_add_u64 v[10:11], v[8:9], 0, s[12:13]
	global_load_dwordx4 v[52:55], v[8:9], off nt
	global_load_dwordx4 v[36:39], v[10:11], off nt
	v_lshl_add_u64 v[8:9], v[10:11], 0, s[12:13]
	global_load_dwordx4 v[48:51], v[8:9], off nt
	v_lshl_add_u64 v[8:9], v[8:9], 0, s[12:13]
	global_load_dwordx4 v[44:47], v[8:9], off nt
	v_lshl_add_u64 v[8:9], v[8:9], 0, s[12:13]
	global_load_dwordx4 v[56:59], v[8:9], off nt
	v_lshl_add_u64 v[8:9], v[8:9], 0, s[12:13]
	global_load_dwordx4 v[32:35], v[8:9], off nt
	v_lshl_add_u64 v[8:9], v[8:9], 0, s[12:13]
	global_load_dwordx4 v[40:43], v[8:9], off nt
	v_lshl_add_u64 v[8:9], v[8:9], 0, s[12:13]
	global_load_dwordx4 v[20:23], v[8:9], off nt
	v_lshl_add_u64 v[8:9], v[8:9], 0, s[12:13]
	v_lshl_add_u64 v[70:71], v[8:9], 0, s[12:13]
	global_load_dwordx4 v[28:31], v[8:9], off nt
	s_nop 0
	global_load_dwordx4 v[8:11], v[70:71], off nt
	global_load_dwordx4 v[60:63], v[68:69], off nt
	global_load_dwordx4 v[16:19], v[66:67], off nt
	v_lshl_add_u32 v69, v75, 8, s9
	v_lshlrev_b32_e32 v70, 2, v75
	v_add3_u32 v78, v69, v70, v72
	v_bitop3_b32 v70, v64, v75, 1 bitop3:0x36
	v_lshl_add_u32 v79, v70, 2, v69
	v_bitop3_b32 v70, v64, v75, 2 bitop3:0x36
	v_lshl_add_u32 v80, v70, 2, v69
	v_bitop3_b32 v70, v64, v75, 3 bitop3:0x36
	v_lshl_add_u32 v81, v70, 2, v69
	v_or_b32_e32 v69, 4, v75
	v_lshl_add_u32 v70, v69, 8, s9
	v_bitop3_b32 v71, v75, v64, 4 bitop3:0x36
	v_lshl_add_u32 v82, v71, 2, v70
	v_bitop3_b32 v71, v64, v69, 1 bitop3:0x36
	v_lshl_add_u32 v83, v71, 2, v70
	v_bitop3_b32 v71, v64, v69, 2 bitop3:0x36
	v_bitop3_b32 v69, v64, v69, 3 bitop3:0x36
	v_lshl_add_u32 v85, v69, 2, v70
	v_or_b32_e32 v69, 8, v75
	v_lshl_add_u32 v84, v71, 2, v70
	v_lshl_add_u32 v70, v69, 8, s9
	v_bitop3_b32 v71, v75, v64, 8 bitop3:0x36
	v_lshl_add_u32 v86, v71, 2, v70
	v_bitop3_b32 v71, v64, v69, 1 bitop3:0x36
	v_lshl_add_u32 v87, v71, 2, v70
	v_bitop3_b32 v71, v64, v69, 2 bitop3:0x36
	v_bitop3_b32 v69, v64, v69, 3 bitop3:0x36
	v_lshl_add_u32 v89, v69, 2, v70
	v_or_b32_e32 v69, 12, v75
	v_lshl_add_u32 v88, v71, 2, v70
	v_lshl_add_u32 v70, v69, 8, s9
	v_bitop3_b32 v71, v75, v64, 12 bitop3:0x36
	v_lshl_add_u32 v90, v71, 2, v70
	v_bitop3_b32 v71, v64, v69, 1 bitop3:0x36
	v_lshl_add_u32 v91, v71, 2, v70
	v_bitop3_b32 v71, v64, v69, 2 bitop3:0x36
	v_bitop3_b32 v69, v64, v69, 3 bitop3:0x36
	v_lshl_add_u32 v93, v69, 2, v70
	v_or_b32_e32 v69, 16, v75
	v_lshl_add_u32 v92, v71, 2, v70
	v_lshl_add_u32 v70, v69, 8, s9
	v_bitop3_b32 v71, v75, v64, 16 bitop3:0x36
	v_lshl_add_u32 v94, v71, 2, v70
	v_bitop3_b32 v71, v64, v69, 1 bitop3:0x36
	v_lshl_add_u32 v95, v71, 2, v70
	v_bitop3_b32 v71, v64, v69, 2 bitop3:0x36
	v_bitop3_b32 v69, v64, v69, 3 bitop3:0x36
	v_lshl_add_u32 v97, v69, 2, v70
	v_or_b32_e32 v69, 20, v75
	v_lshl_add_u32 v96, v71, 2, v70
	v_lshl_add_u32 v70, v69, 8, s9
	v_bitop3_b32 v71, v75, v64, 20 bitop3:0x36
	v_lshl_add_u32 v98, v71, 2, v70
	v_bitop3_b32 v71, v64, v69, 1 bitop3:0x36
	v_lshl_add_u32 v99, v71, 2, v70
	v_bitop3_b32 v71, v64, v69, 2 bitop3:0x36
	v_bitop3_b32 v69, v64, v69, 3 bitop3:0x36
	v_lshl_add_u32 v101, v69, 2, v70
	v_or_b32_e32 v69, 24, v75
	v_lshl_add_u32 v100, v71, 2, v70
	v_lshl_add_u32 v70, v69, 8, s9
	v_bitop3_b32 v71, v75, v64, 24 bitop3:0x36
	v_lshl_add_u32 v102, v71, 2, v70
	v_bitop3_b32 v71, v64, v69, 1 bitop3:0x36
	v_lshl_add_u32 v103, v71, 2, v70
	v_bitop3_b32 v71, v64, v69, 2 bitop3:0x36
	v_bitop3_b32 v69, v64, v69, 3 bitop3:0x36
	v_lshl_add_u32 v105, v69, 2, v70
	v_or_b32_e32 v69, 28, v75
	v_lshl_add_u32 v104, v71, 2, v70
	v_lshl_add_u32 v70, v69, 8, s9
	v_bitop3_b32 v71, v75, v64, 28 bitop3:0x36
	v_lshl_add_u32 v106, v71, 2, v70
	v_bitop3_b32 v71, v64, v69, 1 bitop3:0x36
	v_lshl_add_u32 v107, v71, 2, v70
	v_bitop3_b32 v71, v64, v69, 2 bitop3:0x36
	v_bitop3_b32 v69, v64, v69, 3 bitop3:0x36
	v_lshl_add_u32 v109, v69, 2, v70
	v_or_b32_e32 v69, 36, v75
	v_or_b32_e32 v66, 1, v64
	v_lshl_add_u32 v108, v71, 2, v70
	v_lshl_add_u32 v70, v69, 8, s9
	v_bitop3_b32 v71, v69, v64, 7 bitop3:0x6c
	v_or_b32_e32 v67, 2, v64
	v_or_b32_e32 v68, 3, v64
	v_lshl_add_u32 v110, v71, 2, v70
	v_bitop3_b32 v71, v69, v66, 7 bitop3:0x6c
	v_lshl_add_u32 v111, v71, 2, v70
	v_bitop3_b32 v71, v69, v67, 7 bitop3:0x6c
	v_bitop3_b32 v69, v69, v68, 7 bitop3:0x6c
	v_lshl_add_u32 v113, v69, 2, v70
	v_or_b32_e32 v69, 40, v75
	v_lshl_add_u32 v112, v71, 2, v70
	v_lshl_add_u32 v70, v69, 8, s9
	v_bitop3_b32 v71, v69, v64, 11 bitop3:0x6c
	v_lshl_add_u32 v114, v71, 2, v70
	v_bitop3_b32 v71, v69, v66, 11 bitop3:0x6c
	v_lshl_add_u32 v115, v71, 2, v70
	v_bitop3_b32 v71, v69, v67, 11 bitop3:0x6c
	v_bitop3_b32 v69, v69, v68, 11 bitop3:0x6c
	v_lshl_add_u32 v117, v69, 2, v70
	v_or_b32_e32 v69, 44, v75
	v_lshl_add_u32 v116, v71, 2, v70
	v_lshl_add_u32 v70, v69, 8, s9
	v_bitop3_b32 v71, v69, v64, 15 bitop3:0x6c
	v_lshl_add_u32 v118, v71, 2, v70
	v_bitop3_b32 v71, v69, v66, 15 bitop3:0x6c
	v_lshl_add_u32 v119, v71, 2, v70
	v_bitop3_b32 v71, v69, v67, 15 bitop3:0x6c
	v_bitop3_b32 v69, v69, v68, 15 bitop3:0x6c
	v_lshl_add_u32 v121, v69, 2, v70
	v_or_b32_e32 v69, 48, v75
	v_lshl_add_u32 v120, v71, 2, v70
	v_lshl_add_u32 v70, v69, 8, s9
	v_bitop3_b32 v71, v69, v64, 19 bitop3:0x6c
	v_lshl_add_u32 v122, v71, 2, v70
	v_bitop3_b32 v71, v69, v66, 19 bitop3:0x6c
	v_lshl_add_u32 v123, v71, 2, v70
	v_bitop3_b32 v71, v69, v67, 19 bitop3:0x6c
	v_bitop3_b32 v69, v69, v68, 19 bitop3:0x6c
	v_lshl_add_u32 v125, v69, 2, v70
	v_or_b32_e32 v69, 52, v75
	v_lshl_add_u32 v124, v71, 2, v70
	v_lshl_add_u32 v70, v69, 8, s9
	v_bitop3_b32 v71, v69, v64, 23 bitop3:0x6c
	v_lshl_add_u32 v126, v71, 2, v70
	v_bitop3_b32 v71, v69, v66, 23 bitop3:0x6c
	v_lshl_add_u32 v127, v71, 2, v70
	v_bitop3_b32 v71, v69, v67, 23 bitop3:0x6c
	v_bitop3_b32 v69, v69, v68, 23 bitop3:0x6c
	v_lshl_add_u32 v129, v69, 2, v70
	v_or_b32_e32 v69, 56, v75
	v_lshl_add_u32 v128, v71, 2, v70
	v_lshl_add_u32 v70, v69, 8, s9
	v_bitop3_b32 v71, v69, v64, 27 bitop3:0x6c
	v_lshl_add_u32 v130, v71, 2, v70
	v_bitop3_b32 v71, v69, v66, 27 bitop3:0x6c
	v_lshl_add_u32 v131, v71, 2, v70
	v_bitop3_b32 v71, v69, v67, 27 bitop3:0x6c
	v_bitop3_b32 v69, v69, v68, 27 bitop3:0x6c
	v_lshl_add_u32 v133, v69, 2, v70
	v_or_b32_e32 v69, 60, v75
	v_lshl_add_u32 v132, v71, 2, v70
	v_lshl_add_u32 v70, v69, 8, s9
	v_bitop3_b32 v66, v69, v66, 31 bitop3:0x6c
	v_lshl_add_u32 v135, v66, 2, v70
	v_bitop3_b32 v66, v69, v67, 31 bitop3:0x6c
	v_and_b32_e32 v74, 63, v65
	v_lshl_add_u32 v136, v66, 2, v70
	v_bitop3_b32 v66, v69, v68, 31 bitop3:0x6c
	s_add_u32 s29, s23, 0x1a000000
	v_lshl_add_u32 v137, v66, 2, v70
	s_addc_u32 s30, s24, 0
	v_lshlrev_b32_e32 v66, 3, v74
	s_add_u32 s31, s23, 0x2000000
	v_and_b32_e32 v74, 56, v66
	v_bfe_u32 v138, v65, 3, 3
	v_and_b32_e32 v65, 24, v66
	s_addc_u32 s36, s24, 0
	v_lshl_add_u32 v67, v74, 8, s9
	v_lshlrev_b32_e32 v65, 2, v65
	v_lshlrev_b32_e32 v68, 2, v138
	s_add_u32 s37, s23, 0x1a00000
	v_add3_u32 v146, v67, v65, v68
	v_or_b32_e32 v65, 1, v74
	v_bitop3_b32 v71, v69, v64, 31 bitop3:0x6c
	s_addc_u32 s38, s24, 0
	v_bitop3_b32 v68, v65, v138, 25 bitop3:0x6c
	v_lshl_add_u32 v69, v65, 8, s9
	s_add_u32 s39, s23, 0x1800000
	v_lshl_add_u32 v147, v68, 2, v69
	v_or_b32_e32 v68, 2, v74
	v_lshl_add_u32 v134, v71, 2, v70
	s_addc_u32 s42, s24, 0
	v_bitop3_b32 v70, v68, v138, 26 bitop3:0x6c
	v_lshl_add_u32 v71, v68, 8, s9
	s_add_u32 s43, s23, 0x1500000
	v_or_b32_e32 v139, 8, v138
	v_or_b32_e32 v140, 16, v138
	v_or_b32_e32 v141, 24, v138
	v_or_b32_e32 v142, 32, v138
	v_or_b32_e32 v143, 40, v138
	v_or_b32_e32 v144, 48, v138
	v_or_b32_e32 v145, 56, v138
	v_lshl_add_u32 v148, v70, 2, v71
	v_or_b32_e32 v70, 3, v74
	s_addc_u32 s44, s24, 0
	v_bitop3_b32 v72, v70, v138, 27 bitop3:0x6c
	v_lshl_add_u32 v76, v70, 8, s9
	v_bitop3_b32 v155, v65, v139, 25 bitop3:0x6c
	v_bitop3_b32 v163, v65, v140, 25 bitop3:0x6c
	v_bitop3_b32 v171, v65, v141, 25 bitop3:0x6c
	v_bitop3_b32 v178, v65, v142, 25 bitop3:0x6c
	v_bitop3_b32 v186, v65, v143, 25 bitop3:0x6c
	v_bitop3_b32 v194, v65, v144, 25 bitop3:0x6c
	v_bitop3_b32 v65, v65, v145, 25 bitop3:0x6c
	s_add_u32 s45, s23, 0x1200000
	v_lshl_add_u32 v149, v72, 2, v76
	v_or_b32_e32 v72, 4, v74
	v_lshl_add_u32 v202, v65, 2, v69
	v_bitop3_b32 v65, v68, v145, 26 bitop3:0x6c
	s_addc_u32 s46, s24, 0
	v_bitop3_b32 v77, v72, v138, 28 bitop3:0x6c
	v_lshl_add_u32 v205, v72, 8, s9
	v_lshl_add_u32 v203, v65, 2, v71
	v_bitop3_b32 v65, v70, v145, 27 bitop3:0x6c
	s_add_u32 s47, s23, 0xe00000
	v_lshl_add_u32 v150, v77, 2, v205
	v_or_b32_e32 v77, 5, v74
	v_bitop3_b32 v158, v72, v139, 28 bitop3:0x6c
	v_bitop3_b32 v166, v72, v140, 28 bitop3:0x6c
	v_bitop3_b32 v174, v72, v141, 28 bitop3:0x6c
	v_bitop3_b32 v181, v72, v142, 28 bitop3:0x6c
	v_bitop3_b32 v189, v72, v143, 28 bitop3:0x6c
	v_bitop3_b32 v197, v72, v144, 28 bitop3:0x6c
	v_lshl_add_u32 v204, v65, 2, v76
	v_bitop3_b32 v65, v72, v145, 28 bitop3:0x6c
	s_addc_u32 s48, s24, 0
	v_bitop3_b32 v151, v77, v138, 29 bitop3:0x6c
	v_lshl_add_u32 v206, v77, 8, s9
	v_or_b32_e32 v207, 6, v74
	v_lshl_add_u32 v158, v158, 2, v205
	v_bitop3_b32 v159, v77, v139, 29 bitop3:0x6c
	v_lshl_add_u32 v166, v166, 2, v205
	v_bitop3_b32 v167, v77, v140, 29 bitop3:0x6c
	v_lshl_add_u32 v174, v174, 2, v205
	v_bitop3_b32 v175, v77, v141, 29 bitop3:0x6c
	v_lshl_add_u32 v181, v181, 2, v205
	v_bitop3_b32 v182, v77, v142, 29 bitop3:0x6c
	v_lshl_add_u32 v189, v189, 2, v205
	v_bitop3_b32 v190, v77, v143, 29 bitop3:0x6c
	v_lshl_add_u32 v197, v197, 2, v205
	v_bitop3_b32 v198, v77, v144, 29 bitop3:0x6c
	v_lshl_add_u32 v205, v65, 2, v205
	v_bitop3_b32 v65, v77, v145, 29 bitop3:0x6c
	s_add_u32 s49, s23, 0x200000
	v_lshl_add_u32 v151, v151, 2, v206
	v_lshl_add_u32 v208, v207, 8, s9
	v_or_b32_e32 v209, 7, v74
	v_lshl_add_u32 v159, v159, 2, v206
	v_lshl_add_u32 v167, v167, 2, v206
	v_lshl_add_u32 v175, v175, 2, v206
	v_lshl_add_u32 v182, v182, 2, v206
	v_lshl_add_u32 v190, v190, 2, v206
	v_lshl_add_u32 v198, v198, 2, v206
	v_lshl_add_u32 v206, v65, 2, v206
	v_bitop3_b32 v65, v207, v145, 30 bitop3:0x6c
	s_addc_u32 s50, s24, 0
	v_bitop3_b32 v152, v207, v138, 30 bitop3:0x6c
	v_bitop3_b32 v153, v209, v138, 31 bitop3:0x6c
	v_lshl_add_u32 v210, v209, 8, s9
	v_bitop3_b32 v154, v66, v139, 24 bitop3:0x6c
	v_bitop3_b32 v156, v68, v139, 26 bitop3:0x6c
	v_bitop3_b32 v157, v70, v139, 27 bitop3:0x6c
	v_bitop3_b32 v160, v207, v139, 30 bitop3:0x6c
	v_bitop3_b32 v161, v209, v139, 31 bitop3:0x6c
	v_bitop3_b32 v162, v66, v140, 24 bitop3:0x6c
	v_bitop3_b32 v164, v68, v140, 26 bitop3:0x6c
	v_bitop3_b32 v165, v70, v140, 27 bitop3:0x6c
	v_bitop3_b32 v168, v207, v140, 30 bitop3:0x6c
	v_bitop3_b32 v169, v209, v140, 31 bitop3:0x6c
	v_bitop3_b32 v170, v66, v138, 24 bitop3:0x4e
	v_bitop3_b32 v172, v68, v141, 26 bitop3:0x6c
	v_bitop3_b32 v173, v70, v141, 27 bitop3:0x6c
	v_bitop3_b32 v176, v207, v141, 30 bitop3:0x6c
	v_bitop3_b32 v177, v209, v141, 31 bitop3:0x6c
	v_bitop3_b32 v179, v68, v142, 26 bitop3:0x6c
	v_bitop3_b32 v180, v70, v142, 27 bitop3:0x6c
	v_bitop3_b32 v183, v207, v142, 30 bitop3:0x6c
	v_bitop3_b32 v184, v209, v142, 31 bitop3:0x6c
	v_bitop3_b32 v185, v66, v143, 24 bitop3:0x6c
	v_bitop3_b32 v187, v68, v143, 26 bitop3:0x6c
	v_bitop3_b32 v188, v70, v143, 27 bitop3:0x6c
	v_bitop3_b32 v191, v207, v143, 30 bitop3:0x6c
	v_bitop3_b32 v192, v209, v143, 31 bitop3:0x6c
	v_bitop3_b32 v193, v66, v144, 24 bitop3:0x6c
	v_bitop3_b32 v195, v68, v144, 26 bitop3:0x6c
	v_bitop3_b32 v196, v70, v144, 27 bitop3:0x6c
	v_bitop3_b32 v199, v207, v144, 30 bitop3:0x6c
	v_bitop3_b32 v200, v209, v144, 31 bitop3:0x6c
	v_bitop3_b32 v66, v66, v145, 24 bitop3:0x6c
	v_lshl_add_u32 v207, v65, 2, v208
	v_bitop3_b32 v65, v209, v145, 31 bitop3:0x6c
	s_add_i32 s9, s21, s20
	v_lshl_add_u32 v152, v152, 2, v208
	v_lshl_add_u32 v153, v153, 2, v210
	v_lshl_add_u32 v154, v154, 2, v67
	v_lshl_add_u32 v155, v155, 2, v69
	v_lshl_add_u32 v156, v156, 2, v71
	v_lshl_add_u32 v157, v157, 2, v76
	v_lshl_add_u32 v160, v160, 2, v208
	v_lshl_add_u32 v161, v161, 2, v210
	v_lshl_add_u32 v162, v162, 2, v67
	v_lshl_add_u32 v163, v163, 2, v69
	v_lshl_add_u32 v164, v164, 2, v71
	v_lshl_add_u32 v165, v165, 2, v76
	v_lshl_add_u32 v168, v168, 2, v208
	v_lshl_add_u32 v169, v169, 2, v210
	v_lshl_add_u32 v170, v170, 2, v67
	v_lshl_add_u32 v171, v171, 2, v69
	v_lshl_add_u32 v172, v172, 2, v71
	v_lshl_add_u32 v173, v173, 2, v76
	v_lshl_add_u32 v176, v176, 2, v208
	v_lshl_add_u32 v177, v177, 2, v210
	v_lshl_add_u32 v178, v178, 2, v69
	v_lshl_add_u32 v179, v179, 2, v71
	v_lshl_add_u32 v180, v180, 2, v76
	v_lshl_add_u32 v183, v183, 2, v208
	v_lshl_add_u32 v184, v184, 2, v210
	v_lshl_add_u32 v185, v185, 2, v67
	v_lshl_add_u32 v186, v186, 2, v69
	v_lshl_add_u32 v187, v187, 2, v71
	v_lshl_add_u32 v188, v188, 2, v76
	v_lshl_add_u32 v191, v191, 2, v208
	v_lshl_add_u32 v192, v192, 2, v210
	v_lshl_add_u32 v193, v193, 2, v67
	v_lshl_add_u32 v194, v194, 2, v69
	v_lshl_add_u32 v195, v195, 2, v71
	v_lshl_add_u32 v196, v196, 2, v76
	v_lshl_add_u32 v199, v199, 2, v208
	v_lshl_add_u32 v200, v200, 2, v210
	v_lshl_add_u32 v201, v66, 2, v67
	v_lshl_add_u32 v208, v65, 2, v210
	s_add_i32 s51, s9, 0x7c00
	s_lshl_b32 s52, s22, 6
	v_lshlrev_b32_e32 v76, 2, v64
	v_lshlrev_b32_e32 v72, 1, v74
	s_branch .LBB0_1296

.LBB0_1292:
	s_lshl_b32 s18, s21, 6
	v_or_b32_e32 v0, s18, v75
	s_ashr_i32 s9, s18, 31
	s_mul_i32 s9, s22, s9
	v_mul_lo_u32 v2, s23, v0
	v_mad_u64_u32 v[0:1], s[56:57], s22, v0, 0
	v_add3_u32 v1, v1, s9, v2
	v_lshl_add_u64 v[0:1], v[0:1], 2, s[16:17]
	s_ashr_i32 s21, s20, 31
	v_lshl_add_u64 v[0:1], s[20:21], 2, v[0:1]
	v_mov_b32_e32 v77, v73
	v_lshl_add_u64 v[0:1], v[0:1], 0, v[76:77]
	s_lshl_b64 s[16:17], s[22:23], 4
	v_lshl_add_u64 v[2:3], v[0:1], 0, s[16:17]
	global_load_dwordx4 v[16:19], v[0:1], off nt
	global_load_dwordx4 v[8:11], v[2:3], off nt
	v_lshl_add_u64 v[0:1], v[2:3], 0, s[16:17]
	v_lshl_add_u64 v[2:3], v[0:1], 0, s[16:17]
	global_load_dwordx4 v[28:31], v[0:1], off nt
	global_load_dwordx4 v[20:23], v[2:3], off nt
	v_lshl_add_u64 v[0:1], v[2:3], 0, s[16:17]
	v_lshl_add_u64 v[2:3], v[0:1], 0, s[16:17]
	global_load_dwordx4 v[40:43], v[0:1], off nt
	global_load_dwordx4 v[32:35], v[2:3], off nt
	v_lshl_add_u64 v[0:1], v[2:3], 0, s[16:17]
	v_lshl_add_u64 v[2:3], v[0:1], 0, s[16:17]
	global_load_dwordx4 v[56:59], v[0:1], off nt
	global_load_dwordx4 v[44:47], v[2:3], off nt
	v_lshl_add_u64 v[0:1], v[2:3], 0, s[16:17]
	global_load_dwordx4 v[48:51], v[0:1], off nt
	v_lshl_add_u64 v[0:1], v[0:1], 0, s[16:17]
	global_load_dwordx4 v[36:39], v[0:1], off nt
	v_lshl_add_u64 v[0:1], v[0:1], 0, s[16:17]
	global_load_dwordx4 v[52:55], v[0:1], off nt
	v_lshl_add_u64 v[0:1], v[0:1], 0, s[16:17]
	global_load_dwordx4 v[12:15], v[0:1], off nt
	v_lshl_add_u64 v[0:1], v[0:1], 0, s[16:17]
	v_lshl_add_u64 v[4:5], v[0:1], 0, s[16:17]
	v_lshl_add_u64 v[60:61], v[4:5], 0, s[16:17]
	global_load_dwordx4 v[24:27], v[0:1], off nt
	s_nop 0
	global_load_dwordx4 v[0:3], v[4:5], off nt
	s_nop 0
	global_load_dwordx4 v[4:7], v[60:61], off nt
	v_lshl_add_u64 v[60:61], v[60:61], 0, s[16:17]
	global_load_dwordx4 v[60:63], v[60:61], off nt

.LBB0_1927:
	s_lshl_b32 s6, s18, 14
	s_add_i32 s7, s6, 0
	s_lshl_b32 s6, s23, 6
	v_bfe_u32 v75, v65, 4, 2
	v_or_b32_e32 v0, s6, v75
	s_ashr_i32 s13, s6, 31
	s_mul_i32 s13, s14, s13
	v_mul_lo_u32 v2, s15, v0
	v_mad_u64_u32 v[0:1], s[30:31], s14, v0, 0
	v_add3_u32 v1, v1, s13, v2
	v_lshlrev_b32_e32 v2, 2, v65
	v_lshl_add_u64 v[0:1], v[0:1], 2, s[8:9]
	s_ashr_i32 s13, s12, 31
	v_and_b32_e32 v64, 60, v2
	v_lshl_add_u64 v[0:1], s[12:13], 2, v[0:1]
	v_mov_b32_e32 v73, 0
	v_lshlrev_b32_e32 v72, 2, v64
	s_lshl_b64 s[8:9], s[14:15], 4
	s_mov_b32 s17, 0
	v_lshl_add_u64 v[66:67], v[0:1], 0, v[72:73]
	s_mul_i32 s16, s14, 0xf0
	s_sub_u32 s8, 0, s8
	v_lshl_add_u64 v[68:69], v[66:67], 0, s[16:17]
	s_subb_u32 s9, 0, s9
	v_lshl_add_u64 v[8:9], v[68:69], 0, s[8:9]
	v_lshl_add_u64 v[10:11], v[8:9], 0, s[8:9]
	global_load_dwordx4 v[4:7], v[8:9], off nt
	global_load_dwordx4 v[0:3], v[10:11], off nt
	v_lshl_add_u64 v[8:9], v[10:11], 0, s[8:9]
	v_lshl_add_u64 v[10:11], v[8:9], 0, s[8:9]
	global_load_dwordx4 v[24:27], v[8:9], off nt
	global_load_dwordx4 v[12:15], v[10:11], off nt
	v_lshl_add_u64 v[8:9], v[10:11], 0, s[8:9]
	v_lshl_add_u64 v[10:11], v[8:9], 0, s[8:9]
	global_load_dwordx4 v[52:55], v[8:9], off nt
	global_load_dwordx4 v[36:39], v[10:11], off nt
	v_lshl_add_u64 v[8:9], v[10:11], 0, s[8:9]
	global_load_dwordx4 v[48:51], v[8:9], off nt
	v_lshl_add_u64 v[8:9], v[8:9], 0, s[8:9]
	global_load_dwordx4 v[44:47], v[8:9], off nt
	v_lshl_add_u64 v[8:9], v[8:9], 0, s[8:9]
	global_load_dwordx4 v[56:59], v[8:9], off nt
	v_lshl_add_u64 v[8:9], v[8:9], 0, s[8:9]
	global_load_dwordx4 v[32:35], v[8:9], off nt
	v_lshl_add_u64 v[8:9], v[8:9], 0, s[8:9]
	global_load_dwordx4 v[40:43], v[8:9], off nt
	v_lshl_add_u64 v[8:9], v[8:9], 0, s[8:9]
	global_load_dwordx4 v[20:23], v[8:9], off nt
	v_lshl_add_u64 v[8:9], v[8:9], 0, s[8:9]
	v_lshl_add_u64 v[70:71], v[8:9], 0, s[8:9]
	global_load_dwordx4 v[28:31], v[8:9], off nt
	s_nop 0
	global_load_dwordx4 v[8:11], v[70:71], off nt
	global_load_dwordx4 v[60:63], v[68:69], off nt
	global_load_dwordx4 v[16:19], v[66:67], off nt
	v_lshl_add_u32 v69, v75, 8, s7
	v_lshlrev_b32_e32 v70, 2, v75
	v_add3_u32 v78, v69, v70, v72
	v_bitop3_b32 v70, v64, v75, 1 bitop3:0x36
	v_lshl_add_u32 v79, v70, 2, v69
	v_bitop3_b32 v70, v64, v75, 2 bitop3:0x36
	v_lshl_add_u32 v80, v70, 2, v69
	v_bitop3_b32 v70, v64, v75, 3 bitop3:0x36
	v_lshl_add_u32 v81, v70, 2, v69
	v_or_b32_e32 v69, 4, v75
	v_lshl_add_u32 v70, v69, 8, s7
	v_bitop3_b32 v71, v75, v64, 4 bitop3:0x36
	v_lshl_add_u32 v82, v71, 2, v70
	v_bitop3_b32 v71, v64, v69, 1 bitop3:0x36
	v_lshl_add_u32 v83, v71, 2, v70
	v_bitop3_b32 v71, v64, v69, 2 bitop3:0x36
	v_bitop3_b32 v69, v64, v69, 3 bitop3:0x36
	v_lshl_add_u32 v85, v69, 2, v70
	v_or_b32_e32 v69, 8, v75
	v_lshl_add_u32 v84, v71, 2, v70
	v_lshl_add_u32 v70, v69, 8, s7
	v_bitop3_b32 v71, v75, v64, 8 bitop3:0x36
	v_lshl_add_u32 v86, v71, 2, v70
	v_bitop3_b32 v71, v64, v69, 1 bitop3:0x36
	v_lshl_add_u32 v87, v71, 2, v70
	v_bitop3_b32 v71, v64, v69, 2 bitop3:0x36
	v_bitop3_b32 v69, v64, v69, 3 bitop3:0x36
	v_lshl_add_u32 v89, v69, 2, v70
	v_or_b32_e32 v69, 12, v75
	v_lshl_add_u32 v88, v71, 2, v70
	v_lshl_add_u32 v70, v69, 8, s7
	v_bitop3_b32 v71, v75, v64, 12 bitop3:0x36
	v_lshl_add_u32 v90, v71, 2, v70
	v_bitop3_b32 v71, v64, v69, 1 bitop3:0x36
	v_lshl_add_u32 v91, v71, 2, v70
	v_bitop3_b32 v71, v64, v69, 2 bitop3:0x36
	v_bitop3_b32 v69, v64, v69, 3 bitop3:0x36
	v_lshl_add_u32 v93, v69, 2, v70
	v_or_b32_e32 v69, 16, v75
	v_lshl_add_u32 v92, v71, 2, v70
	v_lshl_add_u32 v70, v69, 8, s7
	v_bitop3_b32 v71, v75, v64, 16 bitop3:0x36
	v_lshl_add_u32 v94, v71, 2, v70
	v_bitop3_b32 v71, v64, v69, 1 bitop3:0x36
	v_lshl_add_u32 v95, v71, 2, v70
	v_bitop3_b32 v71, v64, v69, 2 bitop3:0x36
	v_bitop3_b32 v69, v64, v69, 3 bitop3:0x36
	v_lshl_add_u32 v97, v69, 2, v70
	v_or_b32_e32 v69, 20, v75
	v_lshl_add_u32 v96, v71, 2, v70
	v_lshl_add_u32 v70, v69, 8, s7
	v_bitop3_b32 v71, v75, v64, 20 bitop3:0x36
	v_lshl_add_u32 v98, v71, 2, v70
	v_bitop3_b32 v71, v64, v69, 1 bitop3:0x36
	v_lshl_add_u32 v99, v71, 2, v70
	v_bitop3_b32 v71, v64, v69, 2 bitop3:0x36
	v_bitop3_b32 v69, v64, v69, 3 bitop3:0x36
	v_lshl_add_u32 v101, v69, 2, v70
	v_or_b32_e32 v69, 24, v75
	v_lshl_add_u32 v100, v71, 2, v70
	v_lshl_add_u32 v70, v69, 8, s7
	v_bitop3_b32 v71, v75, v64, 24 bitop3:0x36
	v_lshl_add_u32 v102, v71, 2, v70
	v_bitop3_b32 v71, v64, v69, 1 bitop3:0x36
	v_lshl_add_u32 v103, v71, 2, v70
	v_bitop3_b32 v71, v64, v69, 2 bitop3:0x36
	v_bitop3_b32 v69, v64, v69, 3 bitop3:0x36
	v_lshl_add_u32 v105, v69, 2, v70
	v_or_b32_e32 v69, 28, v75
	v_lshl_add_u32 v104, v71, 2, v70
	v_lshl_add_u32 v70, v69, 8, s7
	v_bitop3_b32 v71, v75, v64, 28 bitop3:0x36
	v_lshl_add_u32 v106, v71, 2, v70
	v_bitop3_b32 v71, v64, v69, 1 bitop3:0x36
	v_lshl_add_u32 v107, v71, 2, v70
	v_bitop3_b32 v71, v64, v69, 2 bitop3:0x36
	v_bitop3_b32 v69, v64, v69, 3 bitop3:0x36
	v_lshl_add_u32 v109, v69, 2, v70
	v_or_b32_e32 v69, 36, v75
	v_or_b32_e32 v66, 1, v64
	v_lshl_add_u32 v108, v71, 2, v70
	v_lshl_add_u32 v70, v69, 8, s7
	v_bitop3_b32 v71, v69, v64, 7 bitop3:0x6c
	v_or_b32_e32 v67, 2, v64
	v_or_b32_e32 v68, 3, v64
	v_lshl_add_u32 v110, v71, 2, v70
	v_bitop3_b32 v71, v69, v66, 7 bitop3:0x6c
	v_lshl_add_u32 v111, v71, 2, v70
	v_bitop3_b32 v71, v69, v67, 7 bitop3:0x6c
	v_bitop3_b32 v69, v69, v68, 7 bitop3:0x6c
	v_lshl_add_u32 v113, v69, 2, v70
	v_or_b32_e32 v69, 40, v75
	v_lshl_add_u32 v112, v71, 2, v70
	v_lshl_add_u32 v70, v69, 8, s7
	v_bitop3_b32 v71, v69, v64, 11 bitop3:0x6c
	v_lshl_add_u32 v114, v71, 2, v70
	v_bitop3_b32 v71, v69, v66, 11 bitop3:0x6c
	v_lshl_add_u32 v115, v71, 2, v70
	v_bitop3_b32 v71, v69, v67, 11 bitop3:0x6c
	v_bitop3_b32 v69, v69, v68, 11 bitop3:0x6c
	v_lshl_add_u32 v117, v69, 2, v70
	v_or_b32_e32 v69, 44, v75
	v_lshl_add_u32 v116, v71, 2, v70
	v_lshl_add_u32 v70, v69, 8, s7
	v_bitop3_b32 v71, v69, v64, 15 bitop3:0x6c
	v_lshl_add_u32 v118, v71, 2, v70
	v_bitop3_b32 v71, v69, v66, 15 bitop3:0x6c
	v_lshl_add_u32 v119, v71, 2, v70
	v_bitop3_b32 v71, v69, v67, 15 bitop3:0x6c
	v_bitop3_b32 v69, v69, v68, 15 bitop3:0x6c
	v_lshl_add_u32 v121, v69, 2, v70
	v_or_b32_e32 v69, 48, v75
	v_lshl_add_u32 v120, v71, 2, v70
	v_lshl_add_u32 v70, v69, 8, s7
	v_bitop3_b32 v71, v69, v64, 19 bitop3:0x6c
	v_lshl_add_u32 v122, v71, 2, v70
	v_bitop3_b32 v71, v69, v66, 19 bitop3:0x6c
	v_lshl_add_u32 v123, v71, 2, v70
	v_bitop3_b32 v71, v69, v67, 19 bitop3:0x6c
	v_bitop3_b32 v69, v69, v68, 19 bitop3:0x6c
	v_lshl_add_u32 v125, v69, 2, v70
	v_or_b32_e32 v69, 52, v75
	v_lshl_add_u32 v124, v71, 2, v70
	v_lshl_add_u32 v70, v69, 8, s7
	v_bitop3_b32 v71, v69, v64, 23 bitop3:0x6c
	v_lshl_add_u32 v126, v71, 2, v70
	v_bitop3_b32 v71, v69, v66, 23 bitop3:0x6c
	v_lshl_add_u32 v127, v71, 2, v70
	v_bitop3_b32 v71, v69, v67, 23 bitop3:0x6c
	v_bitop3_b32 v69, v69, v68, 23 bitop3:0x6c
	v_lshl_add_u32 v129, v69, 2, v70
	v_or_b32_e32 v69, 56, v75
	v_lshl_add_u32 v128, v71, 2, v70
	v_lshl_add_u32 v70, v69, 8, s7
	v_bitop3_b32 v71, v69, v64, 27 bitop3:0x6c
	v_lshl_add_u32 v130, v71, 2, v70
	v_bitop3_b32 v71, v69, v66, 27 bitop3:0x6c
	v_lshl_add_u32 v131, v71, 2, v70
	v_bitop3_b32 v71, v69, v67, 27 bitop3:0x6c
	v_bitop3_b32 v69, v69, v68, 27 bitop3:0x6c
	v_lshl_add_u32 v133, v69, 2, v70
	v_or_b32_e32 v69, 60, v75
	v_lshl_add_u32 v132, v71, 2, v70
	v_lshl_add_u32 v70, v69, 8, s7
	v_bitop3_b32 v66, v69, v66, 31 bitop3:0x6c
	v_lshl_add_u32 v135, v66, 2, v70
	v_bitop3_b32 v66, v69, v67, 31 bitop3:0x6c
	v_and_b32_e32 v74, 63, v65
	v_lshl_add_u32 v136, v66, 2, v70
	v_bitop3_b32 v66, v69, v68, 31 bitop3:0x6c
	s_add_u32 s27, s21, 0x1a000000
	v_lshl_add_u32 v137, v66, 2, v70
	s_addc_u32 s30, s22, 0
	v_lshlrev_b32_e32 v66, 3, v74
	s_add_u32 s31, s21, 0x2000000
	v_and_b32_e32 v74, 56, v66
	v_bfe_u32 v138, v65, 3, 3
	v_and_b32_e32 v65, 24, v66
	s_addc_u32 s36, s22, 0
	v_lshl_add_u32 v67, v74, 8, s7
	v_lshlrev_b32_e32 v65, 2, v65
	v_lshlrev_b32_e32 v68, 2, v138
	s_add_u32 s37, s21, 0x1a00000
	v_add3_u32 v146, v67, v65, v68
	v_or_b32_e32 v65, 1, v74
	v_bitop3_b32 v71, v69, v64, 31 bitop3:0x6c
	s_addc_u32 s38, s22, 0
	v_bitop3_b32 v68, v65, v138, 25 bitop3:0x6c
	v_lshl_add_u32 v69, v65, 8, s7
	s_add_u32 s39, s21, 0x1800000
	v_lshl_add_u32 v147, v68, 2, v69
	v_or_b32_e32 v68, 2, v74
	v_lshl_add_u32 v134, v71, 2, v70
	s_addc_u32 s40, s22, 0
	v_bitop3_b32 v70, v68, v138, 26 bitop3:0x6c
	v_lshl_add_u32 v71, v68, 8, s7
	s_add_u32 s41, s21, 0x1500000
	v_or_b32_e32 v139, 8, v138
	v_or_b32_e32 v140, 16, v138
	v_or_b32_e32 v141, 24, v138
	v_or_b32_e32 v142, 32, v138
	v_or_b32_e32 v143, 40, v138
	v_or_b32_e32 v144, 48, v138
	v_or_b32_e32 v145, 56, v138
	v_lshl_add_u32 v148, v70, 2, v71
	v_or_b32_e32 v70, 3, v74
	s_addc_u32 s45, s22, 0
	v_bitop3_b32 v72, v70, v138, 27 bitop3:0x6c
	v_lshl_add_u32 v76, v70, 8, s7
	v_bitop3_b32 v155, v65, v139, 25 bitop3:0x6c
	v_bitop3_b32 v163, v65, v140, 25 bitop3:0x6c
	v_bitop3_b32 v171, v65, v141, 25 bitop3:0x6c
	v_bitop3_b32 v178, v65, v142, 25 bitop3:0x6c
	v_bitop3_b32 v186, v65, v143, 25 bitop3:0x6c
	v_bitop3_b32 v194, v65, v144, 25 bitop3:0x6c
	v_bitop3_b32 v65, v65, v145, 25 bitop3:0x6c
	s_add_u32 s46, s21, 0x1200000
	v_lshl_add_u32 v149, v72, 2, v76
	v_or_b32_e32 v72, 4, v74
	v_lshl_add_u32 v202, v65, 2, v69
	v_bitop3_b32 v65, v68, v145, 26 bitop3:0x6c
	s_addc_u32 s47, s22, 0
	v_bitop3_b32 v77, v72, v138, 28 bitop3:0x6c
	v_lshl_add_u32 v205, v72, 8, s7
	v_lshl_add_u32 v203, v65, 2, v71
	v_bitop3_b32 v65, v70, v145, 27 bitop3:0x6c
	s_add_u32 s48, s21, 0xe00000
	v_lshl_add_u32 v150, v77, 2, v205
	v_or_b32_e32 v77, 5, v74
	v_bitop3_b32 v158, v72, v139, 28 bitop3:0x6c
	v_bitop3_b32 v166, v72, v140, 28 bitop3:0x6c
	v_bitop3_b32 v174, v72, v141, 28 bitop3:0x6c
	v_bitop3_b32 v181, v72, v142, 28 bitop3:0x6c
	v_bitop3_b32 v189, v72, v143, 28 bitop3:0x6c
	v_bitop3_b32 v197, v72, v144, 28 bitop3:0x6c
	v_lshl_add_u32 v204, v65, 2, v76
	v_bitop3_b32 v65, v72, v145, 28 bitop3:0x6c
	s_addc_u32 s49, s22, 0
	v_bitop3_b32 v151, v77, v138, 29 bitop3:0x6c
	v_lshl_add_u32 v206, v77, 8, s7
	v_or_b32_e32 v207, 6, v74
	v_lshl_add_u32 v158, v158, 2, v205
	v_bitop3_b32 v159, v77, v139, 29 bitop3:0x6c
	v_lshl_add_u32 v166, v166, 2, v205
	v_bitop3_b32 v167, v77, v140, 29 bitop3:0x6c
	v_lshl_add_u32 v174, v174, 2, v205
	v_bitop3_b32 v175, v77, v141, 29 bitop3:0x6c
	v_lshl_add_u32 v181, v181, 2, v205
	v_bitop3_b32 v182, v77, v142, 29 bitop3:0x6c
	v_lshl_add_u32 v189, v189, 2, v205
	v_bitop3_b32 v190, v77, v143, 29 bitop3:0x6c
	v_lshl_add_u32 v197, v197, 2, v205
	v_bitop3_b32 v198, v77, v144, 29 bitop3:0x6c
	v_lshl_add_u32 v205, v65, 2, v205
	v_bitop3_b32 v65, v77, v145, 29 bitop3:0x6c
	s_add_u32 s50, s21, 0x200000
	v_lshl_add_u32 v151, v151, 2, v206
	v_lshl_add_u32 v208, v207, 8, s7
	v_or_b32_e32 v209, 7, v74
	v_lshl_add_u32 v159, v159, 2, v206
	v_lshl_add_u32 v167, v167, 2, v206
	v_lshl_add_u32 v175, v175, 2, v206
	v_lshl_add_u32 v182, v182, 2, v206
	v_lshl_add_u32 v190, v190, 2, v206
	v_lshl_add_u32 v198, v198, 2, v206
	v_lshl_add_u32 v206, v65, 2, v206
	v_bitop3_b32 v65, v207, v145, 30 bitop3:0x6c
	s_addc_u32 s51, s22, 0
	v_bitop3_b32 v152, v207, v138, 30 bitop3:0x6c
	v_bitop3_b32 v153, v209, v138, 31 bitop3:0x6c
	v_lshl_add_u32 v210, v209, 8, s7
	v_bitop3_b32 v154, v66, v139, 24 bitop3:0x6c
	v_bitop3_b32 v156, v68, v139, 26 bitop3:0x6c
	v_bitop3_b32 v157, v70, v139, 27 bitop3:0x6c
	v_bitop3_b32 v160, v207, v139, 30 bitop3:0x6c
	v_bitop3_b32 v161, v209, v139, 31 bitop3:0x6c
	v_bitop3_b32 v162, v66, v140, 24 bitop3:0x6c
	v_bitop3_b32 v164, v68, v140, 26 bitop3:0x6c
	v_bitop3_b32 v165, v70, v140, 27 bitop3:0x6c
	v_bitop3_b32 v168, v207, v140, 30 bitop3:0x6c
	v_bitop3_b32 v169, v209, v140, 31 bitop3:0x6c
	v_bitop3_b32 v170, v66, v138, 24 bitop3:0x4e
	v_bitop3_b32 v172, v68, v141, 26 bitop3:0x6c
	v_bitop3_b32 v173, v70, v141, 27 bitop3:0x6c
	v_bitop3_b32 v176, v207, v141, 30 bitop3:0x6c
	v_bitop3_b32 v177, v209, v141, 31 bitop3:0x6c
	v_bitop3_b32 v179, v68, v142, 26 bitop3:0x6c
	v_bitop3_b32 v180, v70, v142, 27 bitop3:0x6c
	v_bitop3_b32 v183, v207, v142, 30 bitop3:0x6c
	v_bitop3_b32 v184, v209, v142, 31 bitop3:0x6c
	v_bitop3_b32 v185, v66, v143, 24 bitop3:0x6c
	v_bitop3_b32 v187, v68, v143, 26 bitop3:0x6c
	v_bitop3_b32 v188, v70, v143, 27 bitop3:0x6c
	v_bitop3_b32 v191, v207, v143, 30 bitop3:0x6c
	v_bitop3_b32 v192, v209, v143, 31 bitop3:0x6c
	v_bitop3_b32 v193, v66, v144, 24 bitop3:0x6c
	v_bitop3_b32 v195, v68, v144, 26 bitop3:0x6c
	v_bitop3_b32 v196, v70, v144, 27 bitop3:0x6c
	v_bitop3_b32 v199, v207, v144, 30 bitop3:0x6c
	v_bitop3_b32 v200, v209, v144, 31 bitop3:0x6c
	v_bitop3_b32 v66, v66, v145, 24 bitop3:0x6c
	v_lshl_add_u32 v207, v65, 2, v208
	v_bitop3_b32 v65, v209, v145, 31 bitop3:0x6c
	s_add_i32 s7, s19, s18
	v_lshl_add_u32 v152, v152, 2, v208
	v_lshl_add_u32 v153, v153, 2, v210
	v_lshl_add_u32 v154, v154, 2, v67
	v_lshl_add_u32 v155, v155, 2, v69
	v_lshl_add_u32 v156, v156, 2, v71
	v_lshl_add_u32 v157, v157, 2, v76
	v_lshl_add_u32 v160, v160, 2, v208
	v_lshl_add_u32 v161, v161, 2, v210
	v_lshl_add_u32 v162, v162, 2, v67
	v_lshl_add_u32 v163, v163, 2, v69
	v_lshl_add_u32 v164, v164, 2, v71
	v_lshl_add_u32 v165, v165, 2, v76
	v_lshl_add_u32 v168, v168, 2, v208
	v_lshl_add_u32 v169, v169, 2, v210
	v_lshl_add_u32 v170, v170, 2, v67
	v_lshl_add_u32 v171, v171, 2, v69
	v_lshl_add_u32 v172, v172, 2, v71
	v_lshl_add_u32 v173, v173, 2, v76
	v_lshl_add_u32 v176, v176, 2, v208
	v_lshl_add_u32 v177, v177, 2, v210
	v_lshl_add_u32 v178, v178, 2, v69
	v_lshl_add_u32 v179, v179, 2, v71
	v_lshl_add_u32 v180, v180, 2, v76
	v_lshl_add_u32 v183, v183, 2, v208
	v_lshl_add_u32 v184, v184, 2, v210
	v_lshl_add_u32 v185, v185, 2, v67
	v_lshl_add_u32 v186, v186, 2, v69
	v_lshl_add_u32 v187, v187, 2, v71
	v_lshl_add_u32 v188, v188, 2, v76
	v_lshl_add_u32 v191, v191, 2, v208
	v_lshl_add_u32 v192, v192, 2, v210
	v_lshl_add_u32 v193, v193, 2, v67
	v_lshl_add_u32 v194, v194, 2, v69
	v_lshl_add_u32 v195, v195, 2, v71
	v_lshl_add_u32 v196, v196, 2, v76
	v_lshl_add_u32 v199, v199, 2, v208
	v_lshl_add_u32 v200, v200, 2, v210
	v_lshl_add_u32 v201, v66, 2, v67
	v_lshl_add_u32 v208, v65, 2, v210
	s_add_i32 s52, s7, 0x8800
	s_lshl_b32 s53, s20, 6
	v_lshlrev_b32_e32 v76, 2, v64
	v_lshlrev_b32_e32 v72, 1, v74
	s_branch .LBB0_1933

.LBB0_2136:
	s_lshl_b32 s8, s15, 14
	s_add_i32 s9, s8, 0
	s_lshl_b32 s8, s26, 6
	v_bfe_u32 v75, v65, 4, 2
	v_or_b32_e32 v0, s8, v75
	s_ashr_i32 s15, s8, 31
	s_mul_i32 s15, s16, s15
	v_mul_lo_u32 v2, s17, v0
	v_mad_u64_u32 v[0:1], s[26:27], s16, v0, 0
	v_add3_u32 v1, v1, s15, v2
	v_lshlrev_b32_e32 v2, 2, v65
	v_lshl_add_u64 v[0:1], v[0:1], 2, s[12:13]
	s_ashr_i32 s15, s14, 31
	v_and_b32_e32 v64, 60, v2
	v_lshl_add_u64 v[0:1], s[14:15], 2, v[0:1]
	v_mov_b32_e32 v73, 0
	v_lshlrev_b32_e32 v72, 2, v64
	s_lshl_b64 s[12:13], s[16:17], 4
	s_mov_b32 s19, 0
	v_lshl_add_u64 v[66:67], v[0:1], 0, v[72:73]
	s_mul_i32 s18, s16, 0xf0
	s_sub_u32 s12, 0, s12
	v_lshl_add_u64 v[68:69], v[66:67], 0, s[18:19]
	s_subb_u32 s13, 0, s13
	v_lshl_add_u64 v[8:9], v[68:69], 0, s[12:13]
	v_lshl_add_u64 v[10:11], v[8:9], 0, s[12:13]
	global_load_dwordx4 v[4:7], v[8:9], off nt
	global_load_dwordx4 v[0:3], v[10:11], off nt
	v_lshl_add_u64 v[8:9], v[10:11], 0, s[12:13]
	v_lshl_add_u64 v[10:11], v[8:9], 0, s[12:13]
	global_load_dwordx4 v[24:27], v[8:9], off nt
	global_load_dwordx4 v[12:15], v[10:11], off nt
	v_lshl_add_u64 v[8:9], v[10:11], 0, s[12:13]
	v_lshl_add_u64 v[10:11], v[8:9], 0, s[12:13]
	global_load_dwordx4 v[52:55], v[8:9], off nt
	global_load_dwordx4 v[36:39], v[10:11], off nt
	v_lshl_add_u64 v[8:9], v[10:11], 0, s[12:13]
	global_load_dwordx4 v[48:51], v[8:9], off nt
	v_lshl_add_u64 v[8:9], v[8:9], 0, s[12:13]
	global_load_dwordx4 v[44:47], v[8:9], off nt
	v_lshl_add_u64 v[8:9], v[8:9], 0, s[12:13]
	global_load_dwordx4 v[56:59], v[8:9], off nt
	v_lshl_add_u64 v[8:9], v[8:9], 0, s[12:13]
	global_load_dwordx4 v[32:35], v[8:9], off nt
	v_lshl_add_u64 v[8:9], v[8:9], 0, s[12:13]
	global_load_dwordx4 v[40:43], v[8:9], off nt
	v_lshl_add_u64 v[8:9], v[8:9], 0, s[12:13]
	global_load_dwordx4 v[20:23], v[8:9], off nt
	v_lshl_add_u64 v[8:9], v[8:9], 0, s[12:13]
	v_lshl_add_u64 v[70:71], v[8:9], 0, s[12:13]
	global_load_dwordx4 v[28:31], v[8:9], off nt
	s_nop 0
	global_load_dwordx4 v[8:11], v[70:71], off nt
	global_load_dwordx4 v[60:63], v[68:69], off nt
	global_load_dwordx4 v[16:19], v[66:67], off nt
	v_lshl_add_u32 v69, v75, 8, s9
	v_lshlrev_b32_e32 v70, 2, v75
	v_add3_u32 v78, v69, v70, v72
	v_bitop3_b32 v70, v64, v75, 1 bitop3:0x36
	v_lshl_add_u32 v79, v70, 2, v69
	v_bitop3_b32 v70, v64, v75, 2 bitop3:0x36
	v_lshl_add_u32 v80, v70, 2, v69
	v_bitop3_b32 v70, v64, v75, 3 bitop3:0x36
	v_lshl_add_u32 v81, v70, 2, v69
	v_or_b32_e32 v69, 4, v75
	v_lshl_add_u32 v70, v69, 8, s9
	v_bitop3_b32 v71, v75, v64, 4 bitop3:0x36
	v_lshl_add_u32 v82, v71, 2, v70
	v_bitop3_b32 v71, v64, v69, 1 bitop3:0x36
	v_lshl_add_u32 v83, v71, 2, v70
	v_bitop3_b32 v71, v64, v69, 2 bitop3:0x36
	v_bitop3_b32 v69, v64, v69, 3 bitop3:0x36
	v_lshl_add_u32 v85, v69, 2, v70
	v_or_b32_e32 v69, 8, v75
	v_lshl_add_u32 v84, v71, 2, v70
	v_lshl_add_u32 v70, v69, 8, s9
	v_bitop3_b32 v71, v75, v64, 8 bitop3:0x36
	v_lshl_add_u32 v86, v71, 2, v70
	v_bitop3_b32 v71, v64, v69, 1 bitop3:0x36
	v_lshl_add_u32 v87, v71, 2, v70
	v_bitop3_b32 v71, v64, v69, 2 bitop3:0x36
	v_bitop3_b32 v69, v64, v69, 3 bitop3:0x36
	v_lshl_add_u32 v89, v69, 2, v70
	v_or_b32_e32 v69, 12, v75
	v_lshl_add_u32 v88, v71, 2, v70
	v_lshl_add_u32 v70, v69, 8, s9
	v_bitop3_b32 v71, v75, v64, 12 bitop3:0x36
	v_lshl_add_u32 v90, v71, 2, v70
	v_bitop3_b32 v71, v64, v69, 1 bitop3:0x36
	v_lshl_add_u32 v91, v71, 2, v70
	v_bitop3_b32 v71, v64, v69, 2 bitop3:0x36
	v_bitop3_b32 v69, v64, v69, 3 bitop3:0x36
	v_lshl_add_u32 v93, v69, 2, v70
	v_or_b32_e32 v69, 16, v75
	v_lshl_add_u32 v92, v71, 2, v70
	v_lshl_add_u32 v70, v69, 8, s9
	v_bitop3_b32 v71, v75, v64, 16 bitop3:0x36
	v_lshl_add_u32 v94, v71, 2, v70
	v_bitop3_b32 v71, v64, v69, 1 bitop3:0x36
	v_lshl_add_u32 v95, v71, 2, v70
	v_bitop3_b32 v71, v64, v69, 2 bitop3:0x36
	v_bitop3_b32 v69, v64, v69, 3 bitop3:0x36
	v_lshl_add_u32 v97, v69, 2, v70
	v_or_b32_e32 v69, 20, v75
	v_lshl_add_u32 v96, v71, 2, v70
	v_lshl_add_u32 v70, v69, 8, s9
	v_bitop3_b32 v71, v75, v64, 20 bitop3:0x36
	v_lshl_add_u32 v98, v71, 2, v70
	v_bitop3_b32 v71, v64, v69, 1 bitop3:0x36
	v_lshl_add_u32 v99, v71, 2, v70
	v_bitop3_b32 v71, v64, v69, 2 bitop3:0x36
	v_bitop3_b32 v69, v64, v69, 3 bitop3:0x36
	v_lshl_add_u32 v101, v69, 2, v70
	v_or_b32_e32 v69, 24, v75
	v_lshl_add_u32 v100, v71, 2, v70
	v_lshl_add_u32 v70, v69, 8, s9
	v_bitop3_b32 v71, v75, v64, 24 bitop3:0x36
	v_lshl_add_u32 v102, v71, 2, v70
	v_bitop3_b32 v71, v64, v69, 1 bitop3:0x36
	v_lshl_add_u32 v103, v71, 2, v70
	v_bitop3_b32 v71, v64, v69, 2 bitop3:0x36
	v_bitop3_b32 v69, v64, v69, 3 bitop3:0x36
	v_lshl_add_u32 v105, v69, 2, v70
	v_or_b32_e32 v69, 28, v75
	v_lshl_add_u32 v104, v71, 2, v70
	v_lshl_add_u32 v70, v69, 8, s9
	v_bitop3_b32 v71, v75, v64, 28 bitop3:0x36
	v_lshl_add_u32 v106, v71, 2, v70
	v_bitop3_b32 v71, v64, v69, 1 bitop3:0x36
	v_lshl_add_u32 v107, v71, 2, v70
	v_bitop3_b32 v71, v64, v69, 2 bitop3:0x36
	v_bitop3_b32 v69, v64, v69, 3 bitop3:0x36
	v_lshl_add_u32 v109, v69, 2, v70
	v_or_b32_e32 v69, 36, v75
	v_or_b32_e32 v66, 1, v64
	v_lshl_add_u32 v108, v71, 2, v70
	v_lshl_add_u32 v70, v69, 8, s9
	v_bitop3_b32 v71, v69, v64, 7 bitop3:0x6c
	v_or_b32_e32 v67, 2, v64
	v_or_b32_e32 v68, 3, v64
	v_lshl_add_u32 v110, v71, 2, v70
	v_bitop3_b32 v71, v69, v66, 7 bitop3:0x6c
	v_lshl_add_u32 v111, v71, 2, v70
	v_bitop3_b32 v71, v69, v67, 7 bitop3:0x6c
	v_bitop3_b32 v69, v69, v68, 7 bitop3:0x6c
	v_lshl_add_u32 v113, v69, 2, v70
	v_or_b32_e32 v69, 40, v75
	v_lshl_add_u32 v112, v71, 2, v70
	v_lshl_add_u32 v70, v69, 8, s9
	v_bitop3_b32 v71, v69, v64, 11 bitop3:0x6c
	v_lshl_add_u32 v114, v71, 2, v70
	v_bitop3_b32 v71, v69, v66, 11 bitop3:0x6c
	v_lshl_add_u32 v115, v71, 2, v70
	v_bitop3_b32 v71, v69, v67, 11 bitop3:0x6c
	v_bitop3_b32 v69, v69, v68, 11 bitop3:0x6c
	v_lshl_add_u32 v117, v69, 2, v70
	v_or_b32_e32 v69, 44, v75
	v_lshl_add_u32 v116, v71, 2, v70
	v_lshl_add_u32 v70, v69, 8, s9
	v_bitop3_b32 v71, v69, v64, 15 bitop3:0x6c
	v_lshl_add_u32 v118, v71, 2, v70
	v_bitop3_b32 v71, v69, v66, 15 bitop3:0x6c
	v_lshl_add_u32 v119, v71, 2, v70
	v_bitop3_b32 v71, v69, v67, 15 bitop3:0x6c
	v_bitop3_b32 v69, v69, v68, 15 bitop3:0x6c
	v_lshl_add_u32 v121, v69, 2, v70
	v_or_b32_e32 v69, 48, v75
	v_lshl_add_u32 v120, v71, 2, v70
	v_lshl_add_u32 v70, v69, 8, s9
	v_bitop3_b32 v71, v69, v64, 19 bitop3:0x6c
	v_lshl_add_u32 v122, v71, 2, v70
	v_bitop3_b32 v71, v69, v66, 19 bitop3:0x6c
	v_lshl_add_u32 v123, v71, 2, v70
	v_bitop3_b32 v71, v69, v67, 19 bitop3:0x6c
	v_bitop3_b32 v69, v69, v68, 19 bitop3:0x6c
	v_lshl_add_u32 v125, v69, 2, v70
	v_or_b32_e32 v69, 52, v75
	v_lshl_add_u32 v124, v71, 2, v70
	v_lshl_add_u32 v70, v69, 8, s9
	v_bitop3_b32 v71, v69, v64, 23 bitop3:0x6c
	v_lshl_add_u32 v126, v71, 2, v70
	v_bitop3_b32 v71, v69, v66, 23 bitop3:0x6c
	v_lshl_add_u32 v127, v71, 2, v70
	v_bitop3_b32 v71, v69, v67, 23 bitop3:0x6c
	v_bitop3_b32 v69, v69, v68, 23 bitop3:0x6c
	v_lshl_add_u32 v129, v69, 2, v70
	v_or_b32_e32 v69, 56, v75
	v_lshl_add_u32 v128, v71, 2, v70
	v_lshl_add_u32 v70, v69, 8, s9
	v_bitop3_b32 v71, v69, v64, 27 bitop3:0x6c
	v_lshl_add_u32 v130, v71, 2, v70
	v_bitop3_b32 v71, v69, v66, 27 bitop3:0x6c
	v_lshl_add_u32 v131, v71, 2, v70
	v_bitop3_b32 v71, v69, v67, 27 bitop3:0x6c
	v_bitop3_b32 v69, v69, v68, 27 bitop3:0x6c
	v_lshl_add_u32 v133, v69, 2, v70
	v_or_b32_e32 v69, 60, v75
	v_lshl_add_u32 v132, v71, 2, v70
	v_lshl_add_u32 v70, v69, 8, s9
	v_bitop3_b32 v66, v69, v66, 31 bitop3:0x6c
	v_lshl_add_u32 v135, v66, 2, v70
	v_bitop3_b32 v66, v69, v67, 31 bitop3:0x6c
	s_add_u32 s37, s23, 0x1a000000
	v_and_b32_e32 v74, 63, v65
	v_lshl_add_u32 v136, v66, 2, v70
	v_bitop3_b32 v66, v69, v68, 31 bitop3:0x6c
	s_addc_u32 s38, s24, 0
	v_lshl_add_u32 v137, v66, 2, v70
	s_add_u32 s39, s23, 0x2000000
	v_lshlrev_b32_e32 v66, 3, v74
	s_addc_u32 s40, s24, 0
	v_and_b32_e32 v74, 56, v66
	v_bfe_u32 v138, v65, 3, 3
	v_and_b32_e32 v65, 24, v66
	s_add_u32 s41, s23, 0x1a00000
	v_lshl_add_u32 v67, v74, 8, s9
	v_lshlrev_b32_e32 v65, 2, v65
	v_lshlrev_b32_e32 v68, 2, v138
	s_addc_u32 s45, s24, 0
	v_add3_u32 v146, v67, v65, v68
	v_or_b32_e32 v65, 1, v74
	v_bitop3_b32 v71, v69, v64, 31 bitop3:0x6c
	s_add_u32 s46, s23, 0x1800000
	v_bitop3_b32 v68, v65, v138, 25 bitop3:0x6c
	v_lshl_add_u32 v69, v65, 8, s9
	s_addc_u32 s47, s24, 0
	v_lshl_add_u32 v147, v68, 2, v69
	v_or_b32_e32 v68, 2, v74
	v_lshl_add_u32 v134, v71, 2, v70
	s_add_u32 s48, s23, 0x1500000
	v_bitop3_b32 v70, v68, v138, 26 bitop3:0x6c
	v_lshl_add_u32 v71, v68, 8, s9
	s_addc_u32 s49, s24, 0
	v_or_b32_e32 v139, 8, v138
	v_or_b32_e32 v140, 16, v138
	v_or_b32_e32 v141, 24, v138
	v_or_b32_e32 v142, 32, v138
	v_or_b32_e32 v143, 40, v138
	v_or_b32_e32 v144, 48, v138
	v_or_b32_e32 v145, 56, v138
	v_lshl_add_u32 v148, v70, 2, v71
	v_or_b32_e32 v70, 3, v74
	s_add_u32 s50, s23, 0x1200000
	v_bitop3_b32 v72, v70, v138, 27 bitop3:0x6c
	v_lshl_add_u32 v76, v70, 8, s9
	v_bitop3_b32 v155, v65, v139, 25 bitop3:0x6c
	v_bitop3_b32 v163, v65, v140, 25 bitop3:0x6c
	v_bitop3_b32 v171, v65, v141, 25 bitop3:0x6c
	v_bitop3_b32 v178, v65, v142, 25 bitop3:0x6c
	v_bitop3_b32 v186, v65, v143, 25 bitop3:0x6c
	v_bitop3_b32 v194, v65, v144, 25 bitop3:0x6c
	v_bitop3_b32 v65, v65, v145, 25 bitop3:0x6c
	s_addc_u32 s51, s24, 0
	v_lshl_add_u32 v149, v72, 2, v76
	v_or_b32_e32 v72, 4, v74
	v_lshl_add_u32 v202, v65, 2, v69
	v_bitop3_b32 v65, v68, v145, 26 bitop3:0x6c
	s_add_u32 s52, s23, 0xe00000
	v_bitop3_b32 v77, v72, v138, 28 bitop3:0x6c
	v_lshl_add_u32 v205, v72, 8, s9
	v_lshl_add_u32 v203, v65, 2, v71
	v_bitop3_b32 v65, v70, v145, 27 bitop3:0x6c
	s_addc_u32 s53, s24, 0
	v_lshl_add_u32 v150, v77, 2, v205
	v_or_b32_e32 v77, 5, v74
	v_bitop3_b32 v158, v72, v139, 28 bitop3:0x6c
	v_bitop3_b32 v166, v72, v140, 28 bitop3:0x6c
	v_bitop3_b32 v174, v72, v141, 28 bitop3:0x6c
	v_bitop3_b32 v181, v72, v142, 28 bitop3:0x6c
	v_bitop3_b32 v189, v72, v143, 28 bitop3:0x6c
	v_bitop3_b32 v197, v72, v144, 28 bitop3:0x6c
	v_lshl_add_u32 v204, v65, 2, v76
	v_bitop3_b32 v65, v72, v145, 28 bitop3:0x6c
	s_add_u32 s54, s23, 0x200000
	v_bitop3_b32 v151, v77, v138, 29 bitop3:0x6c
	v_lshl_add_u32 v206, v77, 8, s9
	v_or_b32_e32 v207, 6, v74
	v_or_b32_e32 v209, 7, v74
	v_lshl_add_u32 v158, v158, 2, v205
	v_bitop3_b32 v159, v77, v139, 29 bitop3:0x6c
	v_lshl_add_u32 v166, v166, 2, v205
	v_bitop3_b32 v167, v77, v140, 29 bitop3:0x6c
	v_lshl_add_u32 v174, v174, 2, v205
	v_bitop3_b32 v175, v77, v141, 29 bitop3:0x6c
	v_lshl_add_u32 v181, v181, 2, v205
	v_bitop3_b32 v182, v77, v142, 29 bitop3:0x6c
	v_lshl_add_u32 v189, v189, 2, v205
	v_bitop3_b32 v190, v77, v143, 29 bitop3:0x6c
	v_lshl_add_u32 v197, v197, 2, v205
	v_bitop3_b32 v198, v77, v144, 29 bitop3:0x6c
	v_lshl_add_u32 v205, v65, 2, v205
	v_bitop3_b32 v65, v77, v145, 29 bitop3:0x6c
	s_addc_u32 s55, s24, 0
	v_lshl_add_u32 v151, v151, 2, v206
	v_lshl_add_u32 v208, v207, 8, s9
	v_lshl_add_u32 v210, v209, 8, s9
	v_lshl_add_u32 v159, v159, 2, v206
	v_lshl_add_u32 v167, v167, 2, v206
	v_lshl_add_u32 v175, v175, 2, v206
	v_lshl_add_u32 v182, v182, 2, v206
	v_lshl_add_u32 v190, v190, 2, v206
	v_lshl_add_u32 v198, v198, 2, v206
	v_lshl_add_u32 v206, v65, 2, v206
	v_bitop3_b32 v65, v207, v145, 30 bitop3:0x6c
	s_add_i32 s9, s22, s21
	v_bitop3_b32 v152, v207, v138, 30 bitop3:0x6c
	v_bitop3_b32 v153, v209, v138, 31 bitop3:0x6c
	v_bitop3_b32 v154, v66, v139, 24 bitop3:0x6c
	v_bitop3_b32 v156, v68, v139, 26 bitop3:0x6c
	v_bitop3_b32 v157, v70, v139, 27 bitop3:0x6c
	v_bitop3_b32 v160, v207, v139, 30 bitop3:0x6c
	v_bitop3_b32 v161, v209, v139, 31 bitop3:0x6c
	v_bitop3_b32 v162, v66, v140, 24 bitop3:0x6c
	v_bitop3_b32 v164, v68, v140, 26 bitop3:0x6c
	v_bitop3_b32 v165, v70, v140, 27 bitop3:0x6c
	v_bitop3_b32 v168, v207, v140, 30 bitop3:0x6c
	v_bitop3_b32 v169, v209, v140, 31 bitop3:0x6c
	v_bitop3_b32 v170, v66, v138, 24 bitop3:0x4e
	v_bitop3_b32 v172, v68, v141, 26 bitop3:0x6c
	v_bitop3_b32 v173, v70, v141, 27 bitop3:0x6c
	v_bitop3_b32 v176, v207, v141, 30 bitop3:0x6c
	v_bitop3_b32 v177, v209, v141, 31 bitop3:0x6c
	v_bitop3_b32 v179, v68, v142, 26 bitop3:0x6c
	v_bitop3_b32 v180, v70, v142, 27 bitop3:0x6c
	v_bitop3_b32 v183, v207, v142, 30 bitop3:0x6c
	v_bitop3_b32 v184, v209, v142, 31 bitop3:0x6c
	v_bitop3_b32 v185, v66, v143, 24 bitop3:0x6c
	v_bitop3_b32 v187, v68, v143, 26 bitop3:0x6c
	v_bitop3_b32 v188, v70, v143, 27 bitop3:0x6c
	v_bitop3_b32 v191, v207, v143, 30 bitop3:0x6c
	v_bitop3_b32 v192, v209, v143, 31 bitop3:0x6c
	v_bitop3_b32 v193, v66, v144, 24 bitop3:0x6c
	v_bitop3_b32 v195, v68, v144, 26 bitop3:0x6c
	v_bitop3_b32 v196, v70, v144, 27 bitop3:0x6c
	v_bitop3_b32 v199, v207, v144, 30 bitop3:0x6c
	v_bitop3_b32 v200, v209, v144, 31 bitop3:0x6c
	v_bitop3_b32 v66, v66, v145, 24 bitop3:0x6c
	v_lshl_add_u32 v207, v65, 2, v208
	v_bitop3_b32 v65, v209, v145, 31 bitop3:0x6c
	s_add_i32 s56, s9, 0xc400
	s_lshl_b32 s9, s20, 9
	s_lshl_b32 s12, s21, 6
	v_lshl_add_u32 v152, v152, 2, v208
	v_lshl_add_u32 v153, v153, 2, v210
	v_lshl_add_u32 v154, v154, 2, v67
	v_lshl_add_u32 v155, v155, 2, v69
	v_lshl_add_u32 v156, v156, 2, v71
	v_lshl_add_u32 v157, v157, 2, v76
	v_lshl_add_u32 v160, v160, 2, v208
	v_lshl_add_u32 v161, v161, 2, v210
	v_lshl_add_u32 v162, v162, 2, v67
	v_lshl_add_u32 v163, v163, 2, v69
	v_lshl_add_u32 v164, v164, 2, v71
	v_lshl_add_u32 v165, v165, 2, v76
	v_lshl_add_u32 v168, v168, 2, v208
	v_lshl_add_u32 v169, v169, 2, v210
	v_lshl_add_u32 v170, v170, 2, v67
	v_lshl_add_u32 v171, v171, 2, v69
	v_lshl_add_u32 v172, v172, 2, v71
	v_lshl_add_u32 v173, v173, 2, v76
	v_lshl_add_u32 v176, v176, 2, v208
	v_lshl_add_u32 v177, v177, 2, v210
	v_lshl_add_u32 v178, v178, 2, v69
	v_lshl_add_u32 v179, v179, 2, v71
	v_lshl_add_u32 v180, v180, 2, v76
	v_lshl_add_u32 v183, v183, 2, v208
	v_lshl_add_u32 v184, v184, 2, v210
	v_lshl_add_u32 v185, v185, 2, v67
	v_lshl_add_u32 v186, v186, 2, v69
	v_lshl_add_u32 v187, v187, 2, v71
	v_lshl_add_u32 v188, v188, 2, v76
	v_lshl_add_u32 v191, v191, 2, v208
	v_lshl_add_u32 v192, v192, 2, v210
	v_lshl_add_u32 v193, v193, 2, v67
	v_lshl_add_u32 v194, v194, 2, v69
	v_lshl_add_u32 v195, v195, 2, v71
	v_lshl_add_u32 v196, v196, 2, v76
	v_lshl_add_u32 v199, v199, 2, v208
	v_lshl_add_u32 v200, v200, 2, v210
	v_lshl_add_u32 v201, v66, 2, v67
	v_lshl_add_u32 v208, v65, 2, v210
	s_add_i32 s57, s9, s12
	v_lshlrev_b32_e32 v76, 2, v64
	v_lshlrev_b32_e32 v72, 1, v74
	s_branch .LBB0_2142

.LBB0_2223:
	s_lshl_b32 s8, s15, 14
	s_add_i32 s9, s8, 0
	s_lshl_b32 s8, s30, 6
	v_bfe_u32 v75, v65, 4, 2
	v_or_b32_e32 v0, s8, v75
	s_ashr_i32 s15, s8, 31
	s_mul_i32 s15, s16, s15
	v_mul_lo_u32 v2, s17, v0
	v_mad_u64_u32 v[0:1], s[24:25], s16, v0, 0
	v_add3_u32 v1, v1, s15, v2
	v_lshlrev_b32_e32 v2, 2, v65
	v_lshl_add_u64 v[0:1], v[0:1], 2, s[12:13]
	s_ashr_i32 s15, s14, 31
	v_and_b32_e32 v64, 60, v2
	s_lshl_b32 s29, s29, 3
	v_lshl_add_u64 v[0:1], s[14:15], 2, v[0:1]
	v_mov_b32_e32 v73, 0
	v_lshlrev_b32_e32 v72, 2, v64
	s_lshl_b64 s[12:13], s[16:17], 4
	s_mov_b32 s19, 0
	v_lshl_add_u64 v[66:67], v[0:1], 0, v[72:73]
	s_mul_i32 s18, s16, 0xf0
	s_sub_u32 s12, 0, s12
	v_lshl_add_u64 v[68:69], v[66:67], 0, s[18:19]
	s_subb_u32 s13, 0, s13
	v_lshl_add_u64 v[8:9], v[68:69], 0, s[12:13]
	v_lshl_add_u64 v[10:11], v[8:9], 0, s[12:13]
	global_load_dwordx4 v[4:7], v[8:9], off nt
	global_load_dwordx4 v[0:3], v[10:11], off nt
	v_lshl_add_u64 v[8:9], v[10:11], 0, s[12:13]
	v_lshl_add_u64 v[10:11], v[8:9], 0, s[12:13]
	global_load_dwordx4 v[24:27], v[8:9], off nt
	global_load_dwordx4 v[12:15], v[10:11], off nt
	v_lshl_add_u64 v[8:9], v[10:11], 0, s[12:13]
	v_lshl_add_u64 v[10:11], v[8:9], 0, s[12:13]
	global_load_dwordx4 v[52:55], v[8:9], off nt
	global_load_dwordx4 v[36:39], v[10:11], off nt
	v_lshl_add_u64 v[8:9], v[10:11], 0, s[12:13]
	global_load_dwordx4 v[48:51], v[8:9], off nt
	v_lshl_add_u64 v[8:9], v[8:9], 0, s[12:13]
	global_load_dwordx4 v[44:47], v[8:9], off nt
	v_lshl_add_u64 v[8:9], v[8:9], 0, s[12:13]
	global_load_dwordx4 v[56:59], v[8:9], off nt
	v_lshl_add_u64 v[8:9], v[8:9], 0, s[12:13]
	global_load_dwordx4 v[32:35], v[8:9], off nt
	v_lshl_add_u64 v[8:9], v[8:9], 0, s[12:13]
	global_load_dwordx4 v[40:43], v[8:9], off nt
	v_lshl_add_u64 v[8:9], v[8:9], 0, s[12:13]
	global_load_dwordx4 v[20:23], v[8:9], off nt
	v_lshl_add_u64 v[8:9], v[8:9], 0, s[12:13]
	v_lshl_add_u64 v[70:71], v[8:9], 0, s[12:13]
	global_load_dwordx4 v[28:31], v[8:9], off nt
	s_nop 0
	global_load_dwordx4 v[8:11], v[70:71], off nt
	global_load_dwordx4 v[60:63], v[68:69], off nt
	global_load_dwordx4 v[16:19], v[66:67], off nt
	v_lshl_add_u32 v69, v75, 8, s9
	v_lshlrev_b32_e32 v70, 2, v75
	v_add3_u32 v78, v69, v70, v72
	v_bitop3_b32 v70, v64, v75, 1 bitop3:0x36
	v_lshl_add_u32 v79, v70, 2, v69
	v_bitop3_b32 v70, v64, v75, 2 bitop3:0x36
	v_lshl_add_u32 v80, v70, 2, v69
	v_bitop3_b32 v70, v64, v75, 3 bitop3:0x36
	v_lshl_add_u32 v81, v70, 2, v69
	v_or_b32_e32 v69, 4, v75
	v_lshl_add_u32 v70, v69, 8, s9
	v_bitop3_b32 v71, v75, v64, 4 bitop3:0x36
	v_lshl_add_u32 v82, v71, 2, v70
	v_bitop3_b32 v71, v64, v69, 1 bitop3:0x36
	v_lshl_add_u32 v83, v71, 2, v70
	v_bitop3_b32 v71, v64, v69, 2 bitop3:0x36
	v_bitop3_b32 v69, v64, v69, 3 bitop3:0x36
	v_lshl_add_u32 v85, v69, 2, v70
	v_or_b32_e32 v69, 8, v75
	v_lshl_add_u32 v84, v71, 2, v70
	v_lshl_add_u32 v70, v69, 8, s9
	v_bitop3_b32 v71, v75, v64, 8 bitop3:0x36
	v_lshl_add_u32 v86, v71, 2, v70
	v_bitop3_b32 v71, v64, v69, 1 bitop3:0x36
	v_lshl_add_u32 v87, v71, 2, v70
	v_bitop3_b32 v71, v64, v69, 2 bitop3:0x36
	v_bitop3_b32 v69, v64, v69, 3 bitop3:0x36
	v_lshl_add_u32 v89, v69, 2, v70
	v_or_b32_e32 v69, 12, v75
	v_lshl_add_u32 v88, v71, 2, v70
	v_lshl_add_u32 v70, v69, 8, s9
	v_bitop3_b32 v71, v75, v64, 12 bitop3:0x36
	v_lshl_add_u32 v90, v71, 2, v70
	v_bitop3_b32 v71, v64, v69, 1 bitop3:0x36
	v_lshl_add_u32 v91, v71, 2, v70
	v_bitop3_b32 v71, v64, v69, 2 bitop3:0x36
	v_bitop3_b32 v69, v64, v69, 3 bitop3:0x36
	v_lshl_add_u32 v93, v69, 2, v70
	v_or_b32_e32 v69, 16, v75
	v_lshl_add_u32 v92, v71, 2, v70
	v_lshl_add_u32 v70, v69, 8, s9
	v_bitop3_b32 v71, v75, v64, 16 bitop3:0x36
	v_lshl_add_u32 v94, v71, 2, v70
	v_bitop3_b32 v71, v64, v69, 1 bitop3:0x36
	v_lshl_add_u32 v95, v71, 2, v70
	v_bitop3_b32 v71, v64, v69, 2 bitop3:0x36
	v_bitop3_b32 v69, v64, v69, 3 bitop3:0x36
	v_lshl_add_u32 v97, v69, 2, v70
	v_or_b32_e32 v69, 20, v75
	v_lshl_add_u32 v96, v71, 2, v70
	v_lshl_add_u32 v70, v69, 8, s9
	v_bitop3_b32 v71, v75, v64, 20 bitop3:0x36
	v_lshl_add_u32 v98, v71, 2, v70
	v_bitop3_b32 v71, v64, v69, 1 bitop3:0x36
	v_lshl_add_u32 v99, v71, 2, v70
	v_bitop3_b32 v71, v64, v69, 2 bitop3:0x36
	v_bitop3_b32 v69, v64, v69, 3 bitop3:0x36
	v_lshl_add_u32 v101, v69, 2, v70
	v_or_b32_e32 v69, 24, v75
	v_lshl_add_u32 v100, v71, 2, v70
	v_lshl_add_u32 v70, v69, 8, s9
	v_bitop3_b32 v71, v75, v64, 24 bitop3:0x36
	v_lshl_add_u32 v102, v71, 2, v70
	v_bitop3_b32 v71, v64, v69, 1 bitop3:0x36
	v_lshl_add_u32 v103, v71, 2, v70
	v_bitop3_b32 v71, v64, v69, 2 bitop3:0x36
	v_bitop3_b32 v69, v64, v69, 3 bitop3:0x36
	v_lshl_add_u32 v105, v69, 2, v70
	v_or_b32_e32 v69, 28, v75
	v_lshl_add_u32 v104, v71, 2, v70
	v_lshl_add_u32 v70, v69, 8, s9
	v_bitop3_b32 v71, v75, v64, 28 bitop3:0x36
	v_lshl_add_u32 v106, v71, 2, v70
	v_bitop3_b32 v71, v64, v69, 1 bitop3:0x36
	v_lshl_add_u32 v107, v71, 2, v70
	v_bitop3_b32 v71, v64, v69, 2 bitop3:0x36
	v_bitop3_b32 v69, v64, v69, 3 bitop3:0x36
	v_lshl_add_u32 v109, v69, 2, v70
	v_or_b32_e32 v69, 36, v75
	v_or_b32_e32 v66, 1, v64
	v_lshl_add_u32 v108, v71, 2, v70
	v_lshl_add_u32 v70, v69, 8, s9
	v_bitop3_b32 v71, v69, v64, 7 bitop3:0x6c
	v_or_b32_e32 v67, 2, v64
	v_or_b32_e32 v68, 3, v64
	v_lshl_add_u32 v110, v71, 2, v70
	v_bitop3_b32 v71, v69, v66, 7 bitop3:0x6c
	v_lshl_add_u32 v111, v71, 2, v70
	v_bitop3_b32 v71, v69, v67, 7 bitop3:0x6c
	v_bitop3_b32 v69, v69, v68, 7 bitop3:0x6c
	v_lshl_add_u32 v113, v69, 2, v70
	v_or_b32_e32 v69, 40, v75
	v_lshl_add_u32 v112, v71, 2, v70
	v_lshl_add_u32 v70, v69, 8, s9
	v_bitop3_b32 v71, v69, v64, 11 bitop3:0x6c
	v_lshl_add_u32 v114, v71, 2, v70
	v_bitop3_b32 v71, v69, v66, 11 bitop3:0x6c
	v_lshl_add_u32 v115, v71, 2, v70
	v_bitop3_b32 v71, v69, v67, 11 bitop3:0x6c
	v_bitop3_b32 v69, v69, v68, 11 bitop3:0x6c
	v_lshl_add_u32 v117, v69, 2, v70
	v_or_b32_e32 v69, 44, v75
	v_lshl_add_u32 v116, v71, 2, v70
	v_lshl_add_u32 v70, v69, 8, s9
	v_bitop3_b32 v71, v69, v64, 15 bitop3:0x6c
	v_lshl_add_u32 v118, v71, 2, v70
	v_bitop3_b32 v71, v69, v66, 15 bitop3:0x6c
	v_lshl_add_u32 v119, v71, 2, v70
	v_bitop3_b32 v71, v69, v67, 15 bitop3:0x6c
	v_bitop3_b32 v69, v69, v68, 15 bitop3:0x6c
	v_lshl_add_u32 v121, v69, 2, v70
	v_or_b32_e32 v69, 48, v75
	v_lshl_add_u32 v120, v71, 2, v70
	v_lshl_add_u32 v70, v69, 8, s9
	v_bitop3_b32 v71, v69, v64, 19 bitop3:0x6c
	v_lshl_add_u32 v122, v71, 2, v70
	v_bitop3_b32 v71, v69, v66, 19 bitop3:0x6c
	v_lshl_add_u32 v123, v71, 2, v70
	v_bitop3_b32 v71, v69, v67, 19 bitop3:0x6c
	v_bitop3_b32 v69, v69, v68, 19 bitop3:0x6c
	v_lshl_add_u32 v125, v69, 2, v70
	v_or_b32_e32 v69, 52, v75
	v_lshl_add_u32 v124, v71, 2, v70
	v_lshl_add_u32 v70, v69, 8, s9
	v_bitop3_b32 v71, v69, v64, 23 bitop3:0x6c
	v_lshl_add_u32 v126, v71, 2, v70
	v_bitop3_b32 v71, v69, v66, 23 bitop3:0x6c
	v_lshl_add_u32 v127, v71, 2, v70
	v_bitop3_b32 v71, v69, v67, 23 bitop3:0x6c
	v_bitop3_b32 v69, v69, v68, 23 bitop3:0x6c
	v_lshl_add_u32 v129, v69, 2, v70
	v_or_b32_e32 v69, 56, v75
	v_lshl_add_u32 v128, v71, 2, v70
	v_lshl_add_u32 v70, v69, 8, s9
	v_bitop3_b32 v71, v69, v64, 27 bitop3:0x6c
	v_lshl_add_u32 v130, v71, 2, v70
	v_bitop3_b32 v71, v69, v66, 27 bitop3:0x6c
	v_lshl_add_u32 v131, v71, 2, v70
	v_bitop3_b32 v71, v69, v67, 27 bitop3:0x6c
	v_bitop3_b32 v69, v69, v68, 27 bitop3:0x6c
	v_lshl_add_u32 v133, v69, 2, v70
	v_or_b32_e32 v69, 60, v75
	v_lshl_add_u32 v132, v71, 2, v70
	v_lshl_add_u32 v70, v69, 8, s9
	v_bitop3_b32 v66, v69, v66, 31 bitop3:0x6c
	s_add_u32 s30, s22, 0x1a000000
	v_lshl_add_u32 v135, v66, 2, v70
	v_bitop3_b32 v66, v69, v67, 31 bitop3:0x6c
	s_addc_u32 s31, s23, 0
	v_and_b32_e32 v74, 63, v65
	v_lshl_add_u32 v136, v66, 2, v70
	v_bitop3_b32 v66, v69, v68, 31 bitop3:0x6c
	s_add_u32 s36, s22, 0x2000000
	v_lshl_add_u32 v137, v66, 2, v70
	s_addc_u32 s37, s23, 0
	v_lshlrev_b32_e32 v66, 3, v74
	s_add_u32 s38, s22, 0x1a00000
	v_and_b32_e32 v74, 56, v66
	v_bfe_u32 v138, v65, 3, 3
	v_and_b32_e32 v65, 24, v66
	s_addc_u32 s39, s23, 0
	v_lshl_add_u32 v67, v74, 8, s9
	v_lshlrev_b32_e32 v65, 2, v65
	v_lshlrev_b32_e32 v68, 2, v138
	s_add_u32 s40, s22, 0x1800000
	v_add3_u32 v146, v67, v65, v68
	v_or_b32_e32 v65, 1, v74
	v_bitop3_b32 v71, v69, v64, 31 bitop3:0x6c
	s_addc_u32 s41, s23, 0
	v_bitop3_b32 v68, v65, v138, 25 bitop3:0x6c
	v_lshl_add_u32 v69, v65, 8, s9
	s_add_u32 s45, s22, 0x1500000
	v_lshl_add_u32 v147, v68, 2, v69
	v_or_b32_e32 v68, 2, v74
	v_lshl_add_u32 v134, v71, 2, v70
	s_addc_u32 s46, s23, 0
	v_bitop3_b32 v70, v68, v138, 26 bitop3:0x6c
	v_lshl_add_u32 v71, v68, 8, s9
	s_add_u32 s47, s22, 0x1200000
	v_lshl_add_u32 v148, v70, 2, v71
	v_or_b32_e32 v70, 3, v74
	s_addc_u32 s48, s23, 0
	v_bitop3_b32 v72, v70, v138, 27 bitop3:0x6c
	v_lshl_add_u32 v76, v70, 8, s9
	s_add_u32 s49, s22, 0xe00000
	v_lshl_add_u32 v149, v72, 2, v76
	v_or_b32_e32 v72, 4, v74
	s_addc_u32 s50, s23, 0
	v_bitop3_b32 v77, v72, v138, 28 bitop3:0x6c
	v_lshl_add_u32 v205, v72, 8, s9
	s_add_u32 s51, s22, 0x200000
	v_lshl_add_u32 v150, v77, 2, v205
	v_or_b32_e32 v77, 5, v74
	v_or_b32_e32 v207, 6, v74
	v_or_b32_e32 v209, 7, v74
	s_addc_u32 s52, s23, 0
	v_or_b32_e32 v139, 8, v138
	v_or_b32_e32 v140, 16, v138
	v_or_b32_e32 v141, 24, v138
	v_or_b32_e32 v142, 32, v138
	v_or_b32_e32 v143, 40, v138
	v_or_b32_e32 v144, 48, v138
	v_or_b32_e32 v145, 56, v138
	v_lshl_add_u32 v206, v77, 8, s9
	v_lshl_add_u32 v208, v207, 8, s9
	v_lshl_add_u32 v210, v209, 8, s9
	s_lshr_b32 s9, s28, 8
	v_bitop3_b32 v155, v65, v139, 25 bitop3:0x6c
	v_bitop3_b32 v163, v65, v140, 25 bitop3:0x6c
	v_bitop3_b32 v171, v65, v141, 25 bitop3:0x6c
	v_bitop3_b32 v178, v65, v142, 25 bitop3:0x6c
	v_bitop3_b32 v186, v65, v143, 25 bitop3:0x6c
	v_bitop3_b32 v194, v65, v144, 25 bitop3:0x6c
	v_bitop3_b32 v65, v65, v145, 25 bitop3:0x6c
	s_lshl_b32 s53, s20, 3
	s_lshl_b32 s12, s9, 12
	v_lshl_add_u32 v202, v65, 2, v69
	v_bitop3_b32 v65, v68, v145, 26 bitop3:0x6c
	s_add_i32 s13, s21, s12
	s_add_i32 s12, s12, s53
	v_lshl_add_u32 v203, v65, 2, v71
	v_bitop3_b32 v65, v70, v145, 27 bitop3:0x6c
	s_mul_i32 s14, s44, 48
	s_add_i32 s12, s12, s21
	v_bitop3_b32 v158, v72, v139, 28 bitop3:0x6c
	v_bitop3_b32 v166, v72, v140, 28 bitop3:0x6c
	v_bitop3_b32 v174, v72, v141, 28 bitop3:0x6c
	v_bitop3_b32 v181, v72, v142, 28 bitop3:0x6c
	v_bitop3_b32 v189, v72, v143, 28 bitop3:0x6c
	v_bitop3_b32 v197, v72, v144, 28 bitop3:0x6c
	v_lshl_add_u32 v204, v65, 2, v76
	v_bitop3_b32 v65, v72, v145, 28 bitop3:0x6c
	s_sub_i32 s12, s12, s14
	v_bitop3_b32 v151, v77, v138, 29 bitop3:0x6c
	v_lshl_add_u32 v158, v158, 2, v205
	v_bitop3_b32 v159, v77, v139, 29 bitop3:0x6c
	v_lshl_add_u32 v166, v166, 2, v205
	v_bitop3_b32 v167, v77, v140, 29 bitop3:0x6c
	v_lshl_add_u32 v174, v174, 2, v205
	v_bitop3_b32 v175, v77, v141, 29 bitop3:0x6c
	v_lshl_add_u32 v181, v181, 2, v205
	v_bitop3_b32 v182, v77, v142, 29 bitop3:0x6c
	v_lshl_add_u32 v189, v189, 2, v205
	v_bitop3_b32 v190, v77, v143, 29 bitop3:0x6c
	v_lshl_add_u32 v197, v197, 2, v205
	v_bitop3_b32 v198, v77, v144, 29 bitop3:0x6c
	v_lshl_add_u32 v205, v65, 2, v205
	v_bitop3_b32 v65, v77, v145, 29 bitop3:0x6c
	s_sub_i32 s28, s13, s14
	s_add_i32 s54, s12, 0xb400
	s_lshl_b32 s12, s9, 11
	s_add_i32 s13, s13, s53
	v_lshl_add_u32 v151, v151, 2, v206
	v_lshl_add_u32 v159, v159, 2, v206
	v_lshl_add_u32 v167, v167, 2, v206
	v_lshl_add_u32 v175, v175, 2, v206
	v_lshl_add_u32 v182, v182, 2, v206
	v_lshl_add_u32 v190, v190, 2, v206
	v_lshl_add_u32 v198, v198, 2, v206
	v_lshl_add_u32 v206, v65, 2, v206
	v_bitop3_b32 v65, v207, v145, 30 bitop3:0x6c
	s_mul_i32 s15, s44, 24
	s_sub_i32 s13, s13, s14
	s_lshl_b32 s9, s9, 17
	s_mulk_i32 s44, 0x600
	s_add_i32 s21, s21, s12
	v_bitop3_b32 v152, v207, v138, 30 bitop3:0x6c
	v_bitop3_b32 v153, v209, v138, 31 bitop3:0x6c
	v_bitop3_b32 v154, v66, v139, 24 bitop3:0x6c
	v_bitop3_b32 v156, v68, v139, 26 bitop3:0x6c
	v_bitop3_b32 v157, v70, v139, 27 bitop3:0x6c
	v_bitop3_b32 v160, v207, v139, 30 bitop3:0x6c
	v_bitop3_b32 v161, v209, v139, 31 bitop3:0x6c
	v_bitop3_b32 v162, v66, v140, 24 bitop3:0x6c
	v_bitop3_b32 v164, v68, v140, 26 bitop3:0x6c
	v_bitop3_b32 v165, v70, v140, 27 bitop3:0x6c
	v_bitop3_b32 v168, v207, v140, 30 bitop3:0x6c
	v_bitop3_b32 v169, v209, v140, 31 bitop3:0x6c
	v_bitop3_b32 v170, v66, v138, 24 bitop3:0x4e
	v_bitop3_b32 v172, v68, v141, 26 bitop3:0x6c
	v_bitop3_b32 v173, v70, v141, 27 bitop3:0x6c
	v_bitop3_b32 v176, v207, v141, 30 bitop3:0x6c
	v_bitop3_b32 v177, v209, v141, 31 bitop3:0x6c
	v_bitop3_b32 v179, v68, v142, 26 bitop3:0x6c
	v_bitop3_b32 v180, v70, v142, 27 bitop3:0x6c
	v_bitop3_b32 v183, v207, v142, 30 bitop3:0x6c
	v_bitop3_b32 v184, v209, v142, 31 bitop3:0x6c
	v_bitop3_b32 v185, v66, v143, 24 bitop3:0x6c
	v_bitop3_b32 v187, v68, v143, 26 bitop3:0x6c
	v_bitop3_b32 v188, v70, v143, 27 bitop3:0x6c
	v_bitop3_b32 v191, v207, v143, 30 bitop3:0x6c
	v_bitop3_b32 v192, v209, v143, 31 bitop3:0x6c
	v_bitop3_b32 v193, v66, v144, 24 bitop3:0x6c
	v_bitop3_b32 v195, v68, v144, 26 bitop3:0x6c
	v_bitop3_b32 v196, v70, v144, 27 bitop3:0x6c
	v_bitop3_b32 v199, v207, v144, 30 bitop3:0x6c
	v_bitop3_b32 v200, v209, v144, 31 bitop3:0x6c
	v_bitop3_b32 v66, v66, v145, 24 bitop3:0x6c
	v_lshl_add_u32 v207, v65, 2, v208
	v_bitop3_b32 v65, v209, v145, 31 bitop3:0x6c
	s_lshl_b32 s13, s13, 6
	s_sub_i32 s44, s9, s44
	s_sub_i32 s9, s21, s15
	v_lshl_add_u32 v152, v152, 2, v208
	v_lshl_add_u32 v153, v153, 2, v210
	v_lshl_add_u32 v154, v154, 2, v67
	v_lshl_add_u32 v155, v155, 2, v69
	v_lshl_add_u32 v156, v156, 2, v71
	v_lshl_add_u32 v157, v157, 2, v76
	v_lshl_add_u32 v160, v160, 2, v208
	v_lshl_add_u32 v161, v161, 2, v210
	v_lshl_add_u32 v162, v162, 2, v67
	v_lshl_add_u32 v163, v163, 2, v69
	v_lshl_add_u32 v164, v164, 2, v71
	v_lshl_add_u32 v165, v165, 2, v76
	v_lshl_add_u32 v168, v168, 2, v208
	v_lshl_add_u32 v169, v169, 2, v210
	v_lshl_add_u32 v170, v170, 2, v67
	v_lshl_add_u32 v171, v171, 2, v69
	v_lshl_add_u32 v172, v172, 2, v71
	v_lshl_add_u32 v173, v173, 2, v76
	v_lshl_add_u32 v176, v176, 2, v208
	v_lshl_add_u32 v177, v177, 2, v210
	v_lshl_add_u32 v178, v178, 2, v69
	v_lshl_add_u32 v179, v179, 2, v71
	v_lshl_add_u32 v180, v180, 2, v76
	v_lshl_add_u32 v183, v183, 2, v208
	v_lshl_add_u32 v184, v184, 2, v210
	v_lshl_add_u32 v185, v185, 2, v67
	v_lshl_add_u32 v186, v186, 2, v69
	v_lshl_add_u32 v187, v187, 2, v71
	v_lshl_add_u32 v188, v188, 2, v76
	v_lshl_add_u32 v191, v191, 2, v208
	v_lshl_add_u32 v192, v192, 2, v210
	v_lshl_add_u32 v193, v193, 2, v67
	v_lshl_add_u32 v194, v194, 2, v69
	v_lshl_add_u32 v195, v195, 2, v71
	v_lshl_add_u32 v196, v196, 2, v76
	v_lshl_add_u32 v199, v199, 2, v208
	v_lshl_add_u32 v200, v200, 2, v210
	v_lshl_add_u32 v201, v66, 2, v67
	v_lshl_add_u32 v208, v65, 2, v210
	s_sub_i32 s55, s12, s15
	s_add_i32 s56, s13, 0xfffe0000
	s_add_i32 s57, s9, 0xfffff800
	v_lshlrev_b32_e32 v76, 2, v64
	v_lshlrev_b32_e32 v72, 1, v74
	s_branch .LBB0_2229

.LBB0_2911:
	s_lshl_b32 s6, s18, 14
	s_add_i32 s7, s6, 0
	s_lshl_b32 s6, s23, 6
	v_bfe_u32 v75, v65, 4, 2
	v_or_b32_e32 v0, s6, v75
	s_ashr_i32 s13, s6, 31
	s_mul_i32 s13, s14, s13
	v_mul_lo_u32 v2, s15, v0
	v_mad_u64_u32 v[0:1], s[30:31], s14, v0, 0
	v_add3_u32 v1, v1, s13, v2
	v_lshlrev_b32_e32 v2, 2, v65
	v_lshl_add_u64 v[0:1], v[0:1], 2, s[8:9]
	s_ashr_i32 s13, s12, 31
	v_and_b32_e32 v64, 60, v2
	v_lshl_add_u64 v[0:1], s[12:13], 2, v[0:1]
	v_mov_b32_e32 v73, 0
	v_lshlrev_b32_e32 v72, 2, v64
	s_lshl_b64 s[8:9], s[14:15], 4
	s_mov_b32 s17, 0
	v_lshl_add_u64 v[66:67], v[0:1], 0, v[72:73]
	s_mul_i32 s16, s14, 0xf0
	s_sub_u32 s8, 0, s8
	v_lshl_add_u64 v[68:69], v[66:67], 0, s[16:17]
	s_subb_u32 s9, 0, s9
	v_lshl_add_u64 v[8:9], v[68:69], 0, s[8:9]
	v_lshl_add_u64 v[10:11], v[8:9], 0, s[8:9]
	global_load_dwordx4 v[4:7], v[8:9], off nt
	global_load_dwordx4 v[0:3], v[10:11], off nt
	v_lshl_add_u64 v[8:9], v[10:11], 0, s[8:9]
	v_lshl_add_u64 v[10:11], v[8:9], 0, s[8:9]
	global_load_dwordx4 v[24:27], v[8:9], off nt
	global_load_dwordx4 v[12:15], v[10:11], off nt
	v_lshl_add_u64 v[8:9], v[10:11], 0, s[8:9]
	v_lshl_add_u64 v[10:11], v[8:9], 0, s[8:9]
	global_load_dwordx4 v[52:55], v[8:9], off nt
	global_load_dwordx4 v[36:39], v[10:11], off nt
	v_lshl_add_u64 v[8:9], v[10:11], 0, s[8:9]
	global_load_dwordx4 v[48:51], v[8:9], off nt
	v_lshl_add_u64 v[8:9], v[8:9], 0, s[8:9]
	global_load_dwordx4 v[44:47], v[8:9], off nt
	v_lshl_add_u64 v[8:9], v[8:9], 0, s[8:9]
	global_load_dwordx4 v[56:59], v[8:9], off nt
	v_lshl_add_u64 v[8:9], v[8:9], 0, s[8:9]
	global_load_dwordx4 v[32:35], v[8:9], off nt
	v_lshl_add_u64 v[8:9], v[8:9], 0, s[8:9]
	global_load_dwordx4 v[40:43], v[8:9], off nt
	v_lshl_add_u64 v[8:9], v[8:9], 0, s[8:9]
	global_load_dwordx4 v[20:23], v[8:9], off nt
	v_lshl_add_u64 v[8:9], v[8:9], 0, s[8:9]
	v_lshl_add_u64 v[70:71], v[8:9], 0, s[8:9]
	global_load_dwordx4 v[28:31], v[8:9], off nt
	s_nop 0
	global_load_dwordx4 v[8:11], v[70:71], off nt
	global_load_dwordx4 v[60:63], v[68:69], off nt
	global_load_dwordx4 v[16:19], v[66:67], off nt
	v_lshl_add_u32 v69, v75, 8, s7
	v_lshlrev_b32_e32 v70, 2, v75
	v_add3_u32 v78, v69, v70, v72
	v_bitop3_b32 v70, v64, v75, 1 bitop3:0x36
	v_lshl_add_u32 v79, v70, 2, v69
	v_bitop3_b32 v70, v64, v75, 2 bitop3:0x36
	v_lshl_add_u32 v80, v70, 2, v69
	v_bitop3_b32 v70, v64, v75, 3 bitop3:0x36
	v_lshl_add_u32 v81, v70, 2, v69
	v_or_b32_e32 v69, 4, v75
	v_lshl_add_u32 v70, v69, 8, s7
	v_bitop3_b32 v71, v75, v64, 4 bitop3:0x36
	v_lshl_add_u32 v82, v71, 2, v70
	v_bitop3_b32 v71, v64, v69, 1 bitop3:0x36
	v_lshl_add_u32 v83, v71, 2, v70
	v_bitop3_b32 v71, v64, v69, 2 bitop3:0x36
	v_bitop3_b32 v69, v64, v69, 3 bitop3:0x36
	v_lshl_add_u32 v85, v69, 2, v70
	v_or_b32_e32 v69, 8, v75
	v_lshl_add_u32 v84, v71, 2, v70
	v_lshl_add_u32 v70, v69, 8, s7
	v_bitop3_b32 v71, v75, v64, 8 bitop3:0x36
	v_lshl_add_u32 v86, v71, 2, v70
	v_bitop3_b32 v71, v64, v69, 1 bitop3:0x36
	v_lshl_add_u32 v87, v71, 2, v70
	v_bitop3_b32 v71, v64, v69, 2 bitop3:0x36
	v_bitop3_b32 v69, v64, v69, 3 bitop3:0x36
	v_lshl_add_u32 v89, v69, 2, v70
	v_or_b32_e32 v69, 12, v75
	v_lshl_add_u32 v88, v71, 2, v70
	v_lshl_add_u32 v70, v69, 8, s7
	v_bitop3_b32 v71, v75, v64, 12 bitop3:0x36
	v_lshl_add_u32 v90, v71, 2, v70
	v_bitop3_b32 v71, v64, v69, 1 bitop3:0x36
	v_lshl_add_u32 v91, v71, 2, v70
	v_bitop3_b32 v71, v64, v69, 2 bitop3:0x36
	v_bitop3_b32 v69, v64, v69, 3 bitop3:0x36
	v_lshl_add_u32 v93, v69, 2, v70
	v_or_b32_e32 v69, 16, v75
	v_lshl_add_u32 v92, v71, 2, v70
	v_lshl_add_u32 v70, v69, 8, s7
	v_bitop3_b32 v71, v75, v64, 16 bitop3:0x36
	v_lshl_add_u32 v94, v71, 2, v70
	v_bitop3_b32 v71, v64, v69, 1 bitop3:0x36
	v_lshl_add_u32 v95, v71, 2, v70
	v_bitop3_b32 v71, v64, v69, 2 bitop3:0x36
	v_bitop3_b32 v69, v64, v69, 3 bitop3:0x36
	v_lshl_add_u32 v97, v69, 2, v70
	v_or_b32_e32 v69, 20, v75
	v_lshl_add_u32 v96, v71, 2, v70
	v_lshl_add_u32 v70, v69, 8, s7
	v_bitop3_b32 v71, v75, v64, 20 bitop3:0x36
	v_lshl_add_u32 v98, v71, 2, v70
	v_bitop3_b32 v71, v64, v69, 1 bitop3:0x36
	v_lshl_add_u32 v99, v71, 2, v70
	v_bitop3_b32 v71, v64, v69, 2 bitop3:0x36
	v_bitop3_b32 v69, v64, v69, 3 bitop3:0x36
	v_lshl_add_u32 v101, v69, 2, v70
	v_or_b32_e32 v69, 24, v75
	v_lshl_add_u32 v100, v71, 2, v70
	v_lshl_add_u32 v70, v69, 8, s7
	v_bitop3_b32 v71, v75, v64, 24 bitop3:0x36
	v_lshl_add_u32 v102, v71, 2, v70
	v_bitop3_b32 v71, v64, v69, 1 bitop3:0x36
	v_lshl_add_u32 v103, v71, 2, v70
	v_bitop3_b32 v71, v64, v69, 2 bitop3:0x36
	v_bitop3_b32 v69, v64, v69, 3 bitop3:0x36
	v_lshl_add_u32 v105, v69, 2, v70
	v_or_b32_e32 v69, 28, v75
	v_lshl_add_u32 v104, v71, 2, v70
	v_lshl_add_u32 v70, v69, 8, s7
	v_bitop3_b32 v71, v75, v64, 28 bitop3:0x36
	v_lshl_add_u32 v106, v71, 2, v70
	v_bitop3_b32 v71, v64, v69, 1 bitop3:0x36
	v_lshl_add_u32 v107, v71, 2, v70
	v_bitop3_b32 v71, v64, v69, 2 bitop3:0x36
	v_bitop3_b32 v69, v64, v69, 3 bitop3:0x36
	v_lshl_add_u32 v109, v69, 2, v70
	v_or_b32_e32 v69, 36, v75
	v_or_b32_e32 v66, 1, v64
	v_lshl_add_u32 v108, v71, 2, v70
	v_lshl_add_u32 v70, v69, 8, s7
	v_bitop3_b32 v71, v69, v64, 7 bitop3:0x6c
	v_or_b32_e32 v67, 2, v64
	v_or_b32_e32 v68, 3, v64
	v_lshl_add_u32 v110, v71, 2, v70
	v_bitop3_b32 v71, v69, v66, 7 bitop3:0x6c
	v_lshl_add_u32 v111, v71, 2, v70
	v_bitop3_b32 v71, v69, v67, 7 bitop3:0x6c
	v_bitop3_b32 v69, v69, v68, 7 bitop3:0x6c
	v_lshl_add_u32 v113, v69, 2, v70
	v_or_b32_e32 v69, 40, v75
	v_lshl_add_u32 v112, v71, 2, v70
	v_lshl_add_u32 v70, v69, 8, s7
	v_bitop3_b32 v71, v69, v64, 11 bitop3:0x6c
	v_lshl_add_u32 v114, v71, 2, v70
	v_bitop3_b32 v71, v69, v66, 11 bitop3:0x6c
	v_lshl_add_u32 v115, v71, 2, v70
	v_bitop3_b32 v71, v69, v67, 11 bitop3:0x6c
	v_bitop3_b32 v69, v69, v68, 11 bitop3:0x6c
	v_lshl_add_u32 v117, v69, 2, v70
	v_or_b32_e32 v69, 44, v75
	v_lshl_add_u32 v116, v71, 2, v70
	v_lshl_add_u32 v70, v69, 8, s7
	v_bitop3_b32 v71, v69, v64, 15 bitop3:0x6c
	v_lshl_add_u32 v118, v71, 2, v70
	v_bitop3_b32 v71, v69, v66, 15 bitop3:0x6c
	v_lshl_add_u32 v119, v71, 2, v70
	v_bitop3_b32 v71, v69, v67, 15 bitop3:0x6c
	v_bitop3_b32 v69, v69, v68, 15 bitop3:0x6c
	v_lshl_add_u32 v121, v69, 2, v70
	v_or_b32_e32 v69, 48, v75
	v_lshl_add_u32 v120, v71, 2, v70
	v_lshl_add_u32 v70, v69, 8, s7
	v_bitop3_b32 v71, v69, v64, 19 bitop3:0x6c
	v_lshl_add_u32 v122, v71, 2, v70
	v_bitop3_b32 v71, v69, v66, 19 bitop3:0x6c
	v_lshl_add_u32 v123, v71, 2, v70
	v_bitop3_b32 v71, v69, v67, 19 bitop3:0x6c
	v_bitop3_b32 v69, v69, v68, 19 bitop3:0x6c
	v_lshl_add_u32 v125, v69, 2, v70
	v_or_b32_e32 v69, 52, v75
	v_lshl_add_u32 v124, v71, 2, v70
	v_lshl_add_u32 v70, v69, 8, s7
	v_bitop3_b32 v71, v69, v64, 23 bitop3:0x6c
	v_lshl_add_u32 v126, v71, 2, v70
	v_bitop3_b32 v71, v69, v66, 23 bitop3:0x6c
	v_lshl_add_u32 v127, v71, 2, v70
	v_bitop3_b32 v71, v69, v67, 23 bitop3:0x6c
	v_bitop3_b32 v69, v69, v68, 23 bitop3:0x6c
	v_lshl_add_u32 v129, v69, 2, v70
	v_or_b32_e32 v69, 56, v75
	v_lshl_add_u32 v128, v71, 2, v70
	v_lshl_add_u32 v70, v69, 8, s7
	v_bitop3_b32 v71, v69, v64, 27 bitop3:0x6c
	v_lshl_add_u32 v130, v71, 2, v70
	v_bitop3_b32 v71, v69, v66, 27 bitop3:0x6c
	v_lshl_add_u32 v131, v71, 2, v70
	v_bitop3_b32 v71, v69, v67, 27 bitop3:0x6c
	v_bitop3_b32 v69, v69, v68, 27 bitop3:0x6c
	v_lshl_add_u32 v133, v69, 2, v70
	v_or_b32_e32 v69, 60, v75
	v_lshl_add_u32 v132, v71, 2, v70
	v_lshl_add_u32 v70, v69, 8, s7
	v_bitop3_b32 v66, v69, v66, 31 bitop3:0x6c
	v_lshl_add_u32 v135, v66, 2, v70
	v_bitop3_b32 v66, v69, v67, 31 bitop3:0x6c
	v_and_b32_e32 v74, 63, v65
	v_lshl_add_u32 v136, v66, 2, v70
	v_bitop3_b32 v66, v69, v68, 31 bitop3:0x6c
	s_add_u32 s27, s21, 0x1a000000
	v_lshl_add_u32 v137, v66, 2, v70
	s_addc_u32 s30, s22, 0
	v_lshlrev_b32_e32 v66, 3, v74
	s_add_u32 s31, s21, 0x2000000
	v_and_b32_e32 v74, 56, v66
	v_bfe_u32 v138, v65, 3, 3
	v_and_b32_e32 v65, 24, v66
	s_addc_u32 s36, s22, 0
	v_lshl_add_u32 v67, v74, 8, s7
	v_lshlrev_b32_e32 v65, 2, v65
	v_lshlrev_b32_e32 v68, 2, v138
	s_add_u32 s37, s21, 0x1a00000
	v_add3_u32 v146, v67, v65, v68
	v_or_b32_e32 v65, 1, v74
	v_bitop3_b32 v71, v69, v64, 31 bitop3:0x6c
	s_addc_u32 s38, s22, 0
	v_bitop3_b32 v68, v65, v138, 25 bitop3:0x6c
	v_lshl_add_u32 v69, v65, 8, s7
	s_add_u32 s39, s21, 0x1800000
	v_lshl_add_u32 v147, v68, 2, v69
	v_or_b32_e32 v68, 2, v74
	v_lshl_add_u32 v134, v71, 2, v70
	s_addc_u32 s40, s22, 0
	v_bitop3_b32 v70, v68, v138, 26 bitop3:0x6c
	v_lshl_add_u32 v71, v68, 8, s7
	s_add_u32 s41, s21, 0x1500000
	v_or_b32_e32 v139, 8, v138
	v_or_b32_e32 v140, 16, v138
	v_or_b32_e32 v141, 24, v138
	v_or_b32_e32 v142, 32, v138
	v_or_b32_e32 v143, 40, v138
	v_or_b32_e32 v144, 48, v138
	v_or_b32_e32 v145, 56, v138
	v_lshl_add_u32 v148, v70, 2, v71
	v_or_b32_e32 v70, 3, v74
	s_addc_u32 s45, s22, 0
	v_bitop3_b32 v72, v70, v138, 27 bitop3:0x6c
	v_lshl_add_u32 v76, v70, 8, s7
	v_bitop3_b32 v155, v65, v139, 25 bitop3:0x6c
	v_bitop3_b32 v163, v65, v140, 25 bitop3:0x6c
	v_bitop3_b32 v171, v65, v141, 25 bitop3:0x6c
	v_bitop3_b32 v178, v65, v142, 25 bitop3:0x6c
	v_bitop3_b32 v186, v65, v143, 25 bitop3:0x6c
	v_bitop3_b32 v194, v65, v144, 25 bitop3:0x6c
	v_bitop3_b32 v65, v65, v145, 25 bitop3:0x6c
	s_add_u32 s46, s21, 0x1200000
	v_lshl_add_u32 v149, v72, 2, v76
	v_or_b32_e32 v72, 4, v74
	v_lshl_add_u32 v202, v65, 2, v69
	v_bitop3_b32 v65, v68, v145, 26 bitop3:0x6c
	s_addc_u32 s47, s22, 0
	v_bitop3_b32 v77, v72, v138, 28 bitop3:0x6c
	v_lshl_add_u32 v205, v72, 8, s7
	v_lshl_add_u32 v203, v65, 2, v71
	v_bitop3_b32 v65, v70, v145, 27 bitop3:0x6c
	s_add_u32 s48, s21, 0xe00000
	v_lshl_add_u32 v150, v77, 2, v205
	v_or_b32_e32 v77, 5, v74
	v_bitop3_b32 v158, v72, v139, 28 bitop3:0x6c
	v_bitop3_b32 v166, v72, v140, 28 bitop3:0x6c
	v_bitop3_b32 v174, v72, v141, 28 bitop3:0x6c
	v_bitop3_b32 v181, v72, v142, 28 bitop3:0x6c
	v_bitop3_b32 v189, v72, v143, 28 bitop3:0x6c
	v_bitop3_b32 v197, v72, v144, 28 bitop3:0x6c
	v_lshl_add_u32 v204, v65, 2, v76
	v_bitop3_b32 v65, v72, v145, 28 bitop3:0x6c
	s_addc_u32 s49, s22, 0
	v_bitop3_b32 v151, v77, v138, 29 bitop3:0x6c
	v_lshl_add_u32 v206, v77, 8, s7
	v_or_b32_e32 v207, 6, v74
	v_lshl_add_u32 v158, v158, 2, v205
	v_bitop3_b32 v159, v77, v139, 29 bitop3:0x6c
	v_lshl_add_u32 v166, v166, 2, v205
	v_bitop3_b32 v167, v77, v140, 29 bitop3:0x6c
	v_lshl_add_u32 v174, v174, 2, v205
	v_bitop3_b32 v175, v77, v141, 29 bitop3:0x6c
	v_lshl_add_u32 v181, v181, 2, v205
	v_bitop3_b32 v182, v77, v142, 29 bitop3:0x6c
	v_lshl_add_u32 v189, v189, 2, v205
	v_bitop3_b32 v190, v77, v143, 29 bitop3:0x6c
	v_lshl_add_u32 v197, v197, 2, v205
	v_bitop3_b32 v198, v77, v144, 29 bitop3:0x6c
	v_lshl_add_u32 v205, v65, 2, v205
	v_bitop3_b32 v65, v77, v145, 29 bitop3:0x6c
	s_add_u32 s50, s21, 0x200000
	v_lshl_add_u32 v151, v151, 2, v206
	v_lshl_add_u32 v208, v207, 8, s7
	v_or_b32_e32 v209, 7, v74
	v_lshl_add_u32 v159, v159, 2, v206
	v_lshl_add_u32 v167, v167, 2, v206
	v_lshl_add_u32 v175, v175, 2, v206
	v_lshl_add_u32 v182, v182, 2, v206
	v_lshl_add_u32 v190, v190, 2, v206
	v_lshl_add_u32 v198, v198, 2, v206
	v_lshl_add_u32 v206, v65, 2, v206
	v_bitop3_b32 v65, v207, v145, 30 bitop3:0x6c
	s_addc_u32 s51, s22, 0
	v_bitop3_b32 v152, v207, v138, 30 bitop3:0x6c
	v_bitop3_b32 v153, v209, v138, 31 bitop3:0x6c
	v_lshl_add_u32 v210, v209, 8, s7
	v_bitop3_b32 v154, v66, v139, 24 bitop3:0x6c
	v_bitop3_b32 v156, v68, v139, 26 bitop3:0x6c
	v_bitop3_b32 v157, v70, v139, 27 bitop3:0x6c
	v_bitop3_b32 v160, v207, v139, 30 bitop3:0x6c
	v_bitop3_b32 v161, v209, v139, 31 bitop3:0x6c
	v_bitop3_b32 v162, v66, v140, 24 bitop3:0x6c
	v_bitop3_b32 v164, v68, v140, 26 bitop3:0x6c
	v_bitop3_b32 v165, v70, v140, 27 bitop3:0x6c
	v_bitop3_b32 v168, v207, v140, 30 bitop3:0x6c
	v_bitop3_b32 v169, v209, v140, 31 bitop3:0x6c
	v_bitop3_b32 v170, v66, v138, 24 bitop3:0x4e
	v_bitop3_b32 v172, v68, v141, 26 bitop3:0x6c
	v_bitop3_b32 v173, v70, v141, 27 bitop3:0x6c
	v_bitop3_b32 v176, v207, v141, 30 bitop3:0x6c
	v_bitop3_b32 v177, v209, v141, 31 bitop3:0x6c
	v_bitop3_b32 v179, v68, v142, 26 bitop3:0x6c
	v_bitop3_b32 v180, v70, v142, 27 bitop3:0x6c
	v_bitop3_b32 v183, v207, v142, 30 bitop3:0x6c
	v_bitop3_b32 v184, v209, v142, 31 bitop3:0x6c
	v_bitop3_b32 v185, v66, v143, 24 bitop3:0x6c
	v_bitop3_b32 v187, v68, v143, 26 bitop3:0x6c
	v_bitop3_b32 v188, v70, v143, 27 bitop3:0x6c
	v_bitop3_b32 v191, v207, v143, 30 bitop3:0x6c
	v_bitop3_b32 v192, v209, v143, 31 bitop3:0x6c
	v_bitop3_b32 v193, v66, v144, 24 bitop3:0x6c
	v_bitop3_b32 v195, v68, v144, 26 bitop3:0x6c
	v_bitop3_b32 v196, v70, v144, 27 bitop3:0x6c
	v_bitop3_b32 v199, v207, v144, 30 bitop3:0x6c
	v_bitop3_b32 v200, v209, v144, 31 bitop3:0x6c
	v_bitop3_b32 v66, v66, v145, 24 bitop3:0x6c
	v_lshl_add_u32 v207, v65, 2, v208
	v_bitop3_b32 v65, v209, v145, 31 bitop3:0x6c
	s_add_i32 s7, s19, s18
	v_lshl_add_u32 v152, v152, 2, v208
	v_lshl_add_u32 v153, v153, 2, v210
	v_lshl_add_u32 v154, v154, 2, v67
	v_lshl_add_u32 v155, v155, 2, v69
	v_lshl_add_u32 v156, v156, 2, v71
	v_lshl_add_u32 v157, v157, 2, v76
	v_lshl_add_u32 v160, v160, 2, v208
	v_lshl_add_u32 v161, v161, 2, v210
	v_lshl_add_u32 v162, v162, 2, v67
	v_lshl_add_u32 v163, v163, 2, v69
	v_lshl_add_u32 v164, v164, 2, v71
	v_lshl_add_u32 v165, v165, 2, v76
	v_lshl_add_u32 v168, v168, 2, v208
	v_lshl_add_u32 v169, v169, 2, v210
	v_lshl_add_u32 v170, v170, 2, v67
	v_lshl_add_u32 v171, v171, 2, v69
	v_lshl_add_u32 v172, v172, 2, v71
	v_lshl_add_u32 v173, v173, 2, v76
	v_lshl_add_u32 v176, v176, 2, v208
	v_lshl_add_u32 v177, v177, 2, v210
	v_lshl_add_u32 v178, v178, 2, v69
	v_lshl_add_u32 v179, v179, 2, v71
	v_lshl_add_u32 v180, v180, 2, v76
	v_lshl_add_u32 v183, v183, 2, v208
	v_lshl_add_u32 v184, v184, 2, v210
	v_lshl_add_u32 v185, v185, 2, v67
	v_lshl_add_u32 v186, v186, 2, v69
	v_lshl_add_u32 v187, v187, 2, v71
	v_lshl_add_u32 v188, v188, 2, v76
	v_lshl_add_u32 v191, v191, 2, v208
	v_lshl_add_u32 v192, v192, 2, v210
	v_lshl_add_u32 v193, v193, 2, v67
	v_lshl_add_u32 v194, v194, 2, v69
	v_lshl_add_u32 v195, v195, 2, v71
	v_lshl_add_u32 v196, v196, 2, v76
	v_lshl_add_u32 v199, v199, 2, v208
	v_lshl_add_u32 v200, v200, 2, v210
	v_lshl_add_u32 v201, v66, 2, v67
	v_lshl_add_u32 v208, v65, 2, v210
	s_add_i32 s52, s7, 0xd000
	s_lshl_b32 s53, s20, 6
	v_lshlrev_b32_e32 v76, 2, v64
	v_lshlrev_b32_e32 v72, 1, v74
	s_branch .LBB0_2917

.LBB0_3120:
	s_lshl_b32 s8, s15, 14
	s_add_i32 s9, s8, 0
	s_lshl_b32 s8, s25, 6
	v_bfe_u32 v75, v65, 4, 2
	v_or_b32_e32 v0, s8, v75
	s_ashr_i32 s15, s8, 31
	s_mul_i32 s15, s16, s15
	v_mul_lo_u32 v2, s17, v0
	v_mad_u64_u32 v[0:1], s[24:25], s16, v0, 0
	v_add3_u32 v1, v1, s15, v2
	v_lshlrev_b32_e32 v2, 2, v65
	v_lshl_add_u64 v[0:1], v[0:1], 2, s[12:13]
	s_ashr_i32 s15, s14, 31
	v_and_b32_e32 v64, 60, v2
	v_lshl_add_u64 v[0:1], s[14:15], 2, v[0:1]
	v_mov_b32_e32 v73, 0
	v_lshlrev_b32_e32 v72, 2, v64
	s_lshl_b64 s[12:13], s[16:17], 4
	s_mov_b32 s19, 0
	v_lshl_add_u64 v[66:67], v[0:1], 0, v[72:73]
	s_mul_i32 s18, s16, 0xf0
	s_sub_u32 s12, 0, s12
	v_lshl_add_u64 v[68:69], v[66:67], 0, s[18:19]
	s_subb_u32 s13, 0, s13
	v_lshl_add_u64 v[8:9], v[68:69], 0, s[12:13]
	v_lshl_add_u64 v[10:11], v[8:9], 0, s[12:13]
	global_load_dwordx4 v[4:7], v[8:9], off nt
	global_load_dwordx4 v[0:3], v[10:11], off nt
	v_lshl_add_u64 v[8:9], v[10:11], 0, s[12:13]
	v_lshl_add_u64 v[10:11], v[8:9], 0, s[12:13]
	global_load_dwordx4 v[24:27], v[8:9], off nt
	global_load_dwordx4 v[12:15], v[10:11], off nt
	v_lshl_add_u64 v[8:9], v[10:11], 0, s[12:13]
	v_lshl_add_u64 v[10:11], v[8:9], 0, s[12:13]
	global_load_dwordx4 v[52:55], v[8:9], off nt
	global_load_dwordx4 v[36:39], v[10:11], off nt
	v_lshl_add_u64 v[8:9], v[10:11], 0, s[12:13]
	global_load_dwordx4 v[48:51], v[8:9], off nt
	v_lshl_add_u64 v[8:9], v[8:9], 0, s[12:13]
	global_load_dwordx4 v[44:47], v[8:9], off nt
	v_lshl_add_u64 v[8:9], v[8:9], 0, s[12:13]
	global_load_dwordx4 v[56:59], v[8:9], off nt
	v_lshl_add_u64 v[8:9], v[8:9], 0, s[12:13]
	global_load_dwordx4 v[32:35], v[8:9], off nt
	v_lshl_add_u64 v[8:9], v[8:9], 0, s[12:13]
	global_load_dwordx4 v[40:43], v[8:9], off nt
	v_lshl_add_u64 v[8:9], v[8:9], 0, s[12:13]
	global_load_dwordx4 v[20:23], v[8:9], off nt
	v_lshl_add_u64 v[8:9], v[8:9], 0, s[12:13]
	v_lshl_add_u64 v[70:71], v[8:9], 0, s[12:13]
	global_load_dwordx4 v[28:31], v[8:9], off nt
	s_nop 0
	global_load_dwordx4 v[8:11], v[70:71], off nt
	global_load_dwordx4 v[60:63], v[68:69], off nt
	global_load_dwordx4 v[16:19], v[66:67], off nt
	v_lshl_add_u32 v69, v75, 8, s9
	v_lshlrev_b32_e32 v70, 2, v75
	v_add3_u32 v78, v69, v70, v72
	v_bitop3_b32 v70, v64, v75, 1 bitop3:0x36
	v_lshl_add_u32 v79, v70, 2, v69
	v_bitop3_b32 v70, v64, v75, 2 bitop3:0x36
	v_lshl_add_u32 v80, v70, 2, v69
	v_bitop3_b32 v70, v64, v75, 3 bitop3:0x36
	v_lshl_add_u32 v81, v70, 2, v69
	v_or_b32_e32 v69, 4, v75
	v_lshl_add_u32 v70, v69, 8, s9
	v_bitop3_b32 v71, v75, v64, 4 bitop3:0x36
	v_lshl_add_u32 v82, v71, 2, v70
	v_bitop3_b32 v71, v64, v69, 1 bitop3:0x36
	v_lshl_add_u32 v83, v71, 2, v70
	v_bitop3_b32 v71, v64, v69, 2 bitop3:0x36
	v_bitop3_b32 v69, v64, v69, 3 bitop3:0x36
	v_lshl_add_u32 v85, v69, 2, v70
	v_or_b32_e32 v69, 8, v75
	v_lshl_add_u32 v84, v71, 2, v70
	v_lshl_add_u32 v70, v69, 8, s9
	v_bitop3_b32 v71, v75, v64, 8 bitop3:0x36
	v_lshl_add_u32 v86, v71, 2, v70
	v_bitop3_b32 v71, v64, v69, 1 bitop3:0x36
	v_lshl_add_u32 v87, v71, 2, v70
	v_bitop3_b32 v71, v64, v69, 2 bitop3:0x36
	v_bitop3_b32 v69, v64, v69, 3 bitop3:0x36
	v_lshl_add_u32 v89, v69, 2, v70
	v_or_b32_e32 v69, 12, v75
	v_lshl_add_u32 v88, v71, 2, v70
	v_lshl_add_u32 v70, v69, 8, s9
	v_bitop3_b32 v71, v75, v64, 12 bitop3:0x36
	v_lshl_add_u32 v90, v71, 2, v70
	v_bitop3_b32 v71, v64, v69, 1 bitop3:0x36
	v_lshl_add_u32 v91, v71, 2, v70
	v_bitop3_b32 v71, v64, v69, 2 bitop3:0x36
	v_bitop3_b32 v69, v64, v69, 3 bitop3:0x36
	v_lshl_add_u32 v93, v69, 2, v70
	v_or_b32_e32 v69, 16, v75
	v_lshl_add_u32 v92, v71, 2, v70
	v_lshl_add_u32 v70, v69, 8, s9
	v_bitop3_b32 v71, v75, v64, 16 bitop3:0x36
	v_lshl_add_u32 v94, v71, 2, v70
	v_bitop3_b32 v71, v64, v69, 1 bitop3:0x36
	v_lshl_add_u32 v95, v71, 2, v70
	v_bitop3_b32 v71, v64, v69, 2 bitop3:0x36
	v_bitop3_b32 v69, v64, v69, 3 bitop3:0x36
	v_lshl_add_u32 v97, v69, 2, v70
	v_or_b32_e32 v69, 20, v75
	v_lshl_add_u32 v96, v71, 2, v70
	v_lshl_add_u32 v70, v69, 8, s9
	v_bitop3_b32 v71, v75, v64, 20 bitop3:0x36
	v_lshl_add_u32 v98, v71, 2, v70
	v_bitop3_b32 v71, v64, v69, 1 bitop3:0x36
	v_lshl_add_u32 v99, v71, 2, v70
	v_bitop3_b32 v71, v64, v69, 2 bitop3:0x36
	v_bitop3_b32 v69, v64, v69, 3 bitop3:0x36
	v_lshl_add_u32 v101, v69, 2, v70
	v_or_b32_e32 v69, 24, v75
	v_lshl_add_u32 v100, v71, 2, v70
	v_lshl_add_u32 v70, v69, 8, s9
	v_bitop3_b32 v71, v75, v64, 24 bitop3:0x36
	v_lshl_add_u32 v102, v71, 2, v70
	v_bitop3_b32 v71, v64, v69, 1 bitop3:0x36
	v_lshl_add_u32 v103, v71, 2, v70
	v_bitop3_b32 v71, v64, v69, 2 bitop3:0x36
	v_bitop3_b32 v69, v64, v69, 3 bitop3:0x36
	v_lshl_add_u32 v105, v69, 2, v70
	v_or_b32_e32 v69, 28, v75
	v_lshl_add_u32 v104, v71, 2, v70
	v_lshl_add_u32 v70, v69, 8, s9
	v_bitop3_b32 v71, v75, v64, 28 bitop3:0x36
	v_lshl_add_u32 v106, v71, 2, v70
	v_bitop3_b32 v71, v64, v69, 1 bitop3:0x36
	v_lshl_add_u32 v107, v71, 2, v70
	v_bitop3_b32 v71, v64, v69, 2 bitop3:0x36
	v_bitop3_b32 v69, v64, v69, 3 bitop3:0x36
	v_lshl_add_u32 v109, v69, 2, v70
	v_or_b32_e32 v69, 36, v75
	v_or_b32_e32 v66, 1, v64
	v_lshl_add_u32 v108, v71, 2, v70
	v_lshl_add_u32 v70, v69, 8, s9
	v_bitop3_b32 v71, v69, v64, 7 bitop3:0x6c
	v_or_b32_e32 v67, 2, v64
	v_or_b32_e32 v68, 3, v64
	v_lshl_add_u32 v110, v71, 2, v70
	v_bitop3_b32 v71, v69, v66, 7 bitop3:0x6c
	v_lshl_add_u32 v111, v71, 2, v70
	v_bitop3_b32 v71, v69, v67, 7 bitop3:0x6c
	v_bitop3_b32 v69, v69, v68, 7 bitop3:0x6c
	v_lshl_add_u32 v113, v69, 2, v70
	v_or_b32_e32 v69, 40, v75
	v_lshl_add_u32 v112, v71, 2, v70
	v_lshl_add_u32 v70, v69, 8, s9
	v_bitop3_b32 v71, v69, v64, 11 bitop3:0x6c
	v_lshl_add_u32 v114, v71, 2, v70
	v_bitop3_b32 v71, v69, v66, 11 bitop3:0x6c
	v_lshl_add_u32 v115, v71, 2, v70
	v_bitop3_b32 v71, v69, v67, 11 bitop3:0x6c
	v_bitop3_b32 v69, v69, v68, 11 bitop3:0x6c
	v_lshl_add_u32 v117, v69, 2, v70
	v_or_b32_e32 v69, 44, v75
	v_lshl_add_u32 v116, v71, 2, v70
	v_lshl_add_u32 v70, v69, 8, s9
	v_bitop3_b32 v71, v69, v64, 15 bitop3:0x6c
	v_lshl_add_u32 v118, v71, 2, v70
	v_bitop3_b32 v71, v69, v66, 15 bitop3:0x6c
	v_lshl_add_u32 v119, v71, 2, v70
	v_bitop3_b32 v71, v69, v67, 15 bitop3:0x6c
	v_bitop3_b32 v69, v69, v68, 15 bitop3:0x6c
	v_lshl_add_u32 v121, v69, 2, v70
	v_or_b32_e32 v69, 48, v75
	v_lshl_add_u32 v120, v71, 2, v70
	v_lshl_add_u32 v70, v69, 8, s9
	v_bitop3_b32 v71, v69, v64, 19 bitop3:0x6c
	v_lshl_add_u32 v122, v71, 2, v70
	v_bitop3_b32 v71, v69, v66, 19 bitop3:0x6c
	v_lshl_add_u32 v123, v71, 2, v70
	v_bitop3_b32 v71, v69, v67, 19 bitop3:0x6c
	v_bitop3_b32 v69, v69, v68, 19 bitop3:0x6c
	v_lshl_add_u32 v125, v69, 2, v70
	v_or_b32_e32 v69, 52, v75
	v_lshl_add_u32 v124, v71, 2, v70
	v_lshl_add_u32 v70, v69, 8, s9
	v_bitop3_b32 v71, v69, v64, 23 bitop3:0x6c
	v_lshl_add_u32 v126, v71, 2, v70
	v_bitop3_b32 v71, v69, v66, 23 bitop3:0x6c
	v_lshl_add_u32 v127, v71, 2, v70
	v_bitop3_b32 v71, v69, v67, 23 bitop3:0x6c
	v_bitop3_b32 v69, v69, v68, 23 bitop3:0x6c
	v_lshl_add_u32 v129, v69, 2, v70
	v_or_b32_e32 v69, 56, v75
	v_lshl_add_u32 v128, v71, 2, v70
	v_lshl_add_u32 v70, v69, 8, s9
	v_bitop3_b32 v71, v69, v64, 27 bitop3:0x6c
	v_lshl_add_u32 v130, v71, 2, v70
	v_bitop3_b32 v71, v69, v66, 27 bitop3:0x6c
	v_lshl_add_u32 v131, v71, 2, v70
	v_bitop3_b32 v71, v69, v67, 27 bitop3:0x6c
	v_bitop3_b32 v69, v69, v68, 27 bitop3:0x6c
	v_lshl_add_u32 v133, v69, 2, v70
	v_or_b32_e32 v69, 60, v75
	v_lshl_add_u32 v132, v71, 2, v70
	v_lshl_add_u32 v70, v69, 8, s9
	v_bitop3_b32 v66, v69, v66, 31 bitop3:0x6c
	v_lshl_add_u32 v135, v66, 2, v70
	v_bitop3_b32 v66, v69, v67, 31 bitop3:0x6c
	v_and_b32_e32 v74, 63, v65
	v_lshl_add_u32 v136, v66, 2, v70
	v_bitop3_b32 v66, v69, v68, 31 bitop3:0x6c
	s_add_u32 s37, s22, 0x1a000000
	v_lshl_add_u32 v137, v66, 2, v70
	s_addc_u32 s38, s23, 0
	v_lshlrev_b32_e32 v66, 3, v74
	s_add_u32 s39, s22, 0x2000000
	v_and_b32_e32 v74, 56, v66
	v_bfe_u32 v138, v65, 3, 3
	v_and_b32_e32 v65, 24, v66
	s_addc_u32 s40, s23, 0
	v_lshl_add_u32 v67, v74, 8, s9
	v_lshlrev_b32_e32 v65, 2, v65
	v_lshlrev_b32_e32 v68, 2, v138
	s_add_u32 s41, s22, 0x1a00000
	v_add3_u32 v146, v67, v65, v68
	v_or_b32_e32 v65, 1, v74
	v_bitop3_b32 v71, v69, v64, 31 bitop3:0x6c
	s_addc_u32 s45, s23, 0
	v_bitop3_b32 v68, v65, v138, 25 bitop3:0x6c
	v_lshl_add_u32 v69, v65, 8, s9
	s_add_u32 s46, s22, 0x1800000
	v_lshl_add_u32 v147, v68, 2, v69
	v_or_b32_e32 v68, 2, v74
	v_lshl_add_u32 v134, v71, 2, v70
	s_addc_u32 s47, s23, 0
	v_bitop3_b32 v70, v68, v138, 26 bitop3:0x6c
	v_lshl_add_u32 v71, v68, 8, s9
	s_add_u32 s48, s22, 0x1500000
	v_or_b32_e32 v139, 8, v138
	v_or_b32_e32 v140, 16, v138
	v_or_b32_e32 v141, 24, v138
	v_or_b32_e32 v142, 32, v138
	v_or_b32_e32 v143, 40, v138
	v_or_b32_e32 v144, 48, v138
	v_or_b32_e32 v145, 56, v138
	v_lshl_add_u32 v148, v70, 2, v71
	v_or_b32_e32 v70, 3, v74
	s_addc_u32 s49, s23, 0
	v_bitop3_b32 v72, v70, v138, 27 bitop3:0x6c
	v_lshl_add_u32 v76, v70, 8, s9
	v_bitop3_b32 v155, v65, v139, 25 bitop3:0x6c
	v_bitop3_b32 v163, v65, v140, 25 bitop3:0x6c
	v_bitop3_b32 v171, v65, v141, 25 bitop3:0x6c
	v_bitop3_b32 v178, v65, v142, 25 bitop3:0x6c
	v_bitop3_b32 v186, v65, v143, 25 bitop3:0x6c
	v_bitop3_b32 v194, v65, v144, 25 bitop3:0x6c
	v_bitop3_b32 v65, v65, v145, 25 bitop3:0x6c
	s_add_u32 s50, s22, 0x1200000
	v_lshl_add_u32 v149, v72, 2, v76
	v_or_b32_e32 v72, 4, v74
	v_lshl_add_u32 v202, v65, 2, v69
	v_bitop3_b32 v65, v68, v145, 26 bitop3:0x6c
	s_addc_u32 s51, s23, 0
	v_bitop3_b32 v77, v72, v138, 28 bitop3:0x6c
	v_lshl_add_u32 v205, v72, 8, s9
	v_lshl_add_u32 v203, v65, 2, v71
	v_bitop3_b32 v65, v70, v145, 27 bitop3:0x6c
	s_add_u32 s52, s22, 0xe00000
	v_lshl_add_u32 v150, v77, 2, v205
	v_or_b32_e32 v77, 5, v74
	v_bitop3_b32 v158, v72, v139, 28 bitop3:0x6c
	v_bitop3_b32 v166, v72, v140, 28 bitop3:0x6c
	v_bitop3_b32 v174, v72, v141, 28 bitop3:0x6c
	v_bitop3_b32 v181, v72, v142, 28 bitop3:0x6c
	v_bitop3_b32 v189, v72, v143, 28 bitop3:0x6c
	v_bitop3_b32 v197, v72, v144, 28 bitop3:0x6c
	v_lshl_add_u32 v204, v65, 2, v76
	v_bitop3_b32 v65, v72, v145, 28 bitop3:0x6c
	s_addc_u32 s53, s23, 0
	v_bitop3_b32 v151, v77, v138, 29 bitop3:0x6c
	v_lshl_add_u32 v206, v77, 8, s9
	v_or_b32_e32 v207, 6, v74
	v_lshl_add_u32 v158, v158, 2, v205
	v_bitop3_b32 v159, v77, v139, 29 bitop3:0x6c
	v_lshl_add_u32 v166, v166, 2, v205
	v_bitop3_b32 v167, v77, v140, 29 bitop3:0x6c
	v_lshl_add_u32 v174, v174, 2, v205
	v_bitop3_b32 v175, v77, v141, 29 bitop3:0x6c
	v_lshl_add_u32 v181, v181, 2, v205
	v_bitop3_b32 v182, v77, v142, 29 bitop3:0x6c
	v_lshl_add_u32 v189, v189, 2, v205
	v_bitop3_b32 v190, v77, v143, 29 bitop3:0x6c
	v_lshl_add_u32 v197, v197, 2, v205
	v_bitop3_b32 v198, v77, v144, 29 bitop3:0x6c
	v_lshl_add_u32 v205, v65, 2, v205
	v_bitop3_b32 v65, v77, v145, 29 bitop3:0x6c
	s_add_u32 s54, s22, 0x200000
	v_lshl_add_u32 v151, v151, 2, v206
	v_lshl_add_u32 v208, v207, 8, s9
	v_or_b32_e32 v209, 7, v74
	v_lshl_add_u32 v159, v159, 2, v206
	v_lshl_add_u32 v167, v167, 2, v206
	v_lshl_add_u32 v175, v175, 2, v206
	v_lshl_add_u32 v182, v182, 2, v206
	v_lshl_add_u32 v190, v190, 2, v206
	v_lshl_add_u32 v198, v198, 2, v206
	v_lshl_add_u32 v206, v65, 2, v206
	v_bitop3_b32 v65, v207, v145, 30 bitop3:0x6c
	s_addc_u32 s55, s23, 0
	v_bitop3_b32 v152, v207, v138, 30 bitop3:0x6c
	v_bitop3_b32 v153, v209, v138, 31 bitop3:0x6c
	v_lshl_add_u32 v210, v209, 8, s9
	v_bitop3_b32 v154, v66, v139, 24 bitop3:0x6c
	v_bitop3_b32 v156, v68, v139, 26 bitop3:0x6c
	v_bitop3_b32 v157, v70, v139, 27 bitop3:0x6c
	v_bitop3_b32 v160, v207, v139, 30 bitop3:0x6c
	v_bitop3_b32 v161, v209, v139, 31 bitop3:0x6c
	v_bitop3_b32 v162, v66, v140, 24 bitop3:0x6c
	v_bitop3_b32 v164, v68, v140, 26 bitop3:0x6c
	v_bitop3_b32 v165, v70, v140, 27 bitop3:0x6c
	v_bitop3_b32 v168, v207, v140, 30 bitop3:0x6c
	v_bitop3_b32 v169, v209, v140, 31 bitop3:0x6c
	v_bitop3_b32 v170, v66, v138, 24 bitop3:0x4e
	v_bitop3_b32 v172, v68, v141, 26 bitop3:0x6c
	v_bitop3_b32 v173, v70, v141, 27 bitop3:0x6c
	v_bitop3_b32 v176, v207, v141, 30 bitop3:0x6c
	v_bitop3_b32 v177, v209, v141, 31 bitop3:0x6c
	v_bitop3_b32 v179, v68, v142, 26 bitop3:0x6c
	v_bitop3_b32 v180, v70, v142, 27 bitop3:0x6c
	v_bitop3_b32 v183, v207, v142, 30 bitop3:0x6c
	v_bitop3_b32 v184, v209, v142, 31 bitop3:0x6c
	v_bitop3_b32 v185, v66, v143, 24 bitop3:0x6c
	v_bitop3_b32 v187, v68, v143, 26 bitop3:0x6c
	v_bitop3_b32 v188, v70, v143, 27 bitop3:0x6c
	v_bitop3_b32 v191, v207, v143, 30 bitop3:0x6c
	v_bitop3_b32 v192, v209, v143, 31 bitop3:0x6c
	v_bitop3_b32 v193, v66, v144, 24 bitop3:0x6c
	v_bitop3_b32 v195, v68, v144, 26 bitop3:0x6c
	v_bitop3_b32 v196, v70, v144, 27 bitop3:0x6c
	v_bitop3_b32 v199, v207, v144, 30 bitop3:0x6c
	v_bitop3_b32 v200, v209, v144, 31 bitop3:0x6c
	v_bitop3_b32 v66, v66, v145, 24 bitop3:0x6c
	v_lshl_add_u32 v207, v65, 2, v208
	v_bitop3_b32 v65, v209, v145, 31 bitop3:0x6c
	s_lshl_b32 s9, s20, 9
	s_lshl_b32 s12, s21, 6
	v_lshl_add_u32 v152, v152, 2, v208
	v_lshl_add_u32 v153, v153, 2, v210
	v_lshl_add_u32 v154, v154, 2, v67
	v_lshl_add_u32 v155, v155, 2, v69
	v_lshl_add_u32 v156, v156, 2, v71
	v_lshl_add_u32 v157, v157, 2, v76
	v_lshl_add_u32 v160, v160, 2, v208
	v_lshl_add_u32 v161, v161, 2, v210
	v_lshl_add_u32 v162, v162, 2, v67
	v_lshl_add_u32 v163, v163, 2, v69
	v_lshl_add_u32 v164, v164, 2, v71
	v_lshl_add_u32 v165, v165, 2, v76
	v_lshl_add_u32 v168, v168, 2, v208
	v_lshl_add_u32 v169, v169, 2, v210
	v_lshl_add_u32 v170, v170, 2, v67
	v_lshl_add_u32 v171, v171, 2, v69
	v_lshl_add_u32 v172, v172, 2, v71
	v_lshl_add_u32 v173, v173, 2, v76
	v_lshl_add_u32 v176, v176, 2, v208
	v_lshl_add_u32 v177, v177, 2, v210
	v_lshl_add_u32 v178, v178, 2, v69
	v_lshl_add_u32 v179, v179, 2, v71
	v_lshl_add_u32 v180, v180, 2, v76
	v_lshl_add_u32 v183, v183, 2, v208
	v_lshl_add_u32 v184, v184, 2, v210
	v_lshl_add_u32 v185, v185, 2, v67
	v_lshl_add_u32 v186, v186, 2, v69
	v_lshl_add_u32 v187, v187, 2, v71
	v_lshl_add_u32 v188, v188, 2, v76
	v_lshl_add_u32 v191, v191, 2, v208
	v_lshl_add_u32 v192, v192, 2, v210
	v_lshl_add_u32 v193, v193, 2, v67
	v_lshl_add_u32 v194, v194, 2, v69
	v_lshl_add_u32 v195, v195, 2, v71
	v_lshl_add_u32 v196, v196, 2, v76
	v_lshl_add_u32 v199, v199, 2, v208
	v_lshl_add_u32 v200, v200, 2, v210
	v_lshl_add_u32 v201, v66, 2, v67
	v_lshl_add_u32 v208, v65, 2, v210
	s_add_i32 s56, s30, 0x10000
	s_add_i32 s57, s9, s12
	v_lshlrev_b32_e32 v76, 2, v64
	v_lshlrev_b32_e32 v72, 1, v74
	s_branch .LBB0_3126

.LBB0_3207:
	s_lshl_b32 s8, s15, 14
	s_add_i32 s9, s8, 0
	s_lshl_b32 s8, s30, 6
	v_bfe_u32 v75, v65, 4, 2
	v_or_b32_e32 v0, s8, v75
	s_ashr_i32 s15, s8, 31
	s_mul_i32 s15, s16, s15
	v_mul_lo_u32 v2, s17, v0
	v_mad_u64_u32 v[0:1], s[24:25], s16, v0, 0
	v_add3_u32 v1, v1, s15, v2
	v_lshlrev_b32_e32 v2, 2, v65
	v_lshl_add_u64 v[0:1], v[0:1], 2, s[12:13]
	s_ashr_i32 s15, s14, 31
	v_and_b32_e32 v64, 60, v2
	s_lshl_b32 s29, s29, 3
	v_lshl_add_u64 v[0:1], s[14:15], 2, v[0:1]
	v_mov_b32_e32 v73, 0
	v_lshlrev_b32_e32 v72, 2, v64
	s_lshl_b64 s[12:13], s[16:17], 4
	s_mov_b32 s19, 0
	v_lshl_add_u64 v[66:67], v[0:1], 0, v[72:73]
	s_mul_i32 s18, s16, 0xf0
	s_sub_u32 s12, 0, s12
	v_lshl_add_u64 v[68:69], v[66:67], 0, s[18:19]
	s_subb_u32 s13, 0, s13
	v_lshl_add_u64 v[8:9], v[68:69], 0, s[12:13]
	v_lshl_add_u64 v[10:11], v[8:9], 0, s[12:13]
	global_load_dwordx4 v[4:7], v[8:9], off nt
	global_load_dwordx4 v[0:3], v[10:11], off nt
	v_lshl_add_u64 v[8:9], v[10:11], 0, s[12:13]
	v_lshl_add_u64 v[10:11], v[8:9], 0, s[12:13]
	global_load_dwordx4 v[24:27], v[8:9], off nt
	global_load_dwordx4 v[12:15], v[10:11], off nt
	v_lshl_add_u64 v[8:9], v[10:11], 0, s[12:13]
	v_lshl_add_u64 v[10:11], v[8:9], 0, s[12:13]
	global_load_dwordx4 v[52:55], v[8:9], off nt
	global_load_dwordx4 v[36:39], v[10:11], off nt
	v_lshl_add_u64 v[8:9], v[10:11], 0, s[12:13]
	global_load_dwordx4 v[48:51], v[8:9], off nt
	v_lshl_add_u64 v[8:9], v[8:9], 0, s[12:13]
	global_load_dwordx4 v[44:47], v[8:9], off nt
	v_lshl_add_u64 v[8:9], v[8:9], 0, s[12:13]
	global_load_dwordx4 v[56:59], v[8:9], off nt
	v_lshl_add_u64 v[8:9], v[8:9], 0, s[12:13]
	global_load_dwordx4 v[32:35], v[8:9], off nt
	v_lshl_add_u64 v[8:9], v[8:9], 0, s[12:13]
	global_load_dwordx4 v[40:43], v[8:9], off nt
	v_lshl_add_u64 v[8:9], v[8:9], 0, s[12:13]
	global_load_dwordx4 v[20:23], v[8:9], off nt
	v_lshl_add_u64 v[8:9], v[8:9], 0, s[12:13]
	v_lshl_add_u64 v[70:71], v[8:9], 0, s[12:13]
	global_load_dwordx4 v[28:31], v[8:9], off nt
	s_nop 0
	global_load_dwordx4 v[8:11], v[70:71], off nt
	global_load_dwordx4 v[60:63], v[68:69], off nt
	global_load_dwordx4 v[16:19], v[66:67], off nt
	v_lshl_add_u32 v69, v75, 8, s9
	v_lshlrev_b32_e32 v70, 2, v75
	v_add3_u32 v78, v69, v70, v72
	v_bitop3_b32 v70, v64, v75, 1 bitop3:0x36
	v_lshl_add_u32 v79, v70, 2, v69
	v_bitop3_b32 v70, v64, v75, 2 bitop3:0x36
	v_lshl_add_u32 v80, v70, 2, v69
	v_bitop3_b32 v70, v64, v75, 3 bitop3:0x36
	v_lshl_add_u32 v81, v70, 2, v69
	v_or_b32_e32 v69, 4, v75
	v_lshl_add_u32 v70, v69, 8, s9
	v_bitop3_b32 v71, v75, v64, 4 bitop3:0x36
	v_lshl_add_u32 v82, v71, 2, v70
	v_bitop3_b32 v71, v64, v69, 1 bitop3:0x36
	v_lshl_add_u32 v83, v71, 2, v70
	v_bitop3_b32 v71, v64, v69, 2 bitop3:0x36
	v_bitop3_b32 v69, v64, v69, 3 bitop3:0x36
	v_lshl_add_u32 v85, v69, 2, v70
	v_or_b32_e32 v69, 8, v75
	v_lshl_add_u32 v84, v71, 2, v70
	v_lshl_add_u32 v70, v69, 8, s9
	v_bitop3_b32 v71, v75, v64, 8 bitop3:0x36
	v_lshl_add_u32 v86, v71, 2, v70
	v_bitop3_b32 v71, v64, v69, 1 bitop3:0x36
	v_lshl_add_u32 v87, v71, 2, v70
	v_bitop3_b32 v71, v64, v69, 2 bitop3:0x36
	v_bitop3_b32 v69, v64, v69, 3 bitop3:0x36
	v_lshl_add_u32 v89, v69, 2, v70
	v_or_b32_e32 v69, 12, v75
	v_lshl_add_u32 v88, v71, 2, v70
	v_lshl_add_u32 v70, v69, 8, s9
	v_bitop3_b32 v71, v75, v64, 12 bitop3:0x36
	v_lshl_add_u32 v90, v71, 2, v70
	v_bitop3_b32 v71, v64, v69, 1 bitop3:0x36
	v_lshl_add_u32 v91, v71, 2, v70
	v_bitop3_b32 v71, v64, v69, 2 bitop3:0x36
	v_bitop3_b32 v69, v64, v69, 3 bitop3:0x36
	v_lshl_add_u32 v93, v69, 2, v70
	v_or_b32_e32 v69, 16, v75
	v_lshl_add_u32 v92, v71, 2, v70
	v_lshl_add_u32 v70, v69, 8, s9
	v_bitop3_b32 v71, v75, v64, 16 bitop3:0x36
	v_lshl_add_u32 v94, v71, 2, v70
	v_bitop3_b32 v71, v64, v69, 1 bitop3:0x36
	v_lshl_add_u32 v95, v71, 2, v70
	v_bitop3_b32 v71, v64, v69, 2 bitop3:0x36
	v_bitop3_b32 v69, v64, v69, 3 bitop3:0x36
	v_lshl_add_u32 v97, v69, 2, v70
	v_or_b32_e32 v69, 20, v75
	v_lshl_add_u32 v96, v71, 2, v70
	v_lshl_add_u32 v70, v69, 8, s9
	v_bitop3_b32 v71, v75, v64, 20 bitop3:0x36
	v_lshl_add_u32 v98, v71, 2, v70
	v_bitop3_b32 v71, v64, v69, 1 bitop3:0x36
	v_lshl_add_u32 v99, v71, 2, v70
	v_bitop3_b32 v71, v64, v69, 2 bitop3:0x36
	v_bitop3_b32 v69, v64, v69, 3 bitop3:0x36
	v_lshl_add_u32 v101, v69, 2, v70
	v_or_b32_e32 v69, 24, v75
	v_lshl_add_u32 v100, v71, 2, v70
	v_lshl_add_u32 v70, v69, 8, s9
	v_bitop3_b32 v71, v75, v64, 24 bitop3:0x36
	v_lshl_add_u32 v102, v71, 2, v70
	v_bitop3_b32 v71, v64, v69, 1 bitop3:0x36
	v_lshl_add_u32 v103, v71, 2, v70
	v_bitop3_b32 v71, v64, v69, 2 bitop3:0x36
	v_bitop3_b32 v69, v64, v69, 3 bitop3:0x36
	v_lshl_add_u32 v105, v69, 2, v70
	v_or_b32_e32 v69, 28, v75
	v_lshl_add_u32 v104, v71, 2, v70
	v_lshl_add_u32 v70, v69, 8, s9
	v_bitop3_b32 v71, v75, v64, 28 bitop3:0x36
	v_lshl_add_u32 v106, v71, 2, v70
	v_bitop3_b32 v71, v64, v69, 1 bitop3:0x36
	v_lshl_add_u32 v107, v71, 2, v70
	v_bitop3_b32 v71, v64, v69, 2 bitop3:0x36
	v_bitop3_b32 v69, v64, v69, 3 bitop3:0x36
	v_lshl_add_u32 v109, v69, 2, v70
	v_or_b32_e32 v69, 36, v75
	v_or_b32_e32 v66, 1, v64
	v_lshl_add_u32 v108, v71, 2, v70
	v_lshl_add_u32 v70, v69, 8, s9
	v_bitop3_b32 v71, v69, v64, 7 bitop3:0x6c
	v_or_b32_e32 v67, 2, v64
	v_or_b32_e32 v68, 3, v64
	v_lshl_add_u32 v110, v71, 2, v70
	v_bitop3_b32 v71, v69, v66, 7 bitop3:0x6c
	v_lshl_add_u32 v111, v71, 2, v70
	v_bitop3_b32 v71, v69, v67, 7 bitop3:0x6c
	v_bitop3_b32 v69, v69, v68, 7 bitop3:0x6c
	v_lshl_add_u32 v113, v69, 2, v70
	v_or_b32_e32 v69, 40, v75
	v_lshl_add_u32 v112, v71, 2, v70
	v_lshl_add_u32 v70, v69, 8, s9
	v_bitop3_b32 v71, v69, v64, 11 bitop3:0x6c
	v_lshl_add_u32 v114, v71, 2, v70
	v_bitop3_b32 v71, v69, v66, 11 bitop3:0x6c
	v_lshl_add_u32 v115, v71, 2, v70
	v_bitop3_b32 v71, v69, v67, 11 bitop3:0x6c
	v_bitop3_b32 v69, v69, v68, 11 bitop3:0x6c
	v_lshl_add_u32 v117, v69, 2, v70
	v_or_b32_e32 v69, 44, v75
	v_lshl_add_u32 v116, v71, 2, v70
	v_lshl_add_u32 v70, v69, 8, s9
	v_bitop3_b32 v71, v69, v64, 15 bitop3:0x6c
	v_lshl_add_u32 v118, v71, 2, v70
	v_bitop3_b32 v71, v69, v66, 15 bitop3:0x6c
	v_lshl_add_u32 v119, v71, 2, v70
	v_bitop3_b32 v71, v69, v67, 15 bitop3:0x6c
	v_bitop3_b32 v69, v69, v68, 15 bitop3:0x6c
	v_lshl_add_u32 v121, v69, 2, v70
	v_or_b32_e32 v69, 48, v75
	v_lshl_add_u32 v120, v71, 2, v70
	v_lshl_add_u32 v70, v69, 8, s9
	v_bitop3_b32 v71, v69, v64, 19 bitop3:0x6c
	v_lshl_add_u32 v122, v71, 2, v70
	v_bitop3_b32 v71, v69, v66, 19 bitop3:0x6c
	v_lshl_add_u32 v123, v71, 2, v70
	v_bitop3_b32 v71, v69, v67, 19 bitop3:0x6c
	v_bitop3_b32 v69, v69, v68, 19 bitop3:0x6c
	v_lshl_add_u32 v125, v69, 2, v70
	v_or_b32_e32 v69, 52, v75
	v_lshl_add_u32 v124, v71, 2, v70
	v_lshl_add_u32 v70, v69, 8, s9
	v_bitop3_b32 v71, v69, v64, 23 bitop3:0x6c
	v_lshl_add_u32 v126, v71, 2, v70
	v_bitop3_b32 v71, v69, v66, 23 bitop3:0x6c
	v_lshl_add_u32 v127, v71, 2, v70
	v_bitop3_b32 v71, v69, v67, 23 bitop3:0x6c
	v_bitop3_b32 v69, v69, v68, 23 bitop3:0x6c
	v_lshl_add_u32 v129, v69, 2, v70
	v_or_b32_e32 v69, 56, v75
	v_lshl_add_u32 v128, v71, 2, v70
	v_lshl_add_u32 v70, v69, 8, s9
	v_bitop3_b32 v71, v69, v64, 27 bitop3:0x6c
	v_lshl_add_u32 v130, v71, 2, v70
	v_bitop3_b32 v71, v69, v66, 27 bitop3:0x6c
	v_lshl_add_u32 v131, v71, 2, v70
	v_bitop3_b32 v71, v69, v67, 27 bitop3:0x6c
	v_bitop3_b32 v69, v69, v68, 27 bitop3:0x6c
	v_lshl_add_u32 v133, v69, 2, v70
	v_or_b32_e32 v69, 60, v75
	v_lshl_add_u32 v132, v71, 2, v70
	v_lshl_add_u32 v70, v69, 8, s9
	v_bitop3_b32 v66, v69, v66, 31 bitop3:0x6c
	s_add_u32 s30, s22, 0x1a000000
	v_lshl_add_u32 v135, v66, 2, v70
	v_bitop3_b32 v66, v69, v67, 31 bitop3:0x6c
	s_addc_u32 s31, s23, 0
	v_and_b32_e32 v74, 63, v65
	v_lshl_add_u32 v136, v66, 2, v70
	v_bitop3_b32 v66, v69, v68, 31 bitop3:0x6c
	s_add_u32 s36, s22, 0x2000000
	v_lshl_add_u32 v137, v66, 2, v70
	s_addc_u32 s37, s23, 0
	v_lshlrev_b32_e32 v66, 3, v74
	s_add_u32 s38, s22, 0x1a00000
	v_and_b32_e32 v74, 56, v66
	v_bfe_u32 v138, v65, 3, 3
	v_and_b32_e32 v65, 24, v66
	s_addc_u32 s39, s23, 0
	v_lshl_add_u32 v67, v74, 8, s9
	v_lshlrev_b32_e32 v65, 2, v65
	v_lshlrev_b32_e32 v68, 2, v138
	s_add_u32 s40, s22, 0x1800000
	v_add3_u32 v146, v67, v65, v68
	v_or_b32_e32 v65, 1, v74
	v_bitop3_b32 v71, v69, v64, 31 bitop3:0x6c
	s_addc_u32 s41, s23, 0
	v_bitop3_b32 v68, v65, v138, 25 bitop3:0x6c
	v_lshl_add_u32 v69, v65, 8, s9
	s_add_u32 s45, s22, 0x1500000
	v_lshl_add_u32 v147, v68, 2, v69
	v_or_b32_e32 v68, 2, v74
	v_lshl_add_u32 v134, v71, 2, v70
	s_addc_u32 s46, s23, 0
	v_bitop3_b32 v70, v68, v138, 26 bitop3:0x6c
	v_lshl_add_u32 v71, v68, 8, s9
	s_add_u32 s47, s22, 0x1200000
	v_lshl_add_u32 v148, v70, 2, v71
	v_or_b32_e32 v70, 3, v74
	s_addc_u32 s48, s23, 0
	v_bitop3_b32 v72, v70, v138, 27 bitop3:0x6c
	v_lshl_add_u32 v76, v70, 8, s9
	s_add_u32 s49, s22, 0xe00000
	v_lshl_add_u32 v149, v72, 2, v76
	v_or_b32_e32 v72, 4, v74
	s_addc_u32 s50, s23, 0
	v_bitop3_b32 v77, v72, v138, 28 bitop3:0x6c
	v_lshl_add_u32 v205, v72, 8, s9
	s_add_u32 s51, s22, 0x200000
	v_lshl_add_u32 v150, v77, 2, v205
	v_or_b32_e32 v77, 5, v74
	v_or_b32_e32 v207, 6, v74
	v_or_b32_e32 v209, 7, v74
	s_addc_u32 s52, s23, 0
	v_lshl_add_u32 v206, v77, 8, s9
	v_lshl_add_u32 v208, v207, 8, s9
	v_lshl_add_u32 v210, v209, 8, s9
	s_lshr_b32 s9, s28, 8
	v_or_b32_e32 v139, 8, v138
	v_or_b32_e32 v140, 16, v138
	v_or_b32_e32 v141, 24, v138
	v_or_b32_e32 v142, 32, v138
	v_or_b32_e32 v143, 40, v138
	v_or_b32_e32 v144, 48, v138
	v_or_b32_e32 v145, 56, v138
	s_lshl_b32 s12, s9, 12
	v_bitop3_b32 v155, v65, v139, 25 bitop3:0x6c
	v_bitop3_b32 v163, v65, v140, 25 bitop3:0x6c
	v_bitop3_b32 v171, v65, v141, 25 bitop3:0x6c
	v_bitop3_b32 v178, v65, v142, 25 bitop3:0x6c
	v_bitop3_b32 v186, v65, v143, 25 bitop3:0x6c
	v_bitop3_b32 v194, v65, v144, 25 bitop3:0x6c
	v_bitop3_b32 v65, v65, v145, 25 bitop3:0x6c
	s_lshl_b32 s53, s20, 3
	s_add_i32 s12, s21, s12
	s_mul_i32 s13, s44, 48
	v_lshl_add_u32 v202, v65, 2, v69
	v_bitop3_b32 v65, v68, v145, 26 bitop3:0x6c
	s_sub_i32 s28, s12, s13
	s_add_i32 s12, s12, s53
	v_lshl_add_u32 v203, v65, 2, v71
	v_bitop3_b32 v65, v70, v145, 27 bitop3:0x6c
	s_sub_i32 s12, s12, s13
	v_bitop3_b32 v158, v72, v139, 28 bitop3:0x6c
	v_bitop3_b32 v166, v72, v140, 28 bitop3:0x6c
	v_bitop3_b32 v174, v72, v141, 28 bitop3:0x6c
	v_bitop3_b32 v181, v72, v142, 28 bitop3:0x6c
	v_bitop3_b32 v189, v72, v143, 28 bitop3:0x6c
	v_bitop3_b32 v197, v72, v144, 28 bitop3:0x6c
	v_lshl_add_u32 v204, v65, 2, v76
	v_bitop3_b32 v65, v72, v145, 28 bitop3:0x6c
	s_add_i32 s54, s12, 0xf000
	s_lshl_b32 s12, s12, 6
	v_bitop3_b32 v151, v77, v138, 29 bitop3:0x6c
	v_lshl_add_u32 v158, v158, 2, v205
	v_bitop3_b32 v159, v77, v139, 29 bitop3:0x6c
	v_lshl_add_u32 v166, v166, 2, v205
	v_bitop3_b32 v167, v77, v140, 29 bitop3:0x6c
	v_lshl_add_u32 v174, v174, 2, v205
	v_bitop3_b32 v175, v77, v141, 29 bitop3:0x6c
	v_lshl_add_u32 v181, v181, 2, v205
	v_bitop3_b32 v182, v77, v142, 29 bitop3:0x6c
	v_lshl_add_u32 v189, v189, 2, v205
	v_bitop3_b32 v190, v77, v143, 29 bitop3:0x6c
	v_lshl_add_u32 v197, v197, 2, v205
	v_bitop3_b32 v198, v77, v144, 29 bitop3:0x6c
	v_lshl_add_u32 v205, v65, 2, v205
	v_bitop3_b32 v65, v77, v145, 29 bitop3:0x6c
	s_add_i32 s55, s12, 0xfffe0000
	s_lshl_b32 s12, s9, 17
	s_lshl_b32 s9, s9, 11
	v_lshl_add_u32 v151, v151, 2, v206
	v_lshl_add_u32 v159, v159, 2, v206
	v_lshl_add_u32 v167, v167, 2, v206
	v_lshl_add_u32 v175, v175, 2, v206
	v_lshl_add_u32 v182, v182, 2, v206
	v_lshl_add_u32 v190, v190, 2, v206
	v_lshl_add_u32 v198, v198, 2, v206
	v_lshl_add_u32 v206, v65, 2, v206
	v_bitop3_b32 v65, v207, v145, 30 bitop3:0x6c
	s_mul_i32 s13, s44, 0x600
	s_add_i32 s21, s21, s9
	s_mul_i32 s44, s44, 24
	v_bitop3_b32 v152, v207, v138, 30 bitop3:0x6c
	v_bitop3_b32 v153, v209, v138, 31 bitop3:0x6c
	v_bitop3_b32 v154, v66, v139, 24 bitop3:0x6c
	v_bitop3_b32 v156, v68, v139, 26 bitop3:0x6c
	v_bitop3_b32 v157, v70, v139, 27 bitop3:0x6c
	v_bitop3_b32 v160, v207, v139, 30 bitop3:0x6c
	v_bitop3_b32 v161, v209, v139, 31 bitop3:0x6c
	v_bitop3_b32 v162, v66, v140, 24 bitop3:0x6c
	v_bitop3_b32 v164, v68, v140, 26 bitop3:0x6c
	v_bitop3_b32 v165, v70, v140, 27 bitop3:0x6c
	v_bitop3_b32 v168, v207, v140, 30 bitop3:0x6c
	v_bitop3_b32 v169, v209, v140, 31 bitop3:0x6c
	v_bitop3_b32 v170, v66, v138, 24 bitop3:0x4e
	v_bitop3_b32 v172, v68, v141, 26 bitop3:0x6c
	v_bitop3_b32 v173, v70, v141, 27 bitop3:0x6c
	v_bitop3_b32 v176, v207, v141, 30 bitop3:0x6c
	v_bitop3_b32 v177, v209, v141, 31 bitop3:0x6c
	v_bitop3_b32 v179, v68, v142, 26 bitop3:0x6c
	v_bitop3_b32 v180, v70, v142, 27 bitop3:0x6c
	v_bitop3_b32 v183, v207, v142, 30 bitop3:0x6c
	v_bitop3_b32 v184, v209, v142, 31 bitop3:0x6c
	v_bitop3_b32 v185, v66, v143, 24 bitop3:0x6c
	v_bitop3_b32 v187, v68, v143, 26 bitop3:0x6c
	v_bitop3_b32 v188, v70, v143, 27 bitop3:0x6c
	v_bitop3_b32 v191, v207, v143, 30 bitop3:0x6c
	v_bitop3_b32 v192, v209, v143, 31 bitop3:0x6c
	v_bitop3_b32 v193, v66, v144, 24 bitop3:0x6c
	v_bitop3_b32 v195, v68, v144, 26 bitop3:0x6c
	v_bitop3_b32 v196, v70, v144, 27 bitop3:0x6c
	v_bitop3_b32 v199, v207, v144, 30 bitop3:0x6c
	v_bitop3_b32 v200, v209, v144, 31 bitop3:0x6c
	v_bitop3_b32 v66, v66, v145, 24 bitop3:0x6c
	v_lshl_add_u32 v207, v65, 2, v208
	v_bitop3_b32 v65, v209, v145, 31 bitop3:0x6c
	s_sub_i32 s9, s21, s44
	v_lshl_add_u32 v152, v152, 2, v208
	v_lshl_add_u32 v153, v153, 2, v210
	v_lshl_add_u32 v154, v154, 2, v67
	v_lshl_add_u32 v155, v155, 2, v69
	v_lshl_add_u32 v156, v156, 2, v71
	v_lshl_add_u32 v157, v157, 2, v76
	v_lshl_add_u32 v160, v160, 2, v208
	v_lshl_add_u32 v161, v161, 2, v210
	v_lshl_add_u32 v162, v162, 2, v67
	v_lshl_add_u32 v163, v163, 2, v69
	v_lshl_add_u32 v164, v164, 2, v71
	v_lshl_add_u32 v165, v165, 2, v76
	v_lshl_add_u32 v168, v168, 2, v208
	v_lshl_add_u32 v169, v169, 2, v210
	v_lshl_add_u32 v170, v170, 2, v67
	v_lshl_add_u32 v171, v171, 2, v69
	v_lshl_add_u32 v172, v172, 2, v71
	v_lshl_add_u32 v173, v173, 2, v76
	v_lshl_add_u32 v176, v176, 2, v208
	v_lshl_add_u32 v177, v177, 2, v210
	v_lshl_add_u32 v178, v178, 2, v69
	v_lshl_add_u32 v179, v179, 2, v71
	v_lshl_add_u32 v180, v180, 2, v76
	v_lshl_add_u32 v183, v183, 2, v208
	v_lshl_add_u32 v184, v184, 2, v210
	v_lshl_add_u32 v185, v185, 2, v67
	v_lshl_add_u32 v186, v186, 2, v69
	v_lshl_add_u32 v187, v187, 2, v71
	v_lshl_add_u32 v188, v188, 2, v76
	v_lshl_add_u32 v191, v191, 2, v208
	v_lshl_add_u32 v192, v192, 2, v210
	v_lshl_add_u32 v193, v193, 2, v67
	v_lshl_add_u32 v194, v194, 2, v69
	v_lshl_add_u32 v195, v195, 2, v71
	v_lshl_add_u32 v196, v196, 2, v76
	v_lshl_add_u32 v199, v199, 2, v208
	v_lshl_add_u32 v200, v200, 2, v210
	v_lshl_add_u32 v201, v66, 2, v67
	v_lshl_add_u32 v208, v65, 2, v210
	s_sub_i32 s56, s12, s13
	s_add_i32 s44, s9, 0xfffff800
	v_lshlrev_b32_e32 v76, 2, v64
	v_lshlrev_b32_e32 v72, 1, v74
	s_branch .LBB0_3213

.LBB0_3209:
	s_lshl_b32 s18, s21, 6
	v_or_b32_e32 v0, s18, v75
	s_ashr_i32 s9, s18, 31
	s_mul_i32 s9, s22, s9
	v_mul_lo_u32 v2, s23, v0
	v_mad_u64_u32 v[0:1], s[58:59], s22, v0, 0
	v_add3_u32 v1, v1, s9, v2
	v_lshl_add_u64 v[0:1], v[0:1], 2, s[16:17]
	s_ashr_i32 s21, s20, 31
	v_lshl_add_u64 v[0:1], s[20:21], 2, v[0:1]
	v_mov_b32_e32 v77, v73
	v_lshl_add_u64 v[0:1], v[0:1], 0, v[76:77]
	s_lshl_b64 s[16:17], s[22:23], 4
	v_lshl_add_u64 v[2:3], v[0:1], 0, s[16:17]
	global_load_dwordx4 v[16:19], v[0:1], off nt
	global_load_dwordx4 v[8:11], v[2:3], off nt
	v_lshl_add_u64 v[0:1], v[2:3], 0, s[16:17]
	v_lshl_add_u64 v[2:3], v[0:1], 0, s[16:17]
	global_load_dwordx4 v[28:31], v[0:1], off nt
	global_load_dwordx4 v[20:23], v[2:3], off nt
	v_lshl_add_u64 v[0:1], v[2:3], 0, s[16:17]
	v_lshl_add_u64 v[2:3], v[0:1], 0, s[16:17]
	global_load_dwordx4 v[40:43], v[0:1], off nt
	global_load_dwordx4 v[32:35], v[2:3], off nt
	v_lshl_add_u64 v[0:1], v[2:3], 0, s[16:17]
	v_lshl_add_u64 v[2:3], v[0:1], 0, s[16:17]
	global_load_dwordx4 v[56:59], v[0:1], off nt
	global_load_dwordx4 v[44:47], v[2:3], off nt
	v_lshl_add_u64 v[0:1], v[2:3], 0, s[16:17]
	global_load_dwordx4 v[48:51], v[0:1], off nt
	v_lshl_add_u64 v[0:1], v[0:1], 0, s[16:17]
	global_load_dwordx4 v[36:39], v[0:1], off nt
	v_lshl_add_u64 v[0:1], v[0:1], 0, s[16:17]
	global_load_dwordx4 v[52:55], v[0:1], off nt
	v_lshl_add_u64 v[0:1], v[0:1], 0, s[16:17]
	global_load_dwordx4 v[12:15], v[0:1], off nt
	v_lshl_add_u64 v[0:1], v[0:1], 0, s[16:17]
	v_lshl_add_u64 v[4:5], v[0:1], 0, s[16:17]
	v_lshl_add_u64 v[60:61], v[4:5], 0, s[16:17]
	global_load_dwordx4 v[24:27], v[0:1], off nt
	s_nop 0
	global_load_dwordx4 v[0:3], v[4:5], off nt
	s_nop 0
	global_load_dwordx4 v[4:7], v[60:61], off nt
	v_lshl_add_u64 v[60:61], v[60:61], 0, s[16:17]
	global_load_dwordx4 v[60:63], v[60:61], off nt

.LBB0_3564:
	s_lshl_b32 s8, s15, 14
	s_add_i32 s9, s8, 0
	s_lshl_b32 s8, s24, 6
	v_bfe_u32 v75, v65, 4, 2
	v_or_b32_e32 v0, s8, v75
	s_ashr_i32 s15, s8, 31
	s_mul_i32 s15, s16, s15
	v_mul_lo_u32 v2, s17, v0
	v_mad_u64_u32 v[0:1], s[24:25], s16, v0, 0
	v_add3_u32 v1, v1, s15, v2
	v_lshlrev_b32_e32 v2, 2, v65
	v_lshl_add_u64 v[0:1], v[0:1], 2, s[12:13]
	s_ashr_i32 s15, s14, 31
	v_and_b32_e32 v64, 60, v2
	v_lshl_add_u64 v[0:1], s[14:15], 2, v[0:1]
	v_mov_b32_e32 v73, 0
	v_lshlrev_b32_e32 v72, 2, v64
	s_lshl_b64 s[12:13], s[16:17], 4
	s_mov_b32 s19, 0
	v_lshl_add_u64 v[66:67], v[0:1], 0, v[72:73]
	s_mul_i32 s18, s16, 0xf0
	s_sub_u32 s12, 0, s12
	v_lshl_add_u64 v[68:69], v[66:67], 0, s[18:19]
	s_subb_u32 s13, 0, s13
	v_lshl_add_u64 v[8:9], v[68:69], 0, s[12:13]
	v_lshl_add_u64 v[10:11], v[8:9], 0, s[12:13]
	global_load_dwordx4 v[4:7], v[8:9], off nt
	global_load_dwordx4 v[0:3], v[10:11], off nt
	v_lshl_add_u64 v[8:9], v[10:11], 0, s[12:13]
	v_lshl_add_u64 v[10:11], v[8:9], 0, s[12:13]
	global_load_dwordx4 v[24:27], v[8:9], off nt
	global_load_dwordx4 v[12:15], v[10:11], off nt
	v_lshl_add_u64 v[8:9], v[10:11], 0, s[12:13]
	v_lshl_add_u64 v[10:11], v[8:9], 0, s[12:13]
	global_load_dwordx4 v[52:55], v[8:9], off nt
	global_load_dwordx4 v[36:39], v[10:11], off nt
	v_lshl_add_u64 v[8:9], v[10:11], 0, s[12:13]
	global_load_dwordx4 v[48:51], v[8:9], off nt
	v_lshl_add_u64 v[8:9], v[8:9], 0, s[12:13]
	global_load_dwordx4 v[44:47], v[8:9], off nt
	v_lshl_add_u64 v[8:9], v[8:9], 0, s[12:13]
	global_load_dwordx4 v[56:59], v[8:9], off nt
	v_lshl_add_u64 v[8:9], v[8:9], 0, s[12:13]
	global_load_dwordx4 v[32:35], v[8:9], off nt
	v_lshl_add_u64 v[8:9], v[8:9], 0, s[12:13]
	global_load_dwordx4 v[40:43], v[8:9], off nt
	v_lshl_add_u64 v[8:9], v[8:9], 0, s[12:13]
	global_load_dwordx4 v[20:23], v[8:9], off nt
	v_lshl_add_u64 v[8:9], v[8:9], 0, s[12:13]
	v_lshl_add_u64 v[70:71], v[8:9], 0, s[12:13]
	global_load_dwordx4 v[28:31], v[8:9], off nt
	s_nop 0
	global_load_dwordx4 v[8:11], v[70:71], off nt
	global_load_dwordx4 v[60:63], v[68:69], off nt
	global_load_dwordx4 v[16:19], v[66:67], off nt
	v_lshl_add_u32 v69, v75, 8, s9
	v_lshlrev_b32_e32 v70, 2, v75
	v_add3_u32 v78, v69, v70, v72
	v_bitop3_b32 v70, v64, v75, 1 bitop3:0x36
	v_lshl_add_u32 v79, v70, 2, v69
	v_bitop3_b32 v70, v64, v75, 2 bitop3:0x36
	v_lshl_add_u32 v80, v70, 2, v69
	v_bitop3_b32 v70, v64, v75, 3 bitop3:0x36
	v_lshl_add_u32 v81, v70, 2, v69
	v_or_b32_e32 v69, 4, v75
	v_lshl_add_u32 v70, v69, 8, s9
	v_bitop3_b32 v71, v75, v64, 4 bitop3:0x36
	v_lshl_add_u32 v82, v71, 2, v70
	v_bitop3_b32 v71, v64, v69, 1 bitop3:0x36
	v_lshl_add_u32 v83, v71, 2, v70
	v_bitop3_b32 v71, v64, v69, 2 bitop3:0x36
	v_bitop3_b32 v69, v64, v69, 3 bitop3:0x36
	v_lshl_add_u32 v85, v69, 2, v70
	v_or_b32_e32 v69, 8, v75
	v_lshl_add_u32 v84, v71, 2, v70
	v_lshl_add_u32 v70, v69, 8, s9
	v_bitop3_b32 v71, v75, v64, 8 bitop3:0x36
	v_lshl_add_u32 v86, v71, 2, v70
	v_bitop3_b32 v71, v64, v69, 1 bitop3:0x36
	v_lshl_add_u32 v87, v71, 2, v70
	v_bitop3_b32 v71, v64, v69, 2 bitop3:0x36
	v_bitop3_b32 v69, v64, v69, 3 bitop3:0x36
	v_lshl_add_u32 v89, v69, 2, v70
	v_or_b32_e32 v69, 12, v75
	v_lshl_add_u32 v88, v71, 2, v70
	v_lshl_add_u32 v70, v69, 8, s9
	v_bitop3_b32 v71, v75, v64, 12 bitop3:0x36
	v_lshl_add_u32 v90, v71, 2, v70
	v_bitop3_b32 v71, v64, v69, 1 bitop3:0x36
	v_lshl_add_u32 v91, v71, 2, v70
	v_bitop3_b32 v71, v64, v69, 2 bitop3:0x36
	v_bitop3_b32 v69, v64, v69, 3 bitop3:0x36
	v_lshl_add_u32 v93, v69, 2, v70
	v_or_b32_e32 v69, 16, v75
	v_lshl_add_u32 v92, v71, 2, v70
	v_lshl_add_u32 v70, v69, 8, s9
	v_bitop3_b32 v71, v75, v64, 16 bitop3:0x36
	v_lshl_add_u32 v94, v71, 2, v70
	v_bitop3_b32 v71, v64, v69, 1 bitop3:0x36
	v_lshl_add_u32 v95, v71, 2, v70
	v_bitop3_b32 v71, v64, v69, 2 bitop3:0x36
	v_bitop3_b32 v69, v64, v69, 3 bitop3:0x36
	v_lshl_add_u32 v97, v69, 2, v70
	v_or_b32_e32 v69, 20, v75
	v_lshl_add_u32 v96, v71, 2, v70
	v_lshl_add_u32 v70, v69, 8, s9
	v_bitop3_b32 v71, v75, v64, 20 bitop3:0x36
	v_lshl_add_u32 v98, v71, 2, v70
	v_bitop3_b32 v71, v64, v69, 1 bitop3:0x36
	v_lshl_add_u32 v99, v71, 2, v70
	v_bitop3_b32 v71, v64, v69, 2 bitop3:0x36
	v_bitop3_b32 v69, v64, v69, 3 bitop3:0x36
	v_lshl_add_u32 v101, v69, 2, v70
	v_or_b32_e32 v69, 24, v75
	v_lshl_add_u32 v100, v71, 2, v70
	v_lshl_add_u32 v70, v69, 8, s9
	v_bitop3_b32 v71, v75, v64, 24 bitop3:0x36
	v_lshl_add_u32 v102, v71, 2, v70
	v_bitop3_b32 v71, v64, v69, 1 bitop3:0x36
	v_lshl_add_u32 v103, v71, 2, v70
	v_bitop3_b32 v71, v64, v69, 2 bitop3:0x36
	v_bitop3_b32 v69, v64, v69, 3 bitop3:0x36
	v_lshl_add_u32 v105, v69, 2, v70
	v_or_b32_e32 v69, 28, v75
	v_lshl_add_u32 v104, v71, 2, v70
	v_lshl_add_u32 v70, v69, 8, s9
	v_bitop3_b32 v71, v75, v64, 28 bitop3:0x36
	v_lshl_add_u32 v106, v71, 2, v70
	v_bitop3_b32 v71, v64, v69, 1 bitop3:0x36
	v_lshl_add_u32 v107, v71, 2, v70
	v_bitop3_b32 v71, v64, v69, 2 bitop3:0x36
	v_bitop3_b32 v69, v64, v69, 3 bitop3:0x36
	v_lshl_add_u32 v109, v69, 2, v70
	v_or_b32_e32 v69, 36, v75
	v_or_b32_e32 v66, 1, v64
	v_lshl_add_u32 v108, v71, 2, v70
	v_lshl_add_u32 v70, v69, 8, s9
	v_bitop3_b32 v71, v69, v64, 7 bitop3:0x6c
	v_or_b32_e32 v67, 2, v64
	v_or_b32_e32 v68, 3, v64
	v_lshl_add_u32 v110, v71, 2, v70
	v_bitop3_b32 v71, v69, v66, 7 bitop3:0x6c
	v_lshl_add_u32 v111, v71, 2, v70
	v_bitop3_b32 v71, v69, v67, 7 bitop3:0x6c
	v_bitop3_b32 v69, v69, v68, 7 bitop3:0x6c
	v_lshl_add_u32 v113, v69, 2, v70
	v_or_b32_e32 v69, 40, v75
	v_lshl_add_u32 v112, v71, 2, v70
	v_lshl_add_u32 v70, v69, 8, s9
	v_bitop3_b32 v71, v69, v64, 11 bitop3:0x6c
	v_lshl_add_u32 v114, v71, 2, v70
	v_bitop3_b32 v71, v69, v66, 11 bitop3:0x6c
	v_lshl_add_u32 v115, v71, 2, v70
	v_bitop3_b32 v71, v69, v67, 11 bitop3:0x6c
	v_bitop3_b32 v69, v69, v68, 11 bitop3:0x6c
	v_lshl_add_u32 v117, v69, 2, v70
	v_or_b32_e32 v69, 44, v75
	v_lshl_add_u32 v116, v71, 2, v70
	v_lshl_add_u32 v70, v69, 8, s9
	v_bitop3_b32 v71, v69, v64, 15 bitop3:0x6c
	v_lshl_add_u32 v118, v71, 2, v70
	v_bitop3_b32 v71, v69, v66, 15 bitop3:0x6c
	v_lshl_add_u32 v119, v71, 2, v70
	v_bitop3_b32 v71, v69, v67, 15 bitop3:0x6c
	v_bitop3_b32 v69, v69, v68, 15 bitop3:0x6c
	v_lshl_add_u32 v121, v69, 2, v70
	v_or_b32_e32 v69, 48, v75
	v_lshl_add_u32 v120, v71, 2, v70
	v_lshl_add_u32 v70, v69, 8, s9
	v_bitop3_b32 v71, v69, v64, 19 bitop3:0x6c
	v_lshl_add_u32 v122, v71, 2, v70
	v_bitop3_b32 v71, v69, v66, 19 bitop3:0x6c
	v_lshl_add_u32 v123, v71, 2, v70
	v_bitop3_b32 v71, v69, v67, 19 bitop3:0x6c
	v_bitop3_b32 v69, v69, v68, 19 bitop3:0x6c
	v_lshl_add_u32 v125, v69, 2, v70
	v_or_b32_e32 v69, 52, v75
	v_lshl_add_u32 v124, v71, 2, v70
	v_lshl_add_u32 v70, v69, 8, s9
	v_bitop3_b32 v71, v69, v64, 23 bitop3:0x6c
	v_lshl_add_u32 v126, v71, 2, v70
	v_bitop3_b32 v71, v69, v66, 23 bitop3:0x6c
	v_lshl_add_u32 v127, v71, 2, v70
	v_bitop3_b32 v71, v69, v67, 23 bitop3:0x6c
	v_bitop3_b32 v69, v69, v68, 23 bitop3:0x6c
	v_lshl_add_u32 v129, v69, 2, v70
	v_or_b32_e32 v69, 56, v75
	v_lshl_add_u32 v128, v71, 2, v70
	v_lshl_add_u32 v70, v69, 8, s9
	v_bitop3_b32 v71, v69, v64, 27 bitop3:0x6c
	v_lshl_add_u32 v130, v71, 2, v70
	v_bitop3_b32 v71, v69, v66, 27 bitop3:0x6c
	v_lshl_add_u32 v131, v71, 2, v70
	v_bitop3_b32 v71, v69, v67, 27 bitop3:0x6c
	v_bitop3_b32 v69, v69, v68, 27 bitop3:0x6c
	v_lshl_add_u32 v133, v69, 2, v70
	v_or_b32_e32 v69, 60, v75
	v_lshl_add_u32 v132, v71, 2, v70
	v_lshl_add_u32 v70, v69, 8, s9
	v_bitop3_b32 v66, v69, v66, 31 bitop3:0x6c
	v_lshl_add_u32 v135, v66, 2, v70
	v_bitop3_b32 v66, v69, v67, 31 bitop3:0x6c
	v_and_b32_e32 v74, 63, v65
	v_lshl_add_u32 v136, v66, 2, v70
	v_bitop3_b32 v66, v69, v68, 31 bitop3:0x6c
	v_lshl_add_u32 v137, v66, 2, v70
	s_add_u32 s29, s21, 0x1a000000
	v_lshlrev_b32_e32 v66, 3, v74
	s_addc_u32 s30, s22, 0
	v_and_b32_e32 v74, 56, v66
	v_bfe_u32 v138, v65, 3, 3
	v_and_b32_e32 v65, 24, v66
	s_add_u32 s31, s21, 0x2000000
	v_lshl_add_u32 v67, v74, 8, s9
	v_lshlrev_b32_e32 v65, 2, v65
	v_lshlrev_b32_e32 v68, 2, v138
	s_addc_u32 s36, s22, 0
	v_add3_u32 v146, v67, v65, v68
	v_or_b32_e32 v65, 1, v74
	v_bitop3_b32 v71, v69, v64, 31 bitop3:0x6c
	s_add_u32 s37, s21, 0x1a00000
	v_bitop3_b32 v68, v65, v138, 25 bitop3:0x6c
	v_lshl_add_u32 v69, v65, 8, s9
	s_addc_u32 s38, s22, 0
	v_lshl_add_u32 v147, v68, 2, v69
	v_or_b32_e32 v68, 2, v74
	v_lshl_add_u32 v134, v71, 2, v70
	s_add_u32 s39, s21, 0x1800000
	v_bitop3_b32 v70, v68, v138, 26 bitop3:0x6c
	v_lshl_add_u32 v71, v68, 8, s9
	s_addc_u32 s42, s22, 0
	v_or_b32_e32 v139, 8, v138
	v_or_b32_e32 v140, 16, v138
	v_or_b32_e32 v141, 24, v138
	v_or_b32_e32 v142, 32, v138
	v_or_b32_e32 v143, 40, v138
	v_or_b32_e32 v144, 48, v138
	v_or_b32_e32 v145, 56, v138
	v_lshl_add_u32 v148, v70, 2, v71
	v_or_b32_e32 v70, 3, v74
	s_add_u32 s43, s21, 0x1500000
	v_bitop3_b32 v72, v70, v138, 27 bitop3:0x6c
	v_lshl_add_u32 v76, v70, 8, s9
	v_bitop3_b32 v155, v65, v139, 25 bitop3:0x6c
	v_bitop3_b32 v163, v65, v140, 25 bitop3:0x6c
	v_bitop3_b32 v171, v65, v141, 25 bitop3:0x6c
	v_bitop3_b32 v178, v65, v142, 25 bitop3:0x6c
	v_bitop3_b32 v186, v65, v143, 25 bitop3:0x6c
	v_bitop3_b32 v194, v65, v144, 25 bitop3:0x6c
	v_bitop3_b32 v65, v65, v145, 25 bitop3:0x6c
	s_addc_u32 s44, s22, 0
	v_lshl_add_u32 v149, v72, 2, v76
	v_or_b32_e32 v72, 4, v74
	v_lshl_add_u32 v202, v65, 2, v69
	v_bitop3_b32 v65, v68, v145, 26 bitop3:0x6c
	s_add_u32 s45, s21, 0x1200000
	v_bitop3_b32 v77, v72, v138, 28 bitop3:0x6c
	v_lshl_add_u32 v205, v72, 8, s9
	v_lshl_add_u32 v203, v65, 2, v71
	v_bitop3_b32 v65, v70, v145, 27 bitop3:0x6c
	s_addc_u32 s46, s22, 0
	v_lshl_add_u32 v150, v77, 2, v205
	v_or_b32_e32 v77, 5, v74
	v_bitop3_b32 v158, v72, v139, 28 bitop3:0x6c
	v_bitop3_b32 v166, v72, v140, 28 bitop3:0x6c
	v_bitop3_b32 v174, v72, v141, 28 bitop3:0x6c
	v_bitop3_b32 v181, v72, v142, 28 bitop3:0x6c
	v_bitop3_b32 v189, v72, v143, 28 bitop3:0x6c
	v_bitop3_b32 v197, v72, v144, 28 bitop3:0x6c
	v_lshl_add_u32 v204, v65, 2, v76
	v_bitop3_b32 v65, v72, v145, 28 bitop3:0x6c
	s_add_u32 s47, s21, 0xe00000
	v_bitop3_b32 v151, v77, v138, 29 bitop3:0x6c
	v_lshl_add_u32 v206, v77, 8, s9
	v_or_b32_e32 v207, 6, v74
	v_lshl_add_u32 v158, v158, 2, v205
	v_bitop3_b32 v159, v77, v139, 29 bitop3:0x6c
	v_lshl_add_u32 v166, v166, 2, v205
	v_bitop3_b32 v167, v77, v140, 29 bitop3:0x6c
	v_lshl_add_u32 v174, v174, 2, v205
	v_bitop3_b32 v175, v77, v141, 29 bitop3:0x6c
	v_lshl_add_u32 v181, v181, 2, v205
	v_bitop3_b32 v182, v77, v142, 29 bitop3:0x6c
	v_lshl_add_u32 v189, v189, 2, v205
	v_bitop3_b32 v190, v77, v143, 29 bitop3:0x6c
	v_lshl_add_u32 v197, v197, 2, v205
	v_bitop3_b32 v198, v77, v144, 29 bitop3:0x6c
	v_lshl_add_u32 v205, v65, 2, v205
	v_bitop3_b32 v65, v77, v145, 29 bitop3:0x6c
	s_addc_u32 s48, s22, 0
	v_lshl_add_u32 v151, v151, 2, v206
	v_lshl_add_u32 v208, v207, 8, s9
	v_or_b32_e32 v209, 7, v74
	v_lshl_add_u32 v159, v159, 2, v206
	v_lshl_add_u32 v167, v167, 2, v206
	v_lshl_add_u32 v175, v175, 2, v206
	v_lshl_add_u32 v182, v182, 2, v206
	v_lshl_add_u32 v190, v190, 2, v206
	v_lshl_add_u32 v198, v198, 2, v206
	v_lshl_add_u32 v206, v65, 2, v206
	v_bitop3_b32 v65, v207, v145, 30 bitop3:0x6c
	s_add_u32 s49, s21, 0x200000
	v_bitop3_b32 v152, v207, v138, 30 bitop3:0x6c
	v_bitop3_b32 v153, v209, v138, 31 bitop3:0x6c
	v_lshl_add_u32 v210, v209, 8, s9
	v_bitop3_b32 v154, v66, v139, 24 bitop3:0x6c
	v_bitop3_b32 v156, v68, v139, 26 bitop3:0x6c
	v_bitop3_b32 v157, v70, v139, 27 bitop3:0x6c
	v_bitop3_b32 v160, v207, v139, 30 bitop3:0x6c
	v_bitop3_b32 v161, v209, v139, 31 bitop3:0x6c
	v_bitop3_b32 v162, v66, v140, 24 bitop3:0x6c
	v_bitop3_b32 v164, v68, v140, 26 bitop3:0x6c
	v_bitop3_b32 v165, v70, v140, 27 bitop3:0x6c
	v_bitop3_b32 v168, v207, v140, 30 bitop3:0x6c
	v_bitop3_b32 v169, v209, v140, 31 bitop3:0x6c
	v_bitop3_b32 v170, v66, v138, 24 bitop3:0x4e
	v_bitop3_b32 v172, v68, v141, 26 bitop3:0x6c
	v_bitop3_b32 v173, v70, v141, 27 bitop3:0x6c
	v_bitop3_b32 v176, v207, v141, 30 bitop3:0x6c
	v_bitop3_b32 v177, v209, v141, 31 bitop3:0x6c
	v_bitop3_b32 v179, v68, v142, 26 bitop3:0x6c
	v_bitop3_b32 v180, v70, v142, 27 bitop3:0x6c
	v_bitop3_b32 v183, v207, v142, 30 bitop3:0x6c
	v_bitop3_b32 v184, v209, v142, 31 bitop3:0x6c
	v_bitop3_b32 v185, v66, v143, 24 bitop3:0x6c
	v_bitop3_b32 v187, v68, v143, 26 bitop3:0x6c
	v_bitop3_b32 v188, v70, v143, 27 bitop3:0x6c
	v_bitop3_b32 v191, v207, v143, 30 bitop3:0x6c
	v_bitop3_b32 v192, v209, v143, 31 bitop3:0x6c
	v_bitop3_b32 v193, v66, v144, 24 bitop3:0x6c
	v_bitop3_b32 v195, v68, v144, 26 bitop3:0x6c
	v_bitop3_b32 v196, v70, v144, 27 bitop3:0x6c
	v_bitop3_b32 v199, v207, v144, 30 bitop3:0x6c
	v_bitop3_b32 v200, v209, v144, 31 bitop3:0x6c
	v_bitop3_b32 v66, v66, v145, 24 bitop3:0x6c
	v_lshl_add_u32 v207, v65, 2, v208
	v_bitop3_b32 v65, v209, v145, 31 bitop3:0x6c
	s_addc_u32 s50, s22, 0
	v_lshl_add_u32 v152, v152, 2, v208
	v_lshl_add_u32 v153, v153, 2, v210
	v_lshl_add_u32 v154, v154, 2, v67
	v_lshl_add_u32 v155, v155, 2, v69
	v_lshl_add_u32 v156, v156, 2, v71
	v_lshl_add_u32 v157, v157, 2, v76
	v_lshl_add_u32 v160, v160, 2, v208
	v_lshl_add_u32 v161, v161, 2, v210
	v_lshl_add_u32 v162, v162, 2, v67
	v_lshl_add_u32 v163, v163, 2, v69
	v_lshl_add_u32 v164, v164, 2, v71
	v_lshl_add_u32 v165, v165, 2, v76
	v_lshl_add_u32 v168, v168, 2, v208
	v_lshl_add_u32 v169, v169, 2, v210
	v_lshl_add_u32 v170, v170, 2, v67
	v_lshl_add_u32 v171, v171, 2, v69
	v_lshl_add_u32 v172, v172, 2, v71
	v_lshl_add_u32 v173, v173, 2, v76
	v_lshl_add_u32 v176, v176, 2, v208
	v_lshl_add_u32 v177, v177, 2, v210
	v_lshl_add_u32 v178, v178, 2, v69
	v_lshl_add_u32 v179, v179, 2, v71
	v_lshl_add_u32 v180, v180, 2, v76
	v_lshl_add_u32 v183, v183, 2, v208
	v_lshl_add_u32 v184, v184, 2, v210
	v_lshl_add_u32 v185, v185, 2, v67
	v_lshl_add_u32 v186, v186, 2, v69
	v_lshl_add_u32 v187, v187, 2, v71
	v_lshl_add_u32 v188, v188, 2, v76
	v_lshl_add_u32 v191, v191, 2, v208
	v_lshl_add_u32 v192, v192, 2, v210
	v_lshl_add_u32 v193, v193, 2, v67
	v_lshl_add_u32 v194, v194, 2, v69
	v_lshl_add_u32 v195, v195, 2, v71
	v_lshl_add_u32 v196, v196, 2, v76
	v_lshl_add_u32 v199, v199, 2, v208
	v_lshl_add_u32 v200, v200, 2, v210
	v_lshl_add_u32 v201, v66, 2, v67
	v_lshl_add_u32 v208, v65, 2, v210
	s_add_i32 s51, s26, 0x10c00
	s_lshl_b32 s52, s20, 6
	v_lshlrev_b32_e32 v76, 2, v64
	v_lshlrev_b32_e32 v72, 1, v74
	s_branch .LBB0_3570

.LBB0_4201:
	s_lshl_b32 s6, s13, 14
	s_add_i32 s7, s6, 0
	s_lshl_b32 s6, s22, 6
	v_bfe_u32 v75, v65, 4, 2
	v_or_b32_e32 v0, s6, v75
	s_ashr_i32 s13, s6, 31
	s_mul_i32 s13, s14, s13
	v_mul_lo_u32 v2, s15, v0
	v_mad_u64_u32 v[0:1], s[22:23], s14, v0, 0
	v_add3_u32 v1, v1, s13, v2
	v_lshlrev_b32_e32 v2, 2, v65
	v_lshl_add_u64 v[0:1], v[0:1], 2, s[8:9]
	s_ashr_i32 s13, s12, 31
	v_and_b32_e32 v64, 60, v2
	v_lshl_add_u64 v[0:1], s[12:13], 2, v[0:1]
	v_mov_b32_e32 v73, 0
	v_lshlrev_b32_e32 v72, 2, v64
	s_lshl_b64 s[8:9], s[14:15], 4
	s_mov_b32 s17, 0
	v_lshl_add_u64 v[66:67], v[0:1], 0, v[72:73]
	s_mul_i32 s16, s14, 0xf0
	s_sub_u32 s8, 0, s8
	v_lshl_add_u64 v[68:69], v[66:67], 0, s[16:17]
	s_subb_u32 s9, 0, s9
	v_lshl_add_u64 v[8:9], v[68:69], 0, s[8:9]
	v_lshl_add_u64 v[10:11], v[8:9], 0, s[8:9]
	global_load_dwordx4 v[4:7], v[8:9], off nt
	global_load_dwordx4 v[0:3], v[10:11], off nt
	v_lshl_add_u64 v[8:9], v[10:11], 0, s[8:9]
	v_lshl_add_u64 v[10:11], v[8:9], 0, s[8:9]
	global_load_dwordx4 v[24:27], v[8:9], off nt
	global_load_dwordx4 v[12:15], v[10:11], off nt
	v_lshl_add_u64 v[8:9], v[10:11], 0, s[8:9]
	v_lshl_add_u64 v[10:11], v[8:9], 0, s[8:9]
	global_load_dwordx4 v[52:55], v[8:9], off nt
	global_load_dwordx4 v[36:39], v[10:11], off nt
	v_lshl_add_u64 v[8:9], v[10:11], 0, s[8:9]
	global_load_dwordx4 v[48:51], v[8:9], off nt
	v_lshl_add_u64 v[8:9], v[8:9], 0, s[8:9]
	global_load_dwordx4 v[44:47], v[8:9], off nt
	v_lshl_add_u64 v[8:9], v[8:9], 0, s[8:9]
	global_load_dwordx4 v[56:59], v[8:9], off nt
	v_lshl_add_u64 v[8:9], v[8:9], 0, s[8:9]
	global_load_dwordx4 v[32:35], v[8:9], off nt
	v_lshl_add_u64 v[8:9], v[8:9], 0, s[8:9]
	global_load_dwordx4 v[40:43], v[8:9], off nt
	v_lshl_add_u64 v[8:9], v[8:9], 0, s[8:9]
	global_load_dwordx4 v[20:23], v[8:9], off nt
	v_lshl_add_u64 v[8:9], v[8:9], 0, s[8:9]
	v_lshl_add_u64 v[70:71], v[8:9], 0, s[8:9]
	global_load_dwordx4 v[28:31], v[8:9], off nt
	s_nop 0
	global_load_dwordx4 v[8:11], v[70:71], off nt
	global_load_dwordx4 v[60:63], v[68:69], off nt
	global_load_dwordx4 v[16:19], v[66:67], off nt
	v_lshl_add_u32 v69, v75, 8, s7
	v_lshlrev_b32_e32 v70, 2, v75
	v_add3_u32 v78, v69, v70, v72
	v_bitop3_b32 v70, v64, v75, 1 bitop3:0x36
	v_lshl_add_u32 v79, v70, 2, v69
	v_bitop3_b32 v70, v64, v75, 2 bitop3:0x36
	v_lshl_add_u32 v80, v70, 2, v69
	v_bitop3_b32 v70, v64, v75, 3 bitop3:0x36
	v_lshl_add_u32 v81, v70, 2, v69
	v_or_b32_e32 v69, 4, v75
	v_lshl_add_u32 v70, v69, 8, s7
	v_bitop3_b32 v71, v75, v64, 4 bitop3:0x36
	v_lshl_add_u32 v82, v71, 2, v70
	v_bitop3_b32 v71, v64, v69, 1 bitop3:0x36
	v_lshl_add_u32 v83, v71, 2, v70
	v_bitop3_b32 v71, v64, v69, 2 bitop3:0x36
	v_bitop3_b32 v69, v64, v69, 3 bitop3:0x36
	v_lshl_add_u32 v85, v69, 2, v70
	v_or_b32_e32 v69, 8, v75
	v_lshl_add_u32 v84, v71, 2, v70
	v_lshl_add_u32 v70, v69, 8, s7
	v_bitop3_b32 v71, v75, v64, 8 bitop3:0x36
	v_lshl_add_u32 v86, v71, 2, v70
	v_bitop3_b32 v71, v64, v69, 1 bitop3:0x36
	v_lshl_add_u32 v87, v71, 2, v70
	v_bitop3_b32 v71, v64, v69, 2 bitop3:0x36
	v_bitop3_b32 v69, v64, v69, 3 bitop3:0x36
	v_lshl_add_u32 v89, v69, 2, v70
	v_or_b32_e32 v69, 12, v75
	v_lshl_add_u32 v88, v71, 2, v70
	v_lshl_add_u32 v70, v69, 8, s7
	v_bitop3_b32 v71, v75, v64, 12 bitop3:0x36
	v_lshl_add_u32 v90, v71, 2, v70
	v_bitop3_b32 v71, v64, v69, 1 bitop3:0x36
	v_lshl_add_u32 v91, v71, 2, v70
	v_bitop3_b32 v71, v64, v69, 2 bitop3:0x36
	v_bitop3_b32 v69, v64, v69, 3 bitop3:0x36
	v_lshl_add_u32 v93, v69, 2, v70
	v_or_b32_e32 v69, 16, v75
	v_lshl_add_u32 v92, v71, 2, v70
	v_lshl_add_u32 v70, v69, 8, s7
	v_bitop3_b32 v71, v75, v64, 16 bitop3:0x36
	v_lshl_add_u32 v94, v71, 2, v70
	v_bitop3_b32 v71, v64, v69, 1 bitop3:0x36
	v_lshl_add_u32 v95, v71, 2, v70
	v_bitop3_b32 v71, v64, v69, 2 bitop3:0x36
	v_bitop3_b32 v69, v64, v69, 3 bitop3:0x36
	v_lshl_add_u32 v97, v69, 2, v70
	v_or_b32_e32 v69, 20, v75
	v_lshl_add_u32 v96, v71, 2, v70
	v_lshl_add_u32 v70, v69, 8, s7
	v_bitop3_b32 v71, v75, v64, 20 bitop3:0x36
	v_lshl_add_u32 v98, v71, 2, v70
	v_bitop3_b32 v71, v64, v69, 1 bitop3:0x36
	v_lshl_add_u32 v99, v71, 2, v70
	v_bitop3_b32 v71, v64, v69, 2 bitop3:0x36
	v_bitop3_b32 v69, v64, v69, 3 bitop3:0x36
	v_lshl_add_u32 v101, v69, 2, v70
	v_or_b32_e32 v69, 24, v75
	v_lshl_add_u32 v100, v71, 2, v70
	v_lshl_add_u32 v70, v69, 8, s7
	v_bitop3_b32 v71, v75, v64, 24 bitop3:0x36
	v_lshl_add_u32 v102, v71, 2, v70
	v_bitop3_b32 v71, v64, v69, 1 bitop3:0x36
	v_lshl_add_u32 v103, v71, 2, v70
	v_bitop3_b32 v71, v64, v69, 2 bitop3:0x36
	v_bitop3_b32 v69, v64, v69, 3 bitop3:0x36
	v_lshl_add_u32 v105, v69, 2, v70
	v_or_b32_e32 v69, 28, v75
	v_lshl_add_u32 v104, v71, 2, v70
	v_lshl_add_u32 v70, v69, 8, s7
	v_bitop3_b32 v71, v75, v64, 28 bitop3:0x36
	v_lshl_add_u32 v106, v71, 2, v70
	v_bitop3_b32 v71, v64, v69, 1 bitop3:0x36
	v_lshl_add_u32 v107, v71, 2, v70
	v_bitop3_b32 v71, v64, v69, 2 bitop3:0x36
	v_bitop3_b32 v69, v64, v69, 3 bitop3:0x36
	v_lshl_add_u32 v109, v69, 2, v70
	v_or_b32_e32 v69, 36, v75
	v_or_b32_e32 v66, 1, v64
	v_lshl_add_u32 v108, v71, 2, v70
	v_lshl_add_u32 v70, v69, 8, s7
	v_bitop3_b32 v71, v69, v64, 7 bitop3:0x6c
	v_or_b32_e32 v67, 2, v64
	v_or_b32_e32 v68, 3, v64
	v_lshl_add_u32 v110, v71, 2, v70
	v_bitop3_b32 v71, v69, v66, 7 bitop3:0x6c
	v_lshl_add_u32 v111, v71, 2, v70
	v_bitop3_b32 v71, v69, v67, 7 bitop3:0x6c
	v_bitop3_b32 v69, v69, v68, 7 bitop3:0x6c
	v_lshl_add_u32 v113, v69, 2, v70
	v_or_b32_e32 v69, 40, v75
	v_lshl_add_u32 v112, v71, 2, v70
	v_lshl_add_u32 v70, v69, 8, s7
	v_bitop3_b32 v71, v69, v64, 11 bitop3:0x6c
	v_lshl_add_u32 v114, v71, 2, v70
	v_bitop3_b32 v71, v69, v66, 11 bitop3:0x6c
	v_lshl_add_u32 v115, v71, 2, v70
	v_bitop3_b32 v71, v69, v67, 11 bitop3:0x6c
	v_bitop3_b32 v69, v69, v68, 11 bitop3:0x6c
	v_lshl_add_u32 v117, v69, 2, v70
	v_or_b32_e32 v69, 44, v75
	v_lshl_add_u32 v116, v71, 2, v70
	v_lshl_add_u32 v70, v69, 8, s7
	v_bitop3_b32 v71, v69, v64, 15 bitop3:0x6c
	v_lshl_add_u32 v118, v71, 2, v70
	v_bitop3_b32 v71, v69, v66, 15 bitop3:0x6c
	v_lshl_add_u32 v119, v71, 2, v70
	v_bitop3_b32 v71, v69, v67, 15 bitop3:0x6c
	v_bitop3_b32 v69, v69, v68, 15 bitop3:0x6c
	v_lshl_add_u32 v121, v69, 2, v70
	v_or_b32_e32 v69, 48, v75
	v_lshl_add_u32 v120, v71, 2, v70
	v_lshl_add_u32 v70, v69, 8, s7
	v_bitop3_b32 v71, v69, v64, 19 bitop3:0x6c
	v_lshl_add_u32 v122, v71, 2, v70
	v_bitop3_b32 v71, v69, v66, 19 bitop3:0x6c
	v_lshl_add_u32 v123, v71, 2, v70
	v_bitop3_b32 v71, v69, v67, 19 bitop3:0x6c
	v_bitop3_b32 v69, v69, v68, 19 bitop3:0x6c
	v_lshl_add_u32 v125, v69, 2, v70
	v_or_b32_e32 v69, 52, v75
	v_lshl_add_u32 v124, v71, 2, v70
	v_lshl_add_u32 v70, v69, 8, s7
	v_bitop3_b32 v71, v69, v64, 23 bitop3:0x6c
	v_lshl_add_u32 v126, v71, 2, v70
	v_bitop3_b32 v71, v69, v66, 23 bitop3:0x6c
	v_lshl_add_u32 v127, v71, 2, v70
	v_bitop3_b32 v71, v69, v67, 23 bitop3:0x6c
	v_bitop3_b32 v69, v69, v68, 23 bitop3:0x6c
	v_lshl_add_u32 v129, v69, 2, v70
	v_or_b32_e32 v69, 56, v75
	v_lshl_add_u32 v128, v71, 2, v70
	v_lshl_add_u32 v70, v69, 8, s7
	v_bitop3_b32 v71, v69, v64, 27 bitop3:0x6c
	v_lshl_add_u32 v130, v71, 2, v70
	v_bitop3_b32 v71, v69, v66, 27 bitop3:0x6c
	v_lshl_add_u32 v131, v71, 2, v70
	v_bitop3_b32 v71, v69, v67, 27 bitop3:0x6c
	v_bitop3_b32 v69, v69, v68, 27 bitop3:0x6c
	v_lshl_add_u32 v133, v69, 2, v70
	v_or_b32_e32 v69, 60, v75
	v_lshl_add_u32 v132, v71, 2, v70
	v_lshl_add_u32 v70, v69, 8, s7
	v_bitop3_b32 v66, v69, v66, 31 bitop3:0x6c
	v_lshl_add_u32 v135, v66, 2, v70
	v_bitop3_b32 v66, v69, v67, 31 bitop3:0x6c
	v_and_b32_e32 v74, 63, v65
	v_lshl_add_u32 v136, v66, 2, v70
	v_bitop3_b32 v66, v69, v68, 31 bitop3:0x6c
	v_lshl_add_u32 v137, v66, 2, v70
	s_add_u32 s27, s19, 0x1a000000
	v_lshlrev_b32_e32 v66, 3, v74
	s_addc_u32 s30, s20, 0
	v_and_b32_e32 v74, 56, v66
	v_bfe_u32 v138, v65, 3, 3
	v_and_b32_e32 v65, 24, v66
	s_add_u32 s31, s19, 0x2000000
	v_lshl_add_u32 v67, v74, 8, s7
	v_lshlrev_b32_e32 v65, 2, v65
	v_lshlrev_b32_e32 v68, 2, v138
	s_addc_u32 s36, s20, 0
	v_add3_u32 v146, v67, v65, v68
	v_or_b32_e32 v65, 1, v74
	v_bitop3_b32 v71, v69, v64, 31 bitop3:0x6c
	s_add_u32 s37, s19, 0x1a00000
	v_bitop3_b32 v68, v65, v138, 25 bitop3:0x6c
	v_lshl_add_u32 v69, v65, 8, s7
	s_addc_u32 s38, s20, 0
	v_lshl_add_u32 v147, v68, 2, v69
	v_or_b32_e32 v68, 2, v74
	v_lshl_add_u32 v134, v71, 2, v70
	s_add_u32 s39, s19, 0x1800000
	v_bitop3_b32 v70, v68, v138, 26 bitop3:0x6c
	v_lshl_add_u32 v71, v68, 8, s7
	s_addc_u32 s40, s20, 0
	v_or_b32_e32 v139, 8, v138
	v_or_b32_e32 v140, 16, v138
	v_or_b32_e32 v141, 24, v138
	v_or_b32_e32 v142, 32, v138
	v_or_b32_e32 v143, 40, v138
	v_or_b32_e32 v144, 48, v138
	v_or_b32_e32 v145, 56, v138
	v_lshl_add_u32 v148, v70, 2, v71
	v_or_b32_e32 v70, 3, v74
	s_add_u32 s41, s19, 0x1500000
	v_bitop3_b32 v72, v70, v138, 27 bitop3:0x6c
	v_lshl_add_u32 v76, v70, 8, s7
	v_bitop3_b32 v155, v65, v139, 25 bitop3:0x6c
	v_bitop3_b32 v163, v65, v140, 25 bitop3:0x6c
	v_bitop3_b32 v171, v65, v141, 25 bitop3:0x6c
	v_bitop3_b32 v178, v65, v142, 25 bitop3:0x6c
	v_bitop3_b32 v186, v65, v143, 25 bitop3:0x6c
	v_bitop3_b32 v194, v65, v144, 25 bitop3:0x6c
	v_bitop3_b32 v65, v65, v145, 25 bitop3:0x6c
	s_addc_u32 s45, s20, 0
	v_lshl_add_u32 v149, v72, 2, v76
	v_or_b32_e32 v72, 4, v74
	v_lshl_add_u32 v202, v65, 2, v69
	v_bitop3_b32 v65, v68, v145, 26 bitop3:0x6c
	s_add_u32 s46, s19, 0x1200000
	v_bitop3_b32 v77, v72, v138, 28 bitop3:0x6c
	v_lshl_add_u32 v205, v72, 8, s7
	v_lshl_add_u32 v203, v65, 2, v71
	v_bitop3_b32 v65, v70, v145, 27 bitop3:0x6c
	s_addc_u32 s47, s20, 0
	v_lshl_add_u32 v150, v77, 2, v205
	v_or_b32_e32 v77, 5, v74
	v_bitop3_b32 v158, v72, v139, 28 bitop3:0x6c
	v_bitop3_b32 v166, v72, v140, 28 bitop3:0x6c
	v_bitop3_b32 v174, v72, v141, 28 bitop3:0x6c
	v_bitop3_b32 v181, v72, v142, 28 bitop3:0x6c
	v_bitop3_b32 v189, v72, v143, 28 bitop3:0x6c
	v_bitop3_b32 v197, v72, v144, 28 bitop3:0x6c
	v_lshl_add_u32 v204, v65, 2, v76
	v_bitop3_b32 v65, v72, v145, 28 bitop3:0x6c
	s_add_u32 s48, s19, 0xe00000
	v_bitop3_b32 v151, v77, v138, 29 bitop3:0x6c
	v_lshl_add_u32 v206, v77, 8, s7
	v_or_b32_e32 v207, 6, v74
	v_lshl_add_u32 v158, v158, 2, v205
	v_bitop3_b32 v159, v77, v139, 29 bitop3:0x6c
	v_lshl_add_u32 v166, v166, 2, v205
	v_bitop3_b32 v167, v77, v140, 29 bitop3:0x6c
	v_lshl_add_u32 v174, v174, 2, v205
	v_bitop3_b32 v175, v77, v141, 29 bitop3:0x6c
	v_lshl_add_u32 v181, v181, 2, v205
	v_bitop3_b32 v182, v77, v142, 29 bitop3:0x6c
	v_lshl_add_u32 v189, v189, 2, v205
	v_bitop3_b32 v190, v77, v143, 29 bitop3:0x6c
	v_lshl_add_u32 v197, v197, 2, v205
	v_bitop3_b32 v198, v77, v144, 29 bitop3:0x6c
	v_lshl_add_u32 v205, v65, 2, v205
	v_bitop3_b32 v65, v77, v145, 29 bitop3:0x6c
	s_addc_u32 s49, s20, 0
	v_lshl_add_u32 v151, v151, 2, v206
	v_lshl_add_u32 v208, v207, 8, s7
	v_or_b32_e32 v209, 7, v74
	v_lshl_add_u32 v159, v159, 2, v206
	v_lshl_add_u32 v167, v167, 2, v206
	v_lshl_add_u32 v175, v175, 2, v206
	v_lshl_add_u32 v182, v182, 2, v206
	v_lshl_add_u32 v190, v190, 2, v206
	v_lshl_add_u32 v198, v198, 2, v206
	v_lshl_add_u32 v206, v65, 2, v206
	v_bitop3_b32 v65, v207, v145, 30 bitop3:0x6c
	s_add_u32 s50, s19, 0x200000
	v_bitop3_b32 v152, v207, v138, 30 bitop3:0x6c
	v_bitop3_b32 v153, v209, v138, 31 bitop3:0x6c
	v_lshl_add_u32 v210, v209, 8, s7
	v_bitop3_b32 v154, v66, v139, 24 bitop3:0x6c
	v_bitop3_b32 v156, v68, v139, 26 bitop3:0x6c
	v_bitop3_b32 v157, v70, v139, 27 bitop3:0x6c
	v_bitop3_b32 v160, v207, v139, 30 bitop3:0x6c
	v_bitop3_b32 v161, v209, v139, 31 bitop3:0x6c
	v_bitop3_b32 v162, v66, v140, 24 bitop3:0x6c
	v_bitop3_b32 v164, v68, v140, 26 bitop3:0x6c
	v_bitop3_b32 v165, v70, v140, 27 bitop3:0x6c
	v_bitop3_b32 v168, v207, v140, 30 bitop3:0x6c
	v_bitop3_b32 v169, v209, v140, 31 bitop3:0x6c
	v_bitop3_b32 v170, v66, v138, 24 bitop3:0x4e
	v_bitop3_b32 v172, v68, v141, 26 bitop3:0x6c
	v_bitop3_b32 v173, v70, v141, 27 bitop3:0x6c
	v_bitop3_b32 v176, v207, v141, 30 bitop3:0x6c
	v_bitop3_b32 v177, v209, v141, 31 bitop3:0x6c
	v_bitop3_b32 v179, v68, v142, 26 bitop3:0x6c
	v_bitop3_b32 v180, v70, v142, 27 bitop3:0x6c
	v_bitop3_b32 v183, v207, v142, 30 bitop3:0x6c
	v_bitop3_b32 v184, v209, v142, 31 bitop3:0x6c
	v_bitop3_b32 v185, v66, v143, 24 bitop3:0x6c
	v_bitop3_b32 v187, v68, v143, 26 bitop3:0x6c
	v_bitop3_b32 v188, v70, v143, 27 bitop3:0x6c
	v_bitop3_b32 v191, v207, v143, 30 bitop3:0x6c
	v_bitop3_b32 v192, v209, v143, 31 bitop3:0x6c
	v_bitop3_b32 v193, v66, v144, 24 bitop3:0x6c
	v_bitop3_b32 v195, v68, v144, 26 bitop3:0x6c
	v_bitop3_b32 v196, v70, v144, 27 bitop3:0x6c
	v_bitop3_b32 v199, v207, v144, 30 bitop3:0x6c
	v_bitop3_b32 v200, v209, v144, 31 bitop3:0x6c
	v_bitop3_b32 v66, v66, v145, 24 bitop3:0x6c
	v_lshl_add_u32 v207, v65, 2, v208
	v_bitop3_b32 v65, v209, v145, 31 bitop3:0x6c
	s_addc_u32 s51, s20, 0
	v_lshl_add_u32 v152, v152, 2, v208
	v_lshl_add_u32 v153, v153, 2, v210
	v_lshl_add_u32 v154, v154, 2, v67
	v_lshl_add_u32 v155, v155, 2, v69
	v_lshl_add_u32 v156, v156, 2, v71
	v_lshl_add_u32 v157, v157, 2, v76
	v_lshl_add_u32 v160, v160, 2, v208
	v_lshl_add_u32 v161, v161, 2, v210
	v_lshl_add_u32 v162, v162, 2, v67
	v_lshl_add_u32 v163, v163, 2, v69
	v_lshl_add_u32 v164, v164, 2, v71
	v_lshl_add_u32 v165, v165, 2, v76
	v_lshl_add_u32 v168, v168, 2, v208
	v_lshl_add_u32 v169, v169, 2, v210
	v_lshl_add_u32 v170, v170, 2, v67
	v_lshl_add_u32 v171, v171, 2, v69
	v_lshl_add_u32 v172, v172, 2, v71
	v_lshl_add_u32 v173, v173, 2, v76
	v_lshl_add_u32 v176, v176, 2, v208
	v_lshl_add_u32 v177, v177, 2, v210
	v_lshl_add_u32 v178, v178, 2, v69
	v_lshl_add_u32 v179, v179, 2, v71
	v_lshl_add_u32 v180, v180, 2, v76
	v_lshl_add_u32 v183, v183, 2, v208
	v_lshl_add_u32 v184, v184, 2, v210
	v_lshl_add_u32 v185, v185, 2, v67
	v_lshl_add_u32 v186, v186, 2, v69
	v_lshl_add_u32 v187, v187, 2, v71
	v_lshl_add_u32 v188, v188, 2, v76
	v_lshl_add_u32 v191, v191, 2, v208
	v_lshl_add_u32 v192, v192, 2, v210
	v_lshl_add_u32 v193, v193, 2, v67
	v_lshl_add_u32 v194, v194, 2, v69
	v_lshl_add_u32 v195, v195, 2, v71
	v_lshl_add_u32 v196, v196, 2, v76
	v_lshl_add_u32 v199, v199, 2, v208
	v_lshl_add_u32 v200, v200, 2, v210
	v_lshl_add_u32 v201, v66, 2, v67
	v_lshl_add_u32 v208, v65, 2, v210
	s_add_i32 s52, s24, 0x11800
	s_lshl_b32 s53, s18, 6
	v_lshlrev_b32_e32 v76, 2, v64
	v_lshlrev_b32_e32 v72, 1, v74
	s_branch .LBB0_4207
